# attention stagger + saddr-form K/V DMA pieces; P1: drop the loop-preheader vmcnt(0) drain; GEMM K-loops: first K-iteration of later units peeled (MFMA C=0 instead of accumulator clear, first two DMA w
# speedup vs baseline: 1.0208x; 1.0169x over previous
.LBB0_188:
	s_ashr_i32 s21, s20, 31
	s_lshl_b64 s[22:23], s[20:21], 20
	s_add_u32 s22, s31, s22
	s_addc_u32 s23, s34, s23
	s_and_b64 s[24:25], s[2:3], exec
	s_cselect_b32 s5, s23, s29
	s_cselect_b32 s7, s22, s28
	s_ashr_i32 s19, s18, 31
	s_lshl_b64 s[24:25], s[18:19], 20
	s_add_u32 s24, s35, s24
	s_addc_u32 s25, s36, s25
	s_and_b64 s[26:27], s[2:3], exec
	s_cselect_b32 s19, s25, s9
	s_cselect_b32 s21, s24, s8
	s_add_u32 s59, s8, 0x100
	s_addc_u32 s60, s9, 0
	s_add_u32 s8, s28, 0x80080
	v_mov_b32_e32 v0, 0
	s_addc_u32 s9, s29, 0
	s_mov_b32 s61, -2
	s_cmp_eq_u32 s56, 1
	s_cbranch_scc1 .Lpeel_zero_P1
	v_add_u32_e32 v140, s37, v193
	v_add_u32_e32 v160, s40, v193
	ds_read_b128 v[128:131], v140
	ds_read_b128 v[132:135], v140 offset:1024
	ds_read_b128 v[136:139], v140 offset:2048
	ds_read_b128 v[140:143], v140 offset:3072
	ds_read_b128 v[144:147], v160
	ds_read_b128 v[148:151], v160 offset:1024
	ds_read_b128 v[176:179], v160 offset:2048
	ds_read_b128 v[180:183], v160 offset:3072
	s_add_u32 s26, s8, 0xfff80080
	s_addc_u32 s27, s9, -1
	s_cmp_eq_u32 s61, 28
	s_cselect_b32 s29, s5, s27
	s_cselect_b32 s28, s7, s26
	s_cselect_b32 s27, s19, s60
	s_cselect_b32 s26, s21, s59
	v_lshl_add_u64 v[162:163], s[8:9], 0, v[174:175]
	s_add_i32 m0, s43, 0xc000
	ds_read_b128 v[184:187], v199
	ds_read_b128 v[188:191], v199 offset:1024
	ds_read_b128 v[200:203], v199 offset:2048
	ds_read_b128 v[204:207], v199 offset:3072
	ds_read_b128 v[208:211], v199 offset:4096
	ds_read_b128 v[212:215], v199 offset:5120
	ds_read_b128 v[216:219], v199 offset:6144
	ds_read_b128 v[230:233], v199 offset:7168
	global_load_lds_dwordx4 v[162:163], off
	v_lshl_add_u64 v[162:163], s[8:9], 0, v[172:173]
	s_add_i32 m0, s43, 0xe000
	s_nop 0
	global_load_lds_dwordx4 v[162:163], off
	s_waitcnt vmcnt(16)
	s_waitcnt lgkmcnt(0)
	s_barrier
	s_setprio 1
	s_waitcnt lgkmcnt(0)
	v_mfma_f32_16x16x32_bf16 v[124:127], v[128:131], v[184:187], 0
	v_mfma_f32_16x16x32_bf16 v[120:123], v[136:139], v[184:187], 0
	v_mfma_f32_16x16x32_bf16 v[108:111], v[128:131], v[200:203], 0
	v_mfma_f32_16x16x32_bf16 v[104:107], v[136:139], v[200:203], 0
	v_mfma_f32_16x16x32_bf16 v[92:95], v[128:131], v[208:211], 0
	v_mfma_f32_16x16x32_bf16 v[88:91], v[136:139], v[208:211], 0
	v_mfma_f32_16x16x32_bf16 v[76:79], v[128:131], v[216:219], 0
	v_mfma_f32_16x16x32_bf16 v[72:75], v[136:139], v[216:219], 0
	v_mfma_f32_16x16x32_bf16 v[124:127], v[132:135], v[188:191], v[124:127]
	v_mfma_f32_16x16x32_bf16 v[120:123], v[140:143], v[188:191], v[120:123]
	v_mfma_f32_16x16x32_bf16 v[108:111], v[132:135], v[204:207], v[108:111]
	v_mfma_f32_16x16x32_bf16 v[104:107], v[140:143], v[204:207], v[104:107]
	v_mfma_f32_16x16x32_bf16 v[92:95], v[132:135], v[212:215], v[92:95]
	v_mfma_f32_16x16x32_bf16 v[88:91], v[140:143], v[212:215], v[88:91]
	v_mfma_f32_16x16x32_bf16 v[76:79], v[132:135], v[230:233], v[76:79]
	v_mfma_f32_16x16x32_bf16 v[72:75], v[140:143], v[230:233], v[72:75]
	s_setprio 0
	s_setprio 1
	v_mfma_f32_16x16x32_bf16 v[116:119], v[144:147], v[184:187], 0
	v_mfma_f32_16x16x32_bf16 v[112:115], v[176:179], v[184:187], 0
	v_mfma_f32_16x16x32_bf16 v[100:103], v[144:147], v[200:203], 0
	v_mfma_f32_16x16x32_bf16 v[96:99], v[176:179], v[200:203], 0
	v_mfma_f32_16x16x32_bf16 v[84:87], v[144:147], v[208:211], 0
	v_mfma_f32_16x16x32_bf16 v[80:83], v[176:179], v[208:211], 0
	v_mfma_f32_16x16x32_bf16 v[68:71], v[144:147], v[216:219], 0
	v_mfma_f32_16x16x32_bf16 v[64:67], v[176:179], v[216:219], 0
	v_mfma_f32_16x16x32_bf16 v[116:119], v[148:151], v[188:191], v[116:119]
	v_mfma_f32_16x16x32_bf16 v[112:115], v[180:183], v[188:191], v[112:115]
	v_mfma_f32_16x16x32_bf16 v[100:103], v[148:151], v[204:207], v[100:103]
	v_mfma_f32_16x16x32_bf16 v[96:99], v[180:183], v[204:207], v[96:99]
	v_mfma_f32_16x16x32_bf16 v[84:87], v[148:151], v[212:215], v[84:87]
	v_mfma_f32_16x16x32_bf16 v[80:83], v[180:183], v[212:215], v[80:83]
	v_mfma_f32_16x16x32_bf16 v[68:71], v[148:151], v[230:233], v[68:71]
	v_mfma_f32_16x16x32_bf16 v[64:67], v[180:183], v[230:233], v[64:67]
	s_setprio 0
	s_barrier
	s_mov_b32 m0, s38
	v_lshl_add_u64 v[162:163], s[26:27], 0, v[154:155]
	s_add_u32 s62, s26, 0x80000
	ds_read_b128 v[184:187], v199 offset:16384
	ds_read_b128 v[188:191], v199 offset:17408
	ds_read_b128 v[200:203], v199 offset:18432
	ds_read_b128 v[204:207], v199 offset:19456
	ds_read_b128 v[208:211], v199 offset:20480
	ds_read_b128 v[212:215], v199 offset:21504
	ds_read_b128 v[216:219], v199 offset:22528
	ds_read_b128 v[230:233], v199 offset:23552
	global_load_lds_dwordx4 v[162:163], off
	v_lshl_add_u64 v[166:167], s[26:27], 0, v[158:159]
	s_mov_b32 m0, s39
	s_addc_u32 s63, s27, 0
	global_load_lds_dwordx4 v[166:167], off
	v_lshl_add_u64 v[194:195], s[62:63], 0, v[154:155]
	s_mov_b32 m0, s41
	v_lshl_add_u64 v[196:197], s[28:29], 0, v[156:157]
	global_load_lds_dwordx4 v[194:195], off
	v_lshl_add_u64 v[194:195], s[62:63], 0, v[158:159]
	s_mov_b32 m0, s42
	s_nop 0
	global_load_lds_dwordx4 v[194:195], off
	v_lshl_add_u64 v[194:195], s[28:29], 0, v[152:153]
	s_mov_b32 m0, s43
	s_nop 0
	global_load_lds_dwordx4 v[194:195], off
	s_mov_b32 m0, s44
	s_nop 0
	global_load_lds_dwordx4 v[196:197], off
	s_waitcnt vmcnt(16)
	s_waitcnt lgkmcnt(0)
	s_barrier
	s_setprio 1
	s_waitcnt lgkmcnt(0)
	v_mfma_f32_16x16x32_bf16 v[60:63], v[128:131], v[184:187], 0
	v_mfma_f32_16x16x32_bf16 v[56:59], v[136:139], v[184:187], 0
	v_mfma_f32_16x16x32_bf16 v[44:47], v[128:131], v[200:203], 0
	v_mfma_f32_16x16x32_bf16 v[40:43], v[136:139], v[200:203], 0
	v_mfma_f32_16x16x32_bf16 v[28:31], v[128:131], v[208:211], 0
	v_mfma_f32_16x16x32_bf16 v[24:27], v[136:139], v[208:211], 0
	v_mfma_f32_16x16x32_bf16 v[12:15], v[128:131], v[216:219], 0
	v_mfma_f32_16x16x32_bf16 v[8:11], v[136:139], v[216:219], 0
	v_mfma_f32_16x16x32_bf16 v[60:63], v[132:135], v[188:191], v[60:63]
	v_mfma_f32_16x16x32_bf16 v[56:59], v[140:143], v[188:191], v[56:59]
	v_mfma_f32_16x16x32_bf16 v[44:47], v[132:135], v[204:207], v[44:47]
	v_mfma_f32_16x16x32_bf16 v[40:43], v[140:143], v[204:207], v[40:43]
	v_mfma_f32_16x16x32_bf16 v[28:31], v[132:135], v[212:215], v[28:31]
	v_mfma_f32_16x16x32_bf16 v[24:27], v[140:143], v[212:215], v[24:27]
	v_mfma_f32_16x16x32_bf16 v[12:15], v[132:135], v[230:233], v[12:15]
	v_mfma_f32_16x16x32_bf16 v[8:11], v[140:143], v[230:233], v[8:11]
	s_setprio 0
	s_setprio 1
	v_mfma_f32_16x16x32_bf16 v[52:55], v[144:147], v[184:187], 0
	v_mfma_f32_16x16x32_bf16 v[48:51], v[176:179], v[184:187], 0
	v_mfma_f32_16x16x32_bf16 v[36:39], v[144:147], v[200:203], 0
	v_mfma_f32_16x16x32_bf16 v[32:35], v[176:179], v[200:203], 0
	v_mfma_f32_16x16x32_bf16 v[20:23], v[144:147], v[208:211], 0
	v_mfma_f32_16x16x32_bf16 v[16:19], v[176:179], v[208:211], 0
	v_mfma_f32_16x16x32_bf16 v[4:7], v[144:147], v[216:219], 0
	v_mfma_f32_16x16x32_bf16 v[0:3], v[176:179], v[216:219], 0
	v_mfma_f32_16x16x32_bf16 v[52:55], v[148:151], v[188:191], v[52:55]
	v_mfma_f32_16x16x32_bf16 v[48:51], v[180:183], v[188:191], v[48:51]
	v_mfma_f32_16x16x32_bf16 v[36:39], v[148:151], v[204:207], v[36:39]
	v_mfma_f32_16x16x32_bf16 v[32:35], v[180:183], v[204:207], v[32:35]
	v_mfma_f32_16x16x32_bf16 v[20:23], v[148:151], v[212:215], v[20:23]
	v_mfma_f32_16x16x32_bf16 v[16:19], v[180:183], v[212:215], v[16:19]
	v_mfma_f32_16x16x32_bf16 v[4:7], v[148:151], v[230:233], v[4:7]
	v_mfma_f32_16x16x32_bf16 v[0:3], v[180:183], v[230:233], v[0:3]
	s_setprio 0
	s_barrier
	v_add_u32_e32 v140, s48, v193
	v_add_u32_e32 v160, s53, v193
	ds_read_b128 v[128:131], v140
	ds_read_b128 v[132:135], v140 offset:1024
	ds_read_b128 v[136:139], v140 offset:2048
	ds_read_b128 v[140:143], v140 offset:3072
	ds_read_b128 v[144:147], v160
	ds_read_b128 v[148:151], v160 offset:1024
	ds_read_b128 v[176:179], v160 offset:2048
	ds_read_b128 v[180:183], v160 offset:3072
	s_add_u32 s28, s28, 0x80000
	s_addc_u32 s29, s29, 0
	s_mov_b32 m0, s45
	v_lshl_add_u64 v[220:221], s[28:29], 0, v[152:153]
	ds_read_b128 v[184:187], v199 offset:32768
	ds_read_b128 v[188:191], v199 offset:33792
	ds_read_b128 v[200:203], v199 offset:34816
	ds_read_b128 v[204:207], v199 offset:35840
	ds_read_b128 v[208:211], v199 offset:36864
	ds_read_b128 v[212:215], v199 offset:37888
	ds_read_b128 v[216:219], v199 offset:38912
	ds_read_b128 v[230:233], v199 offset:39936
	global_load_lds_dwordx4 v[220:221], off
	v_lshl_add_u64 v[220:221], s[28:29], 0, v[156:157]
	s_mov_b32 m0, s47
	s_nop 0
	global_load_lds_dwordx4 v[220:221], off
	s_waitcnt vmcnt(8)
	s_waitcnt lgkmcnt(0)
	s_barrier
	s_setprio 1
	s_waitcnt lgkmcnt(0)
	v_mfma_f32_16x16x32_bf16 v[124:127], v[128:131], v[184:187], v[124:127]
	v_mfma_f32_16x16x32_bf16 v[120:123], v[136:139], v[184:187], v[120:123]
	v_mfma_f32_16x16x32_bf16 v[108:111], v[128:131], v[200:203], v[108:111]
	v_mfma_f32_16x16x32_bf16 v[104:107], v[136:139], v[200:203], v[104:107]
	v_mfma_f32_16x16x32_bf16 v[92:95], v[128:131], v[208:211], v[92:95]
	v_mfma_f32_16x16x32_bf16 v[88:91], v[136:139], v[208:211], v[88:91]
	v_mfma_f32_16x16x32_bf16 v[76:79], v[128:131], v[216:219], v[76:79]
	v_mfma_f32_16x16x32_bf16 v[72:75], v[136:139], v[216:219], v[72:75]
	v_mfma_f32_16x16x32_bf16 v[124:127], v[132:135], v[188:191], v[124:127]
	v_mfma_f32_16x16x32_bf16 v[120:123], v[140:143], v[188:191], v[120:123]
	v_mfma_f32_16x16x32_bf16 v[108:111], v[132:135], v[204:207], v[108:111]
	v_mfma_f32_16x16x32_bf16 v[104:107], v[140:143], v[204:207], v[104:107]
	v_mfma_f32_16x16x32_bf16 v[92:95], v[132:135], v[212:215], v[92:95]
	v_mfma_f32_16x16x32_bf16 v[88:91], v[140:143], v[212:215], v[88:91]
	v_mfma_f32_16x16x32_bf16 v[76:79], v[132:135], v[230:233], v[76:79]
	v_mfma_f32_16x16x32_bf16 v[72:75], v[140:143], v[230:233], v[72:75]
	s_setprio 0
	s_setprio 1
	v_mfma_f32_16x16x32_bf16 v[116:119], v[144:147], v[184:187], v[116:119]
	v_mfma_f32_16x16x32_bf16 v[112:115], v[176:179], v[184:187], v[112:115]
	v_mfma_f32_16x16x32_bf16 v[100:103], v[144:147], v[200:203], v[100:103]
	v_mfma_f32_16x16x32_bf16 v[96:99], v[176:179], v[200:203], v[96:99]
	v_mfma_f32_16x16x32_bf16 v[84:87], v[144:147], v[208:211], v[84:87]
	v_mfma_f32_16x16x32_bf16 v[80:83], v[176:179], v[208:211], v[80:83]
	v_mfma_f32_16x16x32_bf16 v[68:71], v[144:147], v[216:219], v[68:71]
	v_mfma_f32_16x16x32_bf16 v[64:67], v[176:179], v[216:219], v[64:67]
	v_mfma_f32_16x16x32_bf16 v[116:119], v[148:151], v[188:191], v[116:119]
	v_mfma_f32_16x16x32_bf16 v[112:115], v[180:183], v[188:191], v[112:115]
	v_mfma_f32_16x16x32_bf16 v[100:103], v[148:151], v[204:207], v[100:103]
	v_mfma_f32_16x16x32_bf16 v[96:99], v[180:183], v[204:207], v[96:99]
	v_mfma_f32_16x16x32_bf16 v[84:87], v[148:151], v[212:215], v[84:87]
	v_mfma_f32_16x16x32_bf16 v[80:83], v[180:183], v[212:215], v[80:83]
	v_mfma_f32_16x16x32_bf16 v[68:71], v[148:151], v[230:233], v[68:71]
	v_mfma_f32_16x16x32_bf16 v[64:67], v[180:183], v[230:233], v[64:67]
	s_setprio 0
	s_barrier
	s_mov_b32 m0, s49
	v_lshl_add_u64 v[162:163], v[162:163], 0, s[86:87]
	s_add_u32 s26, s26, 0x80080
	ds_read_b128 v[184:187], v199 offset:49152
	ds_read_b128 v[188:191], v199 offset:50176
	ds_read_b128 v[200:203], v199 offset:51200
	ds_read_b128 v[204:207], v199 offset:52224
	ds_read_b128 v[208:211], v199 offset:53248
	ds_read_b128 v[212:215], v199 offset:54272
	ds_read_b128 v[216:219], v199 offset:55296
	ds_read_b128 v[230:233], v199 offset:56320
	global_load_lds_dwordx4 v[162:163], off
	v_lshl_add_u64 v[162:163], v[166:167], 0, s[86:87]
	s_mov_b32 m0, s50
	s_addc_u32 s27, s27, 0
	global_load_lds_dwordx4 v[162:163], off
	v_lshl_add_u64 v[162:163], s[26:27], 0, v[154:155]
	s_mov_b32 m0, s54
	s_nop 0
	global_load_lds_dwordx4 v[162:163], off
	v_lshl_add_u64 v[162:163], s[26:27], 0, v[158:159]
	s_mov_b32 m0, s55
	s_nop 0
	global_load_lds_dwordx4 v[162:163], off
	v_lshl_add_u64 v[162:163], v[194:195], 0, s[86:87]
	s_mov_b32 m0, s51
	s_nop 0
	global_load_lds_dwordx4 v[162:163], off
	v_lshl_add_u64 v[162:163], v[196:197], 0, s[86:87]
	s_mov_b32 m0, s52
	s_nop 0
	global_load_lds_dwordx4 v[162:163], off
	s_waitcnt vmcnt(8)
	s_waitcnt lgkmcnt(0)
	s_barrier
	s_setprio 1
	s_waitcnt lgkmcnt(0)
	v_mfma_f32_16x16x32_bf16 v[60:63], v[128:131], v[184:187], v[60:63]
	v_mfma_f32_16x16x32_bf16 v[56:59], v[136:139], v[184:187], v[56:59]
	v_mfma_f32_16x16x32_bf16 v[44:47], v[128:131], v[200:203], v[44:47]
	v_mfma_f32_16x16x32_bf16 v[40:43], v[136:139], v[200:203], v[40:43]
	v_mfma_f32_16x16x32_bf16 v[28:31], v[128:131], v[208:211], v[28:31]
	v_mfma_f32_16x16x32_bf16 v[24:27], v[136:139], v[208:211], v[24:27]
	v_mfma_f32_16x16x32_bf16 v[12:15], v[128:131], v[216:219], v[12:15]
	v_mfma_f32_16x16x32_bf16 v[8:11], v[136:139], v[216:219], v[8:11]
	v_mfma_f32_16x16x32_bf16 v[60:63], v[132:135], v[188:191], v[60:63]
	v_mfma_f32_16x16x32_bf16 v[56:59], v[140:143], v[188:191], v[56:59]
	v_mfma_f32_16x16x32_bf16 v[44:47], v[132:135], v[204:207], v[44:47]
	v_mfma_f32_16x16x32_bf16 v[40:43], v[140:143], v[204:207], v[40:43]
	v_mfma_f32_16x16x32_bf16 v[28:31], v[132:135], v[212:215], v[28:31]
	v_mfma_f32_16x16x32_bf16 v[24:27], v[140:143], v[212:215], v[24:27]
	v_mfma_f32_16x16x32_bf16 v[12:15], v[132:135], v[230:233], v[12:15]
	v_mfma_f32_16x16x32_bf16 v[8:11], v[140:143], v[230:233], v[8:11]
	s_setprio 0
	s_setprio 1
	v_mfma_f32_16x16x32_bf16 v[52:55], v[144:147], v[184:187], v[52:55]
	v_mfma_f32_16x16x32_bf16 v[48:51], v[176:179], v[184:187], v[48:51]
	v_mfma_f32_16x16x32_bf16 v[36:39], v[144:147], v[200:203], v[36:39]
	v_mfma_f32_16x16x32_bf16 v[32:35], v[176:179], v[200:203], v[32:35]
	v_mfma_f32_16x16x32_bf16 v[20:23], v[144:147], v[208:211], v[20:23]
	v_mfma_f32_16x16x32_bf16 v[16:19], v[176:179], v[208:211], v[16:19]
	v_mfma_f32_16x16x32_bf16 v[4:7], v[144:147], v[216:219], v[4:7]
	v_mfma_f32_16x16x32_bf16 v[0:3], v[176:179], v[216:219], v[0:3]
	v_mfma_f32_16x16x32_bf16 v[52:55], v[148:151], v[188:191], v[52:55]
	v_mfma_f32_16x16x32_bf16 v[48:51], v[180:183], v[188:191], v[48:51]
	v_mfma_f32_16x16x32_bf16 v[36:39], v[148:151], v[204:207], v[36:39]
	v_mfma_f32_16x16x32_bf16 v[32:35], v[180:183], v[204:207], v[32:35]
	v_mfma_f32_16x16x32_bf16 v[20:23], v[148:151], v[212:215], v[20:23]
	v_mfma_f32_16x16x32_bf16 v[16:19], v[180:183], v[212:215], v[16:19]
	v_mfma_f32_16x16x32_bf16 v[4:7], v[148:151], v[230:233], v[4:7]
	v_mfma_f32_16x16x32_bf16 v[0:3], v[180:183], v[230:233], v[0:3]
	s_setprio 0
	s_barrier
	s_add_i32 s61, s61, 2
	s_add_u32 s59, s59, 0x100
	s_addc_u32 s60, s60, 0
	s_add_u32 s8, s8, 0x100
	s_addc_u32 s9, s9, 0
	s_branch .LBB0_189
.Lpeel_zero_P1:
	v_mov_b32_e32 v1, v0
	v_mov_b32_e32 v2, v0
	v_mov_b32_e32 v3, v0
	v_mov_b32_e32 v4, v0
	v_mov_b32_e32 v5, v0
	v_mov_b32_e32 v6, v0
	v_mov_b32_e32 v7, v0
	v_mov_b32_e32 v16, v0
	v_mov_b32_e32 v17, v0
	v_mov_b32_e32 v18, v0
	v_mov_b32_e32 v19, v0
	v_mov_b32_e32 v20, v0
	v_mov_b32_e32 v21, v0
	v_mov_b32_e32 v22, v0
	v_mov_b32_e32 v23, v0
	v_mov_b32_e32 v32, v0
	v_mov_b32_e32 v33, v0
	v_mov_b32_e32 v34, v0
	v_mov_b32_e32 v35, v0
	v_mov_b32_e32 v36, v0
	v_mov_b32_e32 v37, v0
	v_mov_b32_e32 v38, v0
	v_mov_b32_e32 v39, v0
	v_mov_b32_e32 v48, v0
	v_mov_b32_e32 v49, v0
	v_mov_b32_e32 v50, v0
	v_mov_b32_e32 v51, v0
	v_mov_b32_e32 v52, v0
	v_mov_b32_e32 v53, v0
	v_mov_b32_e32 v54, v0
	v_mov_b32_e32 v55, v0
	v_mov_b32_e32 v8, v0
	v_mov_b32_e32 v9, v0
	v_mov_b32_e32 v10, v0
	v_mov_b32_e32 v11, v0
	v_mov_b32_e32 v12, v0
	v_mov_b32_e32 v13, v0
	v_mov_b32_e32 v14, v0
	v_mov_b32_e32 v15, v0
	v_mov_b32_e32 v24, v0
	v_mov_b32_e32 v25, v0
	v_mov_b32_e32 v26, v0
	v_mov_b32_e32 v27, v0
	v_mov_b32_e32 v28, v0
	v_mov_b32_e32 v29, v0
	v_mov_b32_e32 v30, v0
	v_mov_b32_e32 v31, v0
	v_mov_b32_e32 v40, v0
	v_mov_b32_e32 v41, v0
	v_mov_b32_e32 v42, v0
	v_mov_b32_e32 v43, v0
	v_mov_b32_e32 v44, v0
	v_mov_b32_e32 v45, v0
	v_mov_b32_e32 v46, v0
	v_mov_b32_e32 v47, v0
	v_mov_b32_e32 v56, v0
	v_mov_b32_e32 v57, v0
	v_mov_b32_e32 v58, v0
	v_mov_b32_e32 v59, v0
	v_mov_b32_e32 v60, v0
	v_mov_b32_e32 v61, v0
	v_mov_b32_e32 v62, v0
	v_mov_b32_e32 v63, v0
	v_mov_b32_e32 v64, v0
	v_mov_b32_e32 v65, v0
	v_mov_b32_e32 v66, v0
	v_mov_b32_e32 v67, v0
	v_mov_b32_e32 v68, v0
	v_mov_b32_e32 v69, v0
	v_mov_b32_e32 v70, v0
	v_mov_b32_e32 v71, v0
	v_mov_b32_e32 v80, v0
	v_mov_b32_e32 v81, v0
	v_mov_b32_e32 v82, v0
	v_mov_b32_e32 v83, v0
	v_mov_b32_e32 v84, v0
	v_mov_b32_e32 v85, v0
	v_mov_b32_e32 v86, v0
	v_mov_b32_e32 v87, v0
	v_mov_b32_e32 v96, v0
	v_mov_b32_e32 v97, v0
	v_mov_b32_e32 v98, v0
	v_mov_b32_e32 v99, v0
	v_mov_b32_e32 v100, v0
	v_mov_b32_e32 v101, v0
	v_mov_b32_e32 v102, v0
	v_mov_b32_e32 v103, v0
	v_mov_b32_e32 v112, v0
	v_mov_b32_e32 v113, v0
	v_mov_b32_e32 v114, v0
	v_mov_b32_e32 v115, v0
	v_mov_b32_e32 v116, v0
	v_mov_b32_e32 v117, v0
	v_mov_b32_e32 v118, v0
	v_mov_b32_e32 v119, v0
	v_mov_b32_e32 v72, v0
	v_mov_b32_e32 v73, v0
	v_mov_b32_e32 v74, v0
	v_mov_b32_e32 v75, v0
	v_mov_b32_e32 v76, v0
	v_mov_b32_e32 v77, v0
	v_mov_b32_e32 v78, v0
	v_mov_b32_e32 v79, v0
	v_mov_b32_e32 v88, v0
	v_mov_b32_e32 v89, v0
	v_mov_b32_e32 v90, v0
	v_mov_b32_e32 v91, v0
	v_mov_b32_e32 v92, v0
	v_mov_b32_e32 v93, v0
	v_mov_b32_e32 v94, v0
	v_mov_b32_e32 v95, v0
	v_mov_b32_e32 v104, v0
	v_mov_b32_e32 v105, v0
	v_mov_b32_e32 v106, v0
	v_mov_b32_e32 v107, v0
	v_mov_b32_e32 v108, v0
	v_mov_b32_e32 v109, v0
	v_mov_b32_e32 v110, v0
	v_mov_b32_e32 v111, v0
	v_mov_b32_e32 v120, v0
	v_mov_b32_e32 v121, v0
	v_mov_b32_e32 v122, v0
	v_mov_b32_e32 v123, v0
	v_mov_b32_e32 v124, v0
	v_mov_b32_e32 v125, v0
	v_mov_b32_e32 v126, v0
	v_mov_b32_e32 v127, v0

.Lstg_b8:
	v_mov_b64_e32 v[144:145], s[70:71]
	flat_load_dword v146, v[144:145] sc0 sc1
	s_waitcnt vmcnt(0)
	v_mov_b64_e32 v[144:145], s[76:77]
	flat_load_dword v144, v[144:145] sc0 sc1
	s_waitcnt vmcnt(0) lgkmcnt(0)
	v_readfirstlane_b32 s6, v146
	v_readfirstlane_b32 s7, v144
	s_nop 1
	s_nop 3
	s_mov_b32 m0, s81
	s_nop 0
	global_load_lds_dwordx4 v162, s[6:7]
	s_nop 3
	s_add_i32 m0, s78, 0xffffff80
	s_nop 0
	global_load_lds_dwordx4 v162, s[6:7] offset:128
	s_add_i32 m0, s69, 0xffffff00
	s_nop 0
	global_load_lds_dwordx4 v162, s[6:7] offset:256
	s_add_i32 m0, s68, 0xfffffe80
	s_nop 0
	global_load_lds_dwordx4 v162, s[6:7] offset:384
	ds_read_b64_tr_b16 v[144:145], v177 offset:0x8000
	ds_read_b64_tr_b16 v[146:147], v177 offset:0x9000
	ds_read_b64_tr_b16 v[148:149], v177 offset:0xa000
	ds_read_b64_tr_b16 v[150:151], v177 offset:0xb000
	ds_read_b64_tr_b16 v[152:153], v177 offset:0xc000
	ds_read_b64_tr_b16 v[154:155], v177 offset:0xd000
	ds_read_b64_tr_b16 v[156:157], v177 offset:0xe000
	ds_read_b64_tr_b16 v[158:159], v177 offset:0xf000
	ds_read_b64_tr_b16 v[166:167], v177 offset:0x8200
	ds_read_b64_tr_b16 v[168:169], v177 offset:0x9200
	ds_read_b64_tr_b16 v[170:171], v177 offset:0xa200
	ds_read_b64_tr_b16 v[172:173], v177 offset:0xb200
	ds_read_b64_tr_b16 v[180:181], v177 offset:0xc200
	ds_read_b64_tr_b16 v[182:183], v177 offset:0xd200
	ds_read_b64_tr_b16 v[184:185], v177 offset:0xe200
	ds_read_b64_tr_b16 v[186:187], v177 offset:0xf200
	s_waitcnt lgkmcnt(8)
	s_nop 1
	v_mfma_f32_32x32x16_bf16 v[112:127], v[144:147], v[128:131], v[112:127]
	v_mfma_f32_32x32x16_bf16 v[112:127], v[148:151], v[132:135], v[112:127]
	v_mfma_f32_32x32x16_bf16 v[112:127], v[152:155], v[136:139], v[112:127]
	v_mfma_f32_32x32x16_bf16 v[112:127], v[156:159], v[140:143], v[112:127]
	ds_read_b64_tr_b16 v[144:145], v177 offset:0x8400
	ds_read_b64_tr_b16 v[146:147], v177 offset:0x9400
	ds_read_b64_tr_b16 v[148:149], v177 offset:0xa400
	ds_read_b64_tr_b16 v[150:151], v177 offset:0xb400
	ds_read_b64_tr_b16 v[152:153], v177 offset:0xc400
	ds_read_b64_tr_b16 v[154:155], v177 offset:0xd400
	ds_read_b64_tr_b16 v[156:157], v177 offset:0xe400
	ds_read_b64_tr_b16 v[158:159], v177 offset:0xf400
	s_waitcnt lgkmcnt(8)
	v_mfma_f32_32x32x16_bf16 v[0:15], v[166:169], v[128:131], v[0:15]
	v_mfma_f32_32x32x16_bf16 v[0:15], v[170:173], v[132:135], v[0:15]
	v_mfma_f32_32x32x16_bf16 v[0:15], v[180:183], v[136:139], v[0:15]
	v_mfma_f32_32x32x16_bf16 v[0:15], v[184:187], v[140:143], v[0:15]
	ds_read_b64_tr_b16 v[166:167], v177 offset:0x8600
	ds_read_b64_tr_b16 v[168:169], v177 offset:0x9600
	ds_read_b64_tr_b16 v[170:171], v177 offset:0xa600
	ds_read_b64_tr_b16 v[172:173], v177 offset:0xb600
	ds_read_b64_tr_b16 v[180:181], v177 offset:0xc600
	ds_read_b64_tr_b16 v[182:183], v177 offset:0xd600
	ds_read_b64_tr_b16 v[184:185], v177 offset:0xe600
	ds_read_b64_tr_b16 v[186:187], v177 offset:0xf600
	s_waitcnt lgkmcnt(8)
	v_mfma_f32_32x32x16_bf16 v[16:31], v[144:147], v[128:131], v[16:31]
	v_mfma_f32_32x32x16_bf16 v[16:31], v[148:151], v[132:135], v[16:31]
	v_mfma_f32_32x32x16_bf16 v[16:31], v[152:155], v[136:139], v[16:31]
	v_mfma_f32_32x32x16_bf16 v[16:31], v[156:159], v[140:143], v[16:31]
	ds_read_b64_tr_b16 v[144:145], v177 offset:0x8800
	ds_read_b64_tr_b16 v[146:147], v177 offset:0x9800
	ds_read_b64_tr_b16 v[148:149], v177 offset:0xa800
	ds_read_b64_tr_b16 v[150:151], v177 offset:0xb800
	ds_read_b64_tr_b16 v[152:153], v177 offset:0xc800
	ds_read_b64_tr_b16 v[154:155], v177 offset:0xd800
	ds_read_b64_tr_b16 v[156:157], v177 offset:0xe800
	ds_read_b64_tr_b16 v[158:159], v177 offset:0xf800
	s_waitcnt lgkmcnt(8)
	v_mfma_f32_32x32x16_bf16 v[32:47], v[166:169], v[128:131], v[32:47]
	v_mfma_f32_32x32x16_bf16 v[32:47], v[170:173], v[132:135], v[32:47]
	v_mfma_f32_32x32x16_bf16 v[32:47], v[180:183], v[136:139], v[32:47]
	v_mfma_f32_32x32x16_bf16 v[32:47], v[184:187], v[140:143], v[32:47]
	ds_read_b64_tr_b16 v[166:167], v177 offset:0x8a00
	ds_read_b64_tr_b16 v[168:169], v177 offset:0x9a00
	ds_read_b64_tr_b16 v[170:171], v177 offset:0xaa00
	ds_read_b64_tr_b16 v[172:173], v177 offset:0xba00
	ds_read_b64_tr_b16 v[180:181], v177 offset:0xca00
	ds_read_b64_tr_b16 v[182:183], v177 offset:0xda00
	ds_read_b64_tr_b16 v[184:185], v177 offset:0xea00
	ds_read_b64_tr_b16 v[186:187], v177 offset:0xfa00
	s_waitcnt lgkmcnt(8)
	v_mfma_f32_32x32x16_bf16 v[48:63], v[144:147], v[128:131], v[48:63]
	v_mfma_f32_32x32x16_bf16 v[48:63], v[148:151], v[132:135], v[48:63]
	v_mfma_f32_32x32x16_bf16 v[48:63], v[152:155], v[136:139], v[48:63]
	v_mfma_f32_32x32x16_bf16 v[48:63], v[156:159], v[140:143], v[48:63]
	ds_read_b64_tr_b16 v[144:145], v177 offset:0x8c00
	ds_read_b64_tr_b16 v[146:147], v177 offset:0x9c00
	ds_read_b64_tr_b16 v[148:149], v177 offset:0xac00
	ds_read_b64_tr_b16 v[150:151], v177 offset:0xbc00
	ds_read_b64_tr_b16 v[152:153], v177 offset:0xcc00
	ds_read_b64_tr_b16 v[154:155], v177 offset:0xdc00
	ds_read_b64_tr_b16 v[156:157], v177 offset:0xec00
	ds_read_b64_tr_b16 v[158:159], v177 offset:0xfc00
	s_waitcnt lgkmcnt(8)
	v_mfma_f32_32x32x16_bf16 v[64:79], v[166:169], v[128:131], v[64:79]
	v_mfma_f32_32x32x16_bf16 v[64:79], v[170:173], v[132:135], v[64:79]
	v_mfma_f32_32x32x16_bf16 v[64:79], v[180:183], v[136:139], v[64:79]
	v_mfma_f32_32x32x16_bf16 v[64:79], v[184:187], v[140:143], v[64:79]
	ds_read_b64_tr_b16 v[166:167], v177 offset:0x8e00
	ds_read_b64_tr_b16 v[168:169], v177 offset:0x9e00
	ds_read_b64_tr_b16 v[170:171], v177 offset:0xae00
	ds_read_b64_tr_b16 v[172:173], v177 offset:0xbe00
	ds_read_b64_tr_b16 v[180:181], v177 offset:0xce00
	ds_read_b64_tr_b16 v[182:183], v177 offset:0xde00
	ds_read_b64_tr_b16 v[184:185], v177 offset:0xee00
	ds_read_b64_tr_b16 v[186:187], v177 offset:0xfe00
	s_waitcnt lgkmcnt(8)
	v_mfma_f32_32x32x16_bf16 v[80:95], v[144:147], v[128:131], v[80:95]
	v_mfma_f32_32x32x16_bf16 v[80:95], v[148:151], v[132:135], v[80:95]
	v_mfma_f32_32x32x16_bf16 v[80:95], v[152:155], v[136:139], v[80:95]
	v_mfma_f32_32x32x16_bf16 v[80:95], v[156:159], v[140:143], v[80:95]
	s_waitcnt lgkmcnt(0)
	v_mfma_f32_32x32x16_bf16 v[96:111], v[166:169], v[128:131], v[96:111]
	v_mfma_f32_32x32x16_bf16 v[96:111], v[170:173], v[132:135], v[96:111]
	v_mfma_f32_32x32x16_bf16 v[96:111], v[180:183], v[136:139], v[96:111]
	v_mfma_f32_32x32x16_bf16 v[96:111], v[184:187], v[140:143], v[96:111]
	v_readlane_b32 s6, v255, 31
	v_readlane_b32 s7, v255, 32
	v_readlane_b32 s12, v255, 49
	v_readlane_b32 s13, v255, 50
	v_mov_b64_e32 v[128:129], s[6:7]
	v_readlane_b32 s6, v255, 35
	v_readlane_b32 s7, v255, 36
	flat_load_dword v130, v[128:129] sc0 sc1
	s_waitcnt vmcnt(0)
	s_ashr_i32 s13, s12, 31
	v_mov_b64_e32 v[128:129], s[6:7]
	flat_load_dword v131, v[128:129] sc0 sc1
	s_waitcnt vmcnt(0)
	s_lshl_b64 s[6:7], s[12:13], 11
	v_lshl_or_b32 v128, v175, 11, v174
	v_mov_b32_e32 v129, v161
	s_waitcnt lgkmcnt(0)
	s_barrier
	v_add_f32_e32 v158, v179, v204
	s_waitcnt lgkmcnt(0)
	v_readfirstlane_b32 s9, v130
	s_add_u32 s6, s9, s6
	v_readfirstlane_b32 s8, v131
	s_addc_u32 s7, s8, s7
	v_lshl_add_u64 v[156:157], s[6:7], 0, v[128:129]
	flat_load_dwordx4 v[128:131], v[156:157]
	flat_load_dwordx4 v[132:135], v[156:157] offset:32
	flat_load_dwordx4 v[136:139], v[156:157] offset:64
	flat_load_dwordx4 v[140:143], v[156:157] offset:96
	flat_load_dwordx4 v[144:147], v[156:157] offset:128
	flat_load_dwordx4 v[148:151], v[156:157] offset:160
	flat_load_dwordx4 v[152:155], v[156:157] offset:192
	flat_load_dwordx4 v[166:169], v[156:157] offset:224
	v_readlane_b32 s6, v255, 51
	v_readlane_b32 s7, v255, 52
	s_add_u32 s4, s4, s6
	s_addc_u32 s5, s5, s7
	v_lshl_add_u64 v[156:157], s[4:5], 0, v[160:161]
	flat_load_dword v156, v[156:157]
	v_mov_b32_e32 v157, v158
	s_nop 1
	v_permlane32_swap_b32_e32 v158, v157
	v_add_f32_e32 v157, v158, v157
	s_mul_i32 s5, s12, 0x6800
	s_mul_hi_i32 s4, s12, 0x6800
	s_add_u32 s2, s2, s5
	s_addc_u32 s3, s3, s4
	s_add_u32 s4, s2, 0x1000
	s_addc_u32 s5, s3, 0
	v_readlane_b32 s2, v255, 27
	s_waitcnt vmcnt(0) lgkmcnt(0)
	v_max_f32_e32 v156, v156, v156
	v_max_f32_e64 v156, |v157|, v156
	v_rcp_f32_e32 v194, v156
	s_nop 0
	v_mul_f32_e32 v196, v113, v194
	v_mul_f32_e32 v213, v115, v194
	v_mul_f32_e32 v195, v112, v194
	v_mul_f32_e32 v197, v114, v194
	v_mul_f32_e32 v217, v119, v194
	v_mul_f32_e32 v119, v52, v194
	v_mul_f32_e32 v115, v54, v194
	v_mul_f32_e32 v54, v56, v194
	v_mul_f32_e32 v52, v57, v194
	v_mul_f32_e32 v56, v196, v196
	v_mul_f32_e32 v57, v213, v213
	v_mul_f32_e32 v215, v117, v194
	v_fmac_f32_e32 v56, v195, v195
	v_fmac_f32_e32 v57, v197, v197
	v_mul_f32_e32 v214, v116, v194
	v_mul_f32_e32 v216, v118, v194
	v_mul_f32_e32 v114, v50, v194
	v_mul_f32_e32 v50, v58, v194
	v_add_f32_e32 v56, v56, v57
	v_mul_f32_e32 v57, v215, v215
	v_mul_f32_e32 v58, v217, v217
	v_mul_f32_e32 v219, v121, v194
	v_mul_f32_e32 v210, v123, v194
	v_fmac_f32_e32 v57, v214, v214
	v_fmac_f32_e32 v58, v216, v216
	v_mul_f32_e32 v218, v120, v194
	v_mul_f32_e32 v212, v122, v194
	v_mul_f32_e32 v118, v48, v194
	v_mul_f32_e32 v48, v59, v194
	v_add_f32_e32 v57, v57, v58
	v_mul_f32_e32 v58, v219, v219
	v_mul_f32_e32 v59, v210, v210
	v_mul_f32_e32 v221, v125, v194
	v_mul_f32_e32 v211, v127, v194
	v_fmac_f32_e32 v58, v218, v218
	v_fmac_f32_e32 v59, v212, v212
	v_mul_f32_e32 v220, v124, v194
	v_mul_f32_e32 v222, v126, v194
	v_mul_f32_e32 v113, v55, v194
	v_mul_f32_e32 v55, v60, v194
	v_add_f32_e32 v58, v58, v59
	v_mul_f32_e32 v59, v221, v221
	v_mul_f32_e32 v60, v211, v211
	v_fmac_f32_e32 v59, v220, v220
	v_fmac_f32_e32 v60, v222, v222
	v_add_f32_e32 v59, v59, v60
	v_mul_f32_e32 v206, v1, v194
	v_mul_f32_e32 v202, v3, v194
	v_add_f32_e32 v56, v56, v57
	v_add_f32_e32 v57, v58, v59
	v_mul_f32_e32 v208, v0, v194
	v_mul_f32_e32 v204, v2, v194
	v_add_f32_e32 v56, v56, v57
	v_mul_f32_e32 v57, v206, v206
	v_mul_f32_e32 v58, v202, v202
	v_mul_f32_e32 v207, v5, v194
	v_mul_f32_e32 v203, v7, v194
	v_fmac_f32_e32 v57, v208, v208
	v_fmac_f32_e32 v58, v204, v204
	v_mul_f32_e32 v209, v4, v194
	v_mul_f32_e32 v205, v6, v194
	v_add_f32_e32 v57, v57, v58
	v_mul_f32_e32 v58, v207, v207
	v_mul_f32_e32 v59, v203, v203
	v_mul_f32_e32 v198, v9, v194
	v_mul_f32_e32 v190, v11, v194
	v_fmac_f32_e32 v58, v209, v209
	v_fmac_f32_e32 v59, v205, v205
	v_mul_f32_e32 v200, v8, v194
	v_mul_f32_e32 v192, v10, v194
	v_add_f32_e32 v58, v58, v59
	v_mul_f32_e32 v59, v198, v198
	v_mul_f32_e32 v60, v190, v190
	v_mul_f32_e32 v199, v13, v194
	v_mul_f32_e32 v191, v15, v194
	v_fmac_f32_e32 v59, v200, v200
	v_fmac_f32_e32 v60, v192, v192
	v_mul_f32_e32 v201, v12, v194
	v_mul_f32_e32 v193, v14, v194
	v_mul_f32_e32 v117, v53, v194
	v_mul_f32_e32 v53, v61, v194
	v_add_f32_e32 v59, v59, v60
	v_mul_f32_e32 v60, v199, v199
	v_mul_f32_e32 v61, v191, v191
	v_fmac_f32_e32 v60, v201, v201
	v_fmac_f32_e32 v61, v193, v193
	v_add_f32_e32 v60, v60, v61
	v_add_f32_e32 v57, v57, v58
	v_add_f32_e32 v58, v59, v60
	v_mul_f32_e32 v186, v17, v194
	v_mul_f32_e32 v182, v19, v194
	v_add_f32_e32 v57, v57, v58
	v_mul_f32_e32 v188, v16, v194
	v_mul_f32_e32 v184, v18, v194
	v_add_f32_e32 v56, v56, v57
	v_mul_f32_e32 v57, v186, v186
	v_mul_f32_e32 v58, v182, v182
	v_mul_f32_e32 v187, v21, v194
	v_mul_f32_e32 v183, v23, v194
	v_fmac_f32_e32 v57, v188, v188
	v_fmac_f32_e32 v58, v184, v184
	v_mul_f32_e32 v189, v20, v194
	v_mul_f32_e32 v185, v22, v194
	v_add_f32_e32 v57, v57, v58
	v_mul_f32_e32 v58, v187, v187
	v_mul_f32_e32 v59, v183, v183
	v_mul_f32_e32 v178, v25, v194
	v_mul_f32_e32 v171, v27, v194
	v_fmac_f32_e32 v58, v189, v189
	v_fmac_f32_e32 v59, v185, v185
	v_mul_f32_e32 v180, v24, v194
	v_mul_f32_e32 v173, v26, v194
	v_add_f32_e32 v58, v58, v59
	v_mul_f32_e32 v59, v178, v178
	v_mul_f32_e32 v60, v171, v171
	v_mul_f32_e32 v179, v29, v194
	v_mul_f32_e32 v172, v31, v194
	v_fmac_f32_e32 v59, v180, v180
	v_fmac_f32_e32 v60, v173, v173
	v_mul_f32_e32 v181, v28, v194
	v_mul_f32_e32 v177, v30, v194
	v_add_f32_e32 v59, v59, v60
	v_mul_f32_e32 v60, v179, v179
	v_mul_f32_e32 v61, v172, v172
	v_fmac_f32_e32 v60, v181, v181
	v_fmac_f32_e32 v61, v177, v177
	v_add_f32_e32 v60, v60, v61
	v_add_f32_e32 v57, v57, v58
	v_add_f32_e32 v58, v59, v60
	v_mul_f32_e32 v160, v33, v194
	v_mul_f32_e32 v156, v35, v194
	v_add_f32_e32 v57, v57, v58
	v_mul_f32_e32 v163, v32, v194
	v_mul_f32_e32 v158, v34, v194
	v_add_f32_e32 v56, v57, v56
	v_mul_f32_e32 v57, v160, v160
	v_mul_f32_e32 v58, v156, v156
	v_mul_f32_e32 v162, v37, v194
	v_mul_f32_e32 v157, v39, v194
	v_fmac_f32_e32 v57, v163, v163
	v_fmac_f32_e32 v58, v158, v158
	v_mul_f32_e32 v170, v36, v194
	v_mul_f32_e32 v159, v38, v194
	v_add_f32_e32 v57, v57, v58
	v_mul_f32_e32 v58, v162, v162
	v_mul_f32_e32 v59, v157, v157
	v_mul_f32_e32 v124, v41, v194
	v_mul_f32_e32 v120, v43, v194
	v_fmac_f32_e32 v58, v170, v170
	v_fmac_f32_e32 v59, v159, v159
	v_mul_f32_e32 v126, v40, v194
	v_mul_f32_e32 v122, v42, v194
	v_add_f32_e32 v58, v58, v59
	v_mul_f32_e32 v59, v124, v124
	v_mul_f32_e32 v60, v120, v120
	v_mul_f32_e32 v125, v45, v194
	v_mul_f32_e32 v121, v47, v194
	v_fmac_f32_e32 v59, v126, v126
	v_fmac_f32_e32 v60, v122, v122
	v_mul_f32_e32 v127, v44, v194
	v_mul_f32_e32 v123, v46, v194
	v_add_f32_e32 v59, v59, v60
	v_mul_f32_e32 v60, v125, v125
	v_mul_f32_e32 v61, v121, v121
	v_fmac_f32_e32 v60, v127, v127
	v_fmac_f32_e32 v61, v123, v123
	v_add_f32_e32 v60, v60, v61
	v_add_f32_e32 v57, v57, v58
	v_add_f32_e32 v58, v59, v60
	v_mul_f32_e32 v116, v49, v194
	v_mul_f32_e32 v112, v51, v194
	v_add_f32_e32 v57, v57, v58
	v_add_f32_e32 v56, v57, v56
	v_mul_f32_e32 v57, v116, v116
	v_mul_f32_e32 v58, v112, v112
	v_fmac_f32_e32 v57, v118, v118
	v_fmac_f32_e32 v58, v114, v114
	v_add_f32_e32 v57, v57, v58
	v_mul_f32_e32 v58, v117, v117
	v_mul_f32_e32 v59, v113, v113
	v_fmac_f32_e32 v58, v119, v119
	v_fmac_f32_e32 v59, v115, v115
	v_add_f32_e32 v58, v58, v59
	v_mul_f32_e32 v59, v52, v52
	v_mul_f32_e32 v60, v48, v48
	v_mul_f32_e32 v49, v63, v194
	v_fmac_f32_e32 v59, v54, v54
	v_fmac_f32_e32 v60, v50, v50
	v_mul_f32_e32 v51, v62, v194
	v_add_f32_e32 v59, v59, v60
	v_mul_f32_e32 v60, v53, v53
	v_mul_f32_e32 v61, v49, v49
	v_fmac_f32_e32 v60, v55, v55
	v_fmac_f32_e32 v61, v51, v51
	v_add_f32_e32 v60, v60, v61
	v_add_f32_e32 v57, v57, v58
	v_add_f32_e32 v58, v59, v60
	v_mul_f32_e32 v44, v65, v194
	v_mul_f32_e32 v40, v67, v194
	v_add_f32_e32 v57, v57, v58
	v_mul_f32_e32 v46, v64, v194
	v_mul_f32_e32 v42, v66, v194
	v_add_f32_e32 v56, v57, v56
	v_mul_f32_e32 v57, v44, v44
	v_mul_f32_e32 v58, v40, v40
	v_mul_f32_e32 v45, v69, v194
	v_mul_f32_e32 v41, v71, v194
	v_fmac_f32_e32 v57, v46, v46
	v_fmac_f32_e32 v58, v42, v42
	v_mul_f32_e32 v47, v68, v194
	v_mul_f32_e32 v43, v70, v194
	v_add_f32_e32 v57, v57, v58
	v_mul_f32_e32 v58, v45, v45
	v_mul_f32_e32 v59, v41, v41
	v_mul_f32_e32 v36, v73, v194
	v_mul_f32_e32 v32, v75, v194
	v_fmac_f32_e32 v58, v47, v47
	v_fmac_f32_e32 v59, v43, v43
	v_mul_f32_e32 v38, v72, v194
	v_mul_f32_e32 v34, v74, v194
	v_add_f32_e32 v58, v58, v59
	v_mul_f32_e32 v59, v36, v36
	v_mul_f32_e32 v60, v32, v32
	v_mul_f32_e32 v37, v77, v194
	v_mul_f32_e32 v33, v79, v194
	v_fmac_f32_e32 v59, v38, v38
	v_fmac_f32_e32 v60, v34, v34
	v_mul_f32_e32 v39, v76, v194
	v_mul_f32_e32 v35, v78, v194
	v_add_f32_e32 v59, v59, v60
	v_mul_f32_e32 v60, v37, v37
	v_mul_f32_e32 v61, v33, v33
	v_fmac_f32_e32 v60, v39, v39
	v_fmac_f32_e32 v61, v35, v35
	v_mul_f32_e32 v31, v84, v194
	v_add_f32_e32 v60, v60, v61
	v_mul_u32_u24_e32 v84, 0x6800, v175
	v_add_f32_e32 v57, v57, v58
	v_add_f32_e32 v58, v59, v60
	v_lshl_or_b32 v59, v176, 3, v84
	global_load_dwordx2 v[68:69], v59, s[4:5]
	global_load_dwordx2 v[70:71], v59, s[4:5] offset:16
	global_load_dwordx2 v[72:73], v59, s[4:5] offset:32
	global_load_dwordx2 v[74:75], v59, s[4:5] offset:48
	v_mul_f32_e32 v30, v80, v194
	v_mul_f32_e32 v28, v81, v194
	v_mul_f32_e32 v26, v82, v194
	v_mul_f32_e32 v24, v83, v194
	v_add_f32_e32 v57, v57, v58
	global_load_dwordx2 v[76:77], v59, s[4:5] offset:64
	global_load_dwordx2 v[78:79], v59, s[4:5] offset:80
	global_load_dwordx2 v[80:81], v59, s[4:5] offset:96
	global_load_dwordx2 v[82:83], v59, s[4:5] offset:112
	v_add_f32_e32 v56, v57, v56
	v_mul_f32_e32 v57, v28, v28
	v_mul_f32_e32 v58, v24, v24
	v_mul_f32_e32 v29, v85, v194
	v_mul_f32_e32 v25, v87, v194
	v_fmac_f32_e32 v57, v30, v30
	v_fmac_f32_e32 v58, v26, v26
	v_mul_f32_e32 v27, v86, v194
	v_add_f32_e32 v57, v57, v58
	v_mul_f32_e32 v58, v29, v29
	v_mul_f32_e32 v60, v25, v25
	v_mul_f32_e32 v20, v89, v194
	v_mul_f32_e32 v16, v91, v194
	v_fmac_f32_e32 v58, v31, v31
	v_fmac_f32_e32 v60, v27, v27
	v_mul_f32_e32 v22, v88, v194
	v_mul_f32_e32 v18, v90, v194
	v_add_f32_e32 v58, v58, v60
	v_mul_f32_e32 v60, v20, v20
	v_mul_f32_e32 v61, v16, v16
	v_mul_f32_e32 v21, v93, v194
	v_mul_f32_e32 v17, v95, v194
	v_fmac_f32_e32 v60, v22, v22
	v_fmac_f32_e32 v61, v18, v18
	v_mul_f32_e32 v23, v92, v194
	v_mul_f32_e32 v19, v94, v194
	v_add_f32_e32 v60, v60, v61
	v_mul_f32_e32 v61, v21, v21
	v_mul_f32_e32 v62, v17, v17
	v_fmac_f32_e32 v61, v23, v23
	v_fmac_f32_e32 v62, v19, v19
	v_add_f32_e32 v61, v61, v62
	v_add_f32_e32 v57, v57, v58
	v_add_f32_e32 v58, v60, v61
	v_mul_f32_e32 v12, v97, v194
	v_mul_f32_e32 v8, v99, v194
	v_add_f32_e32 v57, v57, v58
	v_mul_f32_e32 v14, v96, v194
	v_mul_f32_e32 v10, v98, v194
	v_add_f32_e32 v56, v57, v56
	v_mul_f32_e32 v57, v12, v12
	v_mul_f32_e32 v58, v8, v8
	v_mul_f32_e32 v13, v101, v194
	v_mul_f32_e32 v9, v103, v194
	v_fmac_f32_e32 v57, v14, v14
	v_fmac_f32_e32 v58, v10, v10
	v_mul_f32_e32 v15, v100, v194
	v_mul_f32_e32 v11, v102, v194
	v_add_f32_e32 v57, v57, v58
	v_mul_f32_e32 v58, v13, v13
	v_mul_f32_e32 v60, v9, v9
	v_mul_f32_e32 v4, v105, v194
	v_mul_f32_e32 v0, v107, v194
	v_fmac_f32_e32 v58, v15, v15
	v_fmac_f32_e32 v60, v11, v11
	v_mul_f32_e32 v6, v104, v194
	v_mul_f32_e32 v2, v106, v194
	v_add_f32_e32 v58, v58, v60
	v_mul_f32_e32 v60, v4, v4
	v_mul_f32_e32 v61, v0, v0
	v_mul_f32_e32 v5, v109, v194
	v_mul_f32_e32 v1, v111, v194
	v_fmac_f32_e32 v60, v6, v6
	v_fmac_f32_e32 v61, v2, v2
	v_mul_f32_e32 v7, v108, v194
	v_mul_f32_e32 v3, v110, v194
	v_add_f32_e32 v60, v60, v61
	v_mul_f32_e32 v61, v5, v5
	v_mul_f32_e32 v62, v1, v1
	v_fmac_f32_e32 v61, v7, v7
	v_fmac_f32_e32 v62, v3, v3
	v_add_f32_e32 v61, v61, v62
	v_add_f32_e32 v57, v57, v58
	v_add_f32_e32 v58, v60, v61
	v_add_f32_e32 v57, v57, v58
	v_add_f32_e32 v56, v57, v56
	v_mov_b32_e32 v57, v56
	s_nop 1
	v_permlane32_swap_b32_e32 v56, v57
	v_add_f32_e32 v56, v56, v57
	v_fmamk_f32 v56, v56, 0x3b800000, v254
	v_rsq_f32_e32 v56, v56
	v_add_u32_e32 v57, s2, v174
	ds_read_b128 v[60:63], v57
	ds_read_b128 v[64:67], v57 offset:32
	v_mul_f32_e32 v58, v195, v56
	v_mul_f32_e32 v54, v54, v56
	v_mul_f32_e32 v52, v52, v56
	s_waitcnt lgkmcnt(1)
	v_mul_f32_e32 v58, v58, v60
	v_mul_f32_e32 v60, v214, v56
	s_waitcnt lgkmcnt(0)
	v_mul_f32_e32 v60, v60, v64
	v_mul_f32_e32 v64, v196, v56
	v_mul_f32_e32 v61, v64, v61
	v_mul_f32_e32 v64, v215, v56
	v_mul_f32_e32 v64, v64, v65
	v_mul_f32_e32 v65, v197, v56
	v_mul_f32_e32 v62, v65, v62
	v_mul_f32_e32 v65, v216, v56
	v_mul_f32_e32 v65, v65, v66
	v_mul_f32_e32 v66, v213, v56
	v_mul_f32_e32 v63, v66, v63
	v_mul_f32_e32 v66, v217, v56
	v_mul_f32_e32 v66, v66, v67
	s_waitcnt vmcnt(7)
	v_lshlrev_b32_e32 v67, 16, v68
	v_mul_f32_e32 v58, v58, v67
	v_and_b32_e32 v67, 0xffff0000, v68
	v_mul_f32_e32 v61, v61, v67
	v_lshlrev_b32_e32 v67, 16, v69
	v_mul_f32_e32 v62, v62, v67
	v_and_b32_e32 v67, 0xffff0000, v69
	v_mul_f32_e32 v63, v63, v67
	s_waitcnt vmcnt(6)
	v_lshlrev_b32_e32 v67, 16, v70
	v_mul_f32_e32 v67, v60, v67
	v_and_b32_e32 v60, 0xffff0000, v70
	v_mul_f32_e32 v64, v64, v60
	v_lshlrev_b32_e32 v60, 16, v71
	v_mul_f32_e32 v65, v65, v60
	v_and_b32_e32 v60, 0xffff0000, v71
	v_mul_f32_e32 v66, v66, v60
	v_cvt_pk_bf16_f32 v60, v58, v61
	v_cvt_pk_bf16_f32 v61, v62, v63
	v_cvt_pk_bf16_f32 v62, v67, v64
	v_cvt_pk_bf16_f32 v63, v65, v66
	ds_read_b128 v[64:67], v57 offset:64
	ds_read_b128 v[68:71], v57 offset:96
	v_permlane32_swap_b32_e32 v60, v62
	v_permlane32_swap_b32_e32 v61, v63
	v_or_b32_e32 v58, v174, v84
	global_store_dwordx4 v58, v[60:63], s[4:5]
	v_mul_f32_e32 v50, v50, v56
	v_mul_f32_e32 v48, v48, v56
	v_mul_f32_e32 v60, v218, v56
	v_mul_f32_e32 v61, v220, v56
	s_waitcnt lgkmcnt(1)
	v_mul_f32_e32 v60, v60, v64
	s_waitcnt lgkmcnt(0)
	v_mul_f32_e32 v61, v61, v68
	v_mul_f32_e32 v62, v219, v56
	s_waitcnt vmcnt(6)
	v_lshlrev_b32_e32 v68, 16, v72
	v_mul_f32_e32 v62, v62, v65
	v_mul_f32_e32 v64, v212, v56
	v_mul_f32_e32 v60, v60, v68
	v_and_b32_e32 v68, 0xffff0000, v72
	v_mul_f32_e32 v64, v64, v66
	v_mul_f32_e32 v66, v210, v56
	v_mul_f32_e32 v62, v62, v68
	v_lshlrev_b32_e32 v68, 16, v73
	v_mul_f32_e32 v66, v66, v67
	v_mul_f32_e32 v64, v64, v68
	v_and_b32_e32 v68, 0xffff0000, v73
	v_mul_f32_e32 v63, v221, v56
	v_mul_f32_e32 v66, v66, v68
	s_waitcnt vmcnt(5)
	v_lshlrev_b32_e32 v68, 16, v74
	v_mul_f32_e32 v63, v63, v69
	v_mul_f32_e32 v65, v222, v56
	v_mul_f32_e32 v68, v61, v68
	v_and_b32_e32 v61, 0xffff0000, v74
	v_mul_f32_e32 v65, v65, v70
	v_mul_f32_e32 v67, v211, v56
	v_mul_f32_e32 v63, v63, v61
	v_lshlrev_b32_e32 v61, 16, v75
	v_mul_f32_e32 v67, v67, v71
	v_mul_f32_e32 v65, v65, v61
	v_and_b32_e32 v61, 0xffff0000, v75
	v_mul_f32_e32 v67, v67, v61
	v_cvt_pk_bf16_f32 v60, v60, v62
	v_cvt_pk_bf16_f32 v61, v64, v66
	v_cvt_pk_bf16_f32 v62, v68, v63
	v_cvt_pk_bf16_f32 v63, v65, v67
	v_mul_f32_e32 v68, v208, v56
	v_permlane32_swap_b32_e32 v60, v62
	v_permlane32_swap_b32_e32 v61, v63
	global_store_dwordx4 v58, v[60:63], s[4:5] offset:32
	global_load_dwordx2 v[72:73], v59, s[4:5] offset:128
	global_load_dwordx2 v[74:75], v59, s[4:5] offset:144
	global_load_dwordx2 v[84:85], v59, s[4:5] offset:160
	global_load_dwordx2 v[86:87], v59, s[4:5] offset:176
	ds_read_b128 v[60:63], v57 offset:128
	ds_read_b128 v[64:67], v57 offset:160
	v_mul_f32_e32 v55, v55, v56
	v_mul_f32_e32 v53, v53, v56
	v_mul_f32_e32 v51, v51, v56
	s_waitcnt lgkmcnt(1)
	v_mul_f32_e32 v60, v68, v60
	v_mul_f32_e32 v68, v209, v56
	s_waitcnt lgkmcnt(0)
	v_mul_f32_e32 v64, v68, v64
	v_mul_f32_e32 v68, v206, v56
	v_mul_f32_e32 v61, v68, v61
	v_mul_f32_e32 v68, v207, v56
	v_mul_f32_e32 v65, v68, v65
	v_mul_f32_e32 v68, v204, v56
	v_mul_f32_e32 v62, v68, v62
	v_mul_f32_e32 v68, v205, v56
	v_mul_f32_e32 v66, v68, v66
	v_mul_f32_e32 v68, v202, v56
	v_mul_f32_e32 v63, v68, v63
	v_mul_f32_e32 v68, v203, v56
	v_mul_f32_e32 v67, v68, v67
	s_waitcnt vmcnt(9)
	v_lshlrev_b32_e32 v68, 16, v76
	v_mul_f32_e32 v60, v60, v68
	v_and_b32_e32 v68, 0xffff0000, v76
	v_mul_f32_e32 v61, v61, v68
	v_lshlrev_b32_e32 v68, 16, v77
	v_mul_f32_e32 v62, v62, v68
	v_and_b32_e32 v68, 0xffff0000, v77
	v_mul_f32_e32 v63, v63, v68
	s_waitcnt vmcnt(8)
	v_lshlrev_b32_e32 v68, 16, v78
	v_mul_f32_e32 v64, v64, v68
	v_and_b32_e32 v68, 0xffff0000, v78
	v_mul_f32_e32 v65, v65, v68
	v_lshlrev_b32_e32 v68, 16, v79
	v_mul_f32_e32 v66, v66, v68
	v_and_b32_e32 v68, 0xffff0000, v79
	v_mul_f32_e32 v67, v67, v68
	v_cvt_pk_bf16_f32 v60, v60, v61
	v_cvt_pk_bf16_f32 v61, v62, v63
	v_cvt_pk_bf16_f32 v62, v64, v65
	v_cvt_pk_bf16_f32 v63, v66, v67
	ds_read_b128 v[64:67], v57 offset:192
	ds_read_b128 v[68:71], v57 offset:224
	v_permlane32_swap_b32_e32 v60, v62
	v_permlane32_swap_b32_e32 v61, v63
	global_store_dwordx4 v58, v[60:63], s[4:5] offset:64
	v_mul_f32_e32 v49, v49, v56
	v_mul_f32_e32 v46, v46, v56
	v_mul_f32_e32 v60, v200, v56
	v_mul_f32_e32 v61, v201, v56
	s_waitcnt lgkmcnt(1)
	v_mul_f32_e32 v60, v60, v64
	s_waitcnt lgkmcnt(0)
	v_mul_f32_e32 v61, v61, v68
	v_mul_f32_e32 v62, v198, v56
	s_waitcnt vmcnt(8)
	v_lshlrev_b32_e32 v68, 16, v80
	v_mul_f32_e32 v62, v62, v65
	v_mul_f32_e32 v64, v192, v56
	v_mul_f32_e32 v60, v60, v68
	v_and_b32_e32 v68, 0xffff0000, v80
	v_mul_f32_e32 v64, v64, v66
	v_mul_f32_e32 v66, v190, v56
	v_mul_f32_e32 v62, v62, v68
	v_lshlrev_b32_e32 v68, 16, v81
	v_mul_f32_e32 v66, v66, v67
	v_mul_f32_e32 v64, v64, v68
	v_and_b32_e32 v68, 0xffff0000, v81
	v_mul_f32_e32 v63, v199, v56
	v_mul_f32_e32 v66, v66, v68
	s_waitcnt vmcnt(7)
	v_lshlrev_b32_e32 v68, 16, v82
	v_mul_f32_e32 v63, v63, v69
	v_mul_f32_e32 v65, v193, v56
	v_mul_f32_e32 v68, v61, v68
	v_and_b32_e32 v61, 0xffff0000, v82
	v_mul_f32_e32 v65, v65, v70
	v_mul_f32_e32 v67, v191, v56
	v_mul_f32_e32 v63, v63, v61
	v_lshlrev_b32_e32 v61, 16, v83
	v_mul_f32_e32 v67, v67, v71
	v_mul_f32_e32 v65, v65, v61
	v_and_b32_e32 v61, 0xffff0000, v83
	v_mul_f32_e32 v67, v67, v61
	v_cvt_pk_bf16_f32 v60, v60, v62
	v_cvt_pk_bf16_f32 v61, v64, v66
	v_cvt_pk_bf16_f32 v62, v68, v63
	v_cvt_pk_bf16_f32 v63, v65, v67
	v_or_b32_e32 v64, 64, v58
	v_permlane32_swap_b32_e32 v60, v62
	v_permlane32_swap_b32_e32 v61, v63
	global_store_dwordx4 v64, v[60:63], s[4:5] offset:32
	global_load_dwordx2 v[76:77], v59, s[4:5] offset:192
	global_load_dwordx2 v[78:79], v59, s[4:5] offset:208
	global_load_dwordx2 v[80:81], v59, s[4:5] offset:224
	global_load_dwordx2 v[82:83], v59, s[4:5] offset:240
	ds_read_b128 v[60:63], v57 offset:256
	ds_read_b128 v[64:67], v57 offset:288
	v_mul_f32_e32 v68, v188, v56
	v_mul_f32_e32 v44, v44, v56
	v_mul_f32_e32 v42, v42, v56
	s_waitcnt lgkmcnt(1)
	v_mul_f32_e32 v60, v68, v60
	v_mul_f32_e32 v68, v189, v56
	s_waitcnt lgkmcnt(0)
	v_mul_f32_e32 v64, v68, v64
	v_mul_f32_e32 v68, v186, v56
	v_mul_f32_e32 v61, v68, v61
	v_mul_f32_e32 v68, v187, v56
	v_mul_f32_e32 v65, v68, v65
	v_mul_f32_e32 v68, v184, v56
	v_mul_f32_e32 v62, v68, v62
	v_mul_f32_e32 v68, v185, v56
	v_mul_f32_e32 v66, v68, v66
	v_mul_f32_e32 v68, v182, v56
	v_mul_f32_e32 v63, v68, v63
	v_mul_f32_e32 v68, v183, v56
	v_mul_f32_e32 v67, v68, v67
	s_waitcnt vmcnt(9)
	v_lshlrev_b32_e32 v68, 16, v72
	v_mul_f32_e32 v60, v60, v68
	v_and_b32_e32 v68, 0xffff0000, v72
	v_mul_f32_e32 v61, v61, v68
	v_lshlrev_b32_e32 v68, 16, v73
	v_mul_f32_e32 v62, v62, v68
	v_and_b32_e32 v68, 0xffff0000, v73
	v_mul_f32_e32 v63, v63, v68
	s_waitcnt vmcnt(8)
	v_lshlrev_b32_e32 v68, 16, v74
	v_mul_f32_e32 v64, v64, v68
	v_and_b32_e32 v68, 0xffff0000, v74
	v_mul_f32_e32 v65, v65, v68
	v_lshlrev_b32_e32 v68, 16, v75
	v_mul_f32_e32 v66, v66, v68
	v_and_b32_e32 v68, 0xffff0000, v75
	v_mul_f32_e32 v67, v67, v68
	v_cvt_pk_bf16_f32 v60, v60, v61
	v_cvt_pk_bf16_f32 v61, v62, v63
	v_cvt_pk_bf16_f32 v62, v64, v65
	v_cvt_pk_bf16_f32 v63, v66, v67
	ds_read_b128 v[64:67], v57 offset:320
	ds_read_b128 v[68:71], v57 offset:352
	v_permlane32_swap_b32_e32 v60, v62
	v_permlane32_swap_b32_e32 v61, v63
	global_store_dwordx4 v58, v[60:63], s[4:5] offset:128
	v_mul_f32_e32 v40, v40, v56
	v_mul_f32_e32 v47, v47, v56
	v_mul_f32_e32 v60, v180, v56
	v_mul_f32_e32 v61, v181, v56
	s_waitcnt lgkmcnt(1)
	v_mul_f32_e32 v60, v60, v64
	s_waitcnt lgkmcnt(0)
	v_mul_f32_e32 v61, v61, v68
	v_mul_f32_e32 v62, v178, v56
	s_waitcnt vmcnt(8)
	v_lshlrev_b32_e32 v68, 16, v84
	v_mul_f32_e32 v62, v62, v65
	v_mul_f32_e32 v64, v173, v56
	v_mul_f32_e32 v60, v60, v68
	v_and_b32_e32 v68, 0xffff0000, v84
	v_mul_f32_e32 v64, v64, v66
	v_mul_f32_e32 v66, v171, v56
	v_mul_f32_e32 v62, v62, v68
	v_lshlrev_b32_e32 v68, 16, v85
	v_mul_f32_e32 v66, v66, v67
	v_mul_f32_e32 v64, v64, v68
	v_and_b32_e32 v68, 0xffff0000, v85
	v_mul_f32_e32 v63, v179, v56
	v_mul_f32_e32 v66, v66, v68
	s_waitcnt vmcnt(7)
	v_lshlrev_b32_e32 v68, 16, v86
	v_mul_f32_e32 v63, v63, v69
	v_mul_f32_e32 v65, v177, v56
	v_mul_f32_e32 v68, v61, v68
	v_and_b32_e32 v61, 0xffff0000, v86
	v_mul_f32_e32 v65, v65, v70
	v_mul_f32_e32 v67, v172, v56
	v_mul_f32_e32 v63, v63, v61
	v_lshlrev_b32_e32 v61, 16, v87
	v_mul_f32_e32 v67, v67, v71
	v_mul_f32_e32 v65, v65, v61
	v_and_b32_e32 v61, 0xffff0000, v87
	v_mul_f32_e32 v67, v67, v61
	v_cvt_pk_bf16_f32 v60, v60, v62
	v_cvt_pk_bf16_f32 v61, v64, v66
	v_cvt_pk_bf16_f32 v62, v68, v63
	v_cvt_pk_bf16_f32 v63, v65, v67
	v_or_b32_e32 v64, 0x80, v58
	v_permlane32_swap_b32_e32 v60, v62
	v_permlane32_swap_b32_e32 v61, v63
	global_store_dwordx4 v64, v[60:63], s[4:5] offset:32
	global_load_dwordx2 v[72:73], v59, s[4:5] offset:256
	global_load_dwordx2 v[74:75], v59, s[4:5] offset:272
	global_load_dwordx2 v[84:85], v59, s[4:5] offset:288
	global_load_dwordx2 v[86:87], v59, s[4:5] offset:304
	ds_read_b128 v[60:63], v57 offset:384
	ds_read_b128 v[64:67], v57 offset:416
	v_mul_f32_e32 v68, v163, v56
	v_mul_f32_e32 v45, v45, v56
	v_mul_f32_e32 v43, v43, v56
	s_waitcnt lgkmcnt(1)
	v_mul_f32_e32 v60, v68, v60
	v_mul_f32_e32 v68, v170, v56
	s_waitcnt lgkmcnt(0)
	v_mul_f32_e32 v64, v68, v64
	v_mul_f32_e32 v68, v160, v56
	v_mul_f32_e32 v61, v68, v61
	v_mul_f32_e32 v68, v162, v56
	v_mul_f32_e32 v65, v68, v65
	v_mul_f32_e32 v68, v158, v56
	v_mul_f32_e32 v62, v68, v62
	v_mul_f32_e32 v68, v159, v56
	v_mul_f32_e32 v66, v68, v66
	v_mul_f32_e32 v68, v156, v56
	v_mul_f32_e32 v63, v68, v63
	v_mul_f32_e32 v68, v157, v56
	v_mul_f32_e32 v67, v68, v67
	s_waitcnt vmcnt(9)
	v_lshlrev_b32_e32 v68, 16, v76
	v_mul_f32_e32 v60, v60, v68
	v_and_b32_e32 v68, 0xffff0000, v76
	v_mul_f32_e32 v61, v61, v68
	v_lshlrev_b32_e32 v68, 16, v77
	v_mul_f32_e32 v62, v62, v68
	v_and_b32_e32 v68, 0xffff0000, v77
	v_mul_f32_e32 v63, v63, v68
	s_waitcnt vmcnt(8)
	v_lshlrev_b32_e32 v68, 16, v78
	v_mul_f32_e32 v64, v64, v68
	v_and_b32_e32 v68, 0xffff0000, v78
	v_mul_f32_e32 v65, v65, v68
	v_lshlrev_b32_e32 v68, 16, v79
	v_mul_f32_e32 v66, v66, v68
	v_and_b32_e32 v68, 0xffff0000, v79
	v_mul_f32_e32 v67, v67, v68
	v_cvt_pk_bf16_f32 v60, v60, v61
	v_cvt_pk_bf16_f32 v61, v62, v63
	v_cvt_pk_bf16_f32 v62, v64, v65
	v_cvt_pk_bf16_f32 v63, v66, v67
	ds_read_b128 v[64:67], v57 offset:448
	ds_read_b128 v[68:71], v57 offset:480
	v_permlane32_swap_b32_e32 v60, v62
	v_permlane32_swap_b32_e32 v61, v63
	global_store_dwordx4 v58, v[60:63], s[4:5] offset:192
	v_mul_f32_e32 v41, v41, v56
	v_mul_f32_e32 v38, v38, v56
	v_mul_f32_e32 v60, v126, v56
	v_mul_f32_e32 v61, v127, v56
	s_waitcnt lgkmcnt(1)
	v_mul_f32_e32 v60, v60, v64
	s_waitcnt lgkmcnt(0)
	v_mul_f32_e32 v61, v61, v68
	v_mul_f32_e32 v62, v124, v56
	s_waitcnt vmcnt(8)
	v_lshlrev_b32_e32 v68, 16, v80
	v_mul_f32_e32 v62, v62, v65
	v_mul_f32_e32 v64, v122, v56
	v_mul_f32_e32 v60, v60, v68
	v_and_b32_e32 v68, 0xffff0000, v80
	v_mul_f32_e32 v64, v64, v66
	v_mul_f32_e32 v66, v120, v56
	v_mul_f32_e32 v62, v62, v68
	v_lshlrev_b32_e32 v68, 16, v81
	v_mul_f32_e32 v66, v66, v67
	v_mul_f32_e32 v64, v64, v68
	v_and_b32_e32 v68, 0xffff0000, v81
	v_mul_f32_e32 v63, v125, v56
	v_mul_f32_e32 v66, v66, v68
	s_waitcnt vmcnt(7)
	v_lshlrev_b32_e32 v68, 16, v82
	v_mul_f32_e32 v63, v63, v69
	v_mul_f32_e32 v65, v123, v56
	v_mul_f32_e32 v68, v61, v68
	v_and_b32_e32 v61, 0xffff0000, v82
	v_mul_f32_e32 v65, v65, v70
	v_mul_f32_e32 v67, v121, v56
	v_mul_f32_e32 v63, v63, v61
	v_lshlrev_b32_e32 v61, 16, v83
	v_mul_f32_e32 v67, v67, v71
	v_mul_f32_e32 v65, v65, v61
	v_and_b32_e32 v61, 0xffff0000, v83
	v_mul_f32_e32 v67, v67, v61
	v_cvt_pk_bf16_f32 v60, v60, v62
	v_cvt_pk_bf16_f32 v61, v64, v66
	v_cvt_pk_bf16_f32 v62, v68, v63
	v_cvt_pk_bf16_f32 v63, v65, v67
	v_or_b32_e32 v64, 0xc0, v58
	v_permlane32_swap_b32_e32 v60, v62
	v_permlane32_swap_b32_e32 v61, v63
	global_store_dwordx4 v64, v[60:63], s[4:5] offset:32
	global_load_dwordx2 v[76:77], v59, s[4:5] offset:320
	global_load_dwordx2 v[78:79], v59, s[4:5] offset:336
	global_load_dwordx2 v[80:81], v59, s[4:5] offset:352
	global_load_dwordx2 v[82:83], v59, s[4:5] offset:368
	ds_read_b128 v[60:63], v57 offset:512
	ds_read_b128 v[64:67], v57 offset:544
	v_mul_f32_e32 v68, v118, v56
	v_mul_f32_e32 v36, v36, v56
	v_mul_f32_e32 v34, v34, v56
	s_waitcnt lgkmcnt(1)
	v_mul_f32_e32 v60, v68, v60
	v_mul_f32_e32 v68, v119, v56
	s_waitcnt lgkmcnt(0)
	v_mul_f32_e32 v64, v68, v64
	v_mul_f32_e32 v68, v116, v56
	v_mul_f32_e32 v61, v68, v61
	v_mul_f32_e32 v68, v117, v56
	v_mul_f32_e32 v65, v68, v65
	v_mul_f32_e32 v68, v114, v56
	v_mul_f32_e32 v62, v68, v62
	v_mul_f32_e32 v68, v115, v56
	v_mul_f32_e32 v66, v68, v66
	v_mul_f32_e32 v68, v112, v56
	v_mul_f32_e32 v63, v68, v63
	v_mul_f32_e32 v68, v113, v56
	v_mul_f32_e32 v67, v68, v67
	s_waitcnt vmcnt(9)
	v_lshlrev_b32_e32 v68, 16, v72
	v_mul_f32_e32 v60, v60, v68
	v_and_b32_e32 v68, 0xffff0000, v72
	v_mul_f32_e32 v61, v61, v68
	v_lshlrev_b32_e32 v68, 16, v73
	v_mul_f32_e32 v62, v62, v68
	v_and_b32_e32 v68, 0xffff0000, v73
	v_mul_f32_e32 v63, v63, v68
	s_waitcnt vmcnt(8)
	v_lshlrev_b32_e32 v68, 16, v74
	v_mul_f32_e32 v64, v64, v68
	v_and_b32_e32 v68, 0xffff0000, v74
	v_mul_f32_e32 v65, v65, v68
	v_lshlrev_b32_e32 v68, 16, v75
	v_mul_f32_e32 v66, v66, v68
	v_and_b32_e32 v68, 0xffff0000, v75
	v_mul_f32_e32 v67, v67, v68
	v_cvt_pk_bf16_f32 v60, v60, v61
	v_cvt_pk_bf16_f32 v61, v62, v63
	v_cvt_pk_bf16_f32 v62, v64, v65
	v_cvt_pk_bf16_f32 v63, v66, v67
	ds_read_b128 v[64:67], v57 offset:576
	ds_read_b128 v[68:71], v57 offset:608
	v_permlane32_swap_b32_e32 v60, v62
	v_permlane32_swap_b32_e32 v61, v63
	global_store_dwordx4 v58, v[60:63], s[4:5] offset:256
	s_waitcnt lgkmcnt(1)
	v_mul_f32_e32 v54, v54, v64
	v_mul_f32_e32 v52, v52, v65
	s_waitcnt vmcnt(8)
	v_lshlrev_b32_e32 v60, 16, v84
	v_mul_f32_e32 v54, v54, v60
	v_and_b32_e32 v60, 0xffff0000, v84
	v_mul_f32_e32 v50, v50, v66
	v_mul_f32_e32 v52, v52, v60
	v_lshlrev_b32_e32 v60, 16, v85
	v_mul_f32_e32 v48, v48, v67
	v_mul_f32_e32 v50, v50, v60
	v_and_b32_e32 v60, 0xffff0000, v85
	s_waitcnt lgkmcnt(0)
	v_mul_f32_e32 v55, v55, v68
	v_mul_f32_e32 v60, v48, v60
	s_waitcnt vmcnt(7)
	v_lshlrev_b32_e32 v48, 16, v86
	v_mul_f32_e32 v53, v53, v69
	v_mul_f32_e32 v55, v55, v48
	v_and_b32_e32 v48, 0xffff0000, v86
	v_mul_f32_e32 v51, v51, v70
	v_mul_f32_e32 v53, v53, v48
	v_lshlrev_b32_e32 v48, 16, v87
	v_mul_f32_e32 v49, v49, v71
	v_mul_f32_e32 v51, v51, v48
	v_and_b32_e32 v48, 0xffff0000, v87
	v_mul_f32_e32 v61, v49, v48
	v_cvt_pk_bf16_f32 v48, v54, v52
	v_cvt_pk_bf16_f32 v49, v50, v60
	v_cvt_pk_bf16_f32 v50, v55, v53
	v_cvt_pk_bf16_f32 v51, v51, v61
	v_or_b32_e32 v52, 0x100, v58
	v_permlane32_swap_b32_e32 v48, v50
	v_permlane32_swap_b32_e32 v49, v51
	global_store_dwordx4 v52, v[48:51], s[4:5] offset:32
	global_load_dwordx2 v[60:61], v59, s[4:5] offset:384
	global_load_dwordx2 v[62:63], v59, s[4:5] offset:400
	global_load_dwordx2 v[64:65], v59, s[4:5] offset:416
	global_load_dwordx2 v[66:67], v59, s[4:5] offset:432
	ds_read_b128 v[48:51], v57 offset:640
	ds_read_b128 v[52:55], v57 offset:672
	v_mul_f32_e32 v32, v32, v56
	v_mul_f32_e32 v39, v39, v56
	v_mul_f32_e32 v37, v37, v56
	s_waitcnt lgkmcnt(1)
	v_mul_f32_e32 v46, v46, v48
	s_waitcnt vmcnt(9)
	v_lshlrev_b32_e32 v48, 16, v76
	v_mul_f32_e32 v44, v44, v49
	v_mul_f32_e32 v46, v46, v48
	v_and_b32_e32 v48, 0xffff0000, v76
	v_mul_f32_e32 v42, v42, v50
	v_mul_f32_e32 v44, v44, v48
	v_lshlrev_b32_e32 v48, 16, v77
	v_mul_f32_e32 v40, v40, v51
	v_mul_f32_e32 v42, v42, v48
	v_and_b32_e32 v48, 0xffff0000, v77
	s_waitcnt lgkmcnt(0)
	v_mul_f32_e32 v47, v47, v52
	v_mul_f32_e32 v48, v40, v48
	s_waitcnt vmcnt(8)
	v_lshlrev_b32_e32 v40, 16, v78
	v_mul_f32_e32 v45, v45, v53
	v_mul_f32_e32 v47, v47, v40
	v_and_b32_e32 v40, 0xffff0000, v78
	v_mul_f32_e32 v43, v43, v54
	v_mul_f32_e32 v45, v45, v40
	v_lshlrev_b32_e32 v40, 16, v79
	v_mul_f32_e32 v41, v41, v55
	v_mul_f32_e32 v43, v43, v40
	v_and_b32_e32 v40, 0xffff0000, v79
	v_mul_f32_e32 v49, v41, v40
	v_cvt_pk_bf16_f32 v40, v46, v44
	v_cvt_pk_bf16_f32 v41, v42, v48
	v_cvt_pk_bf16_f32 v42, v47, v45
	v_cvt_pk_bf16_f32 v43, v43, v49
	ds_read_b128 v[44:47], v57 offset:704
	ds_read_b128 v[48:51], v57 offset:736
	v_permlane32_swap_b32_e32 v40, v42
	v_permlane32_swap_b32_e32 v41, v43
	global_store_dwordx4 v58, v[40:43], s[4:5] offset:320
	s_waitcnt lgkmcnt(1)
	v_mul_f32_e32 v38, v38, v44
	v_mul_f32_e32 v36, v36, v45
	s_waitcnt vmcnt(8)
	v_lshlrev_b32_e32 v40, 16, v80
	v_mul_f32_e32 v38, v38, v40
	v_and_b32_e32 v40, 0xffff0000, v80
	v_mul_f32_e32 v34, v34, v46
	v_mul_f32_e32 v36, v36, v40
	v_lshlrev_b32_e32 v40, 16, v81
	v_mul_f32_e32 v32, v32, v47
	v_mul_f32_e32 v34, v34, v40
	v_and_b32_e32 v40, 0xffff0000, v81
	s_waitcnt lgkmcnt(0)
	v_mul_f32_e32 v39, v39, v48
	v_mul_f32_e32 v40, v32, v40
	s_waitcnt vmcnt(7)
	v_lshlrev_b32_e32 v32, 16, v82
	v_mul_f32_e32 v37, v37, v49
	v_mul_f32_e32 v35, v35, v56
	v_mul_f32_e32 v39, v39, v32
	v_and_b32_e32 v32, 0xffff0000, v82
	v_mul_f32_e32 v35, v35, v50
	v_mul_f32_e32 v33, v33, v56
	v_mul_f32_e32 v37, v37, v32
	v_lshlrev_b32_e32 v32, 16, v83
	v_mul_f32_e32 v33, v33, v51
	v_mul_f32_e32 v35, v35, v32
	v_and_b32_e32 v32, 0xffff0000, v83
	v_mul_f32_e32 v41, v33, v32
	v_cvt_pk_bf16_f32 v32, v38, v36
	v_cvt_pk_bf16_f32 v33, v34, v40
	v_cvt_pk_bf16_f32 v34, v39, v37
	v_cvt_pk_bf16_f32 v35, v35, v41
	v_or_b32_e32 v36, 0x140, v58
	v_permlane32_swap_b32_e32 v32, v34
	v_permlane32_swap_b32_e32 v33, v35
	global_store_dwordx4 v36, v[32:35], s[4:5] offset:32
	global_load_dwordx2 v[40:41], v59, s[4:5] offset:448
	global_load_dwordx2 v[42:43], v59, s[4:5] offset:464
	global_load_dwordx2 v[44:45], v59, s[4:5] offset:480
	global_load_dwordx2 v[46:47], v59, s[4:5] offset:496
	ds_read_b128 v[32:35], v57 offset:768
	ds_read_b128 v[36:39], v57 offset:800
	v_mul_f32_e32 v30, v30, v56
	v_mul_f32_e32 v28, v28, v56
	v_mul_f32_e32 v26, v26, v56
	s_waitcnt lgkmcnt(1)
	v_mul_f32_e32 v30, v30, v32
	s_waitcnt vmcnt(9)
	v_lshlrev_b32_e32 v32, 16, v60
	v_mul_f32_e32 v28, v28, v33
	v_mul_f32_e32 v30, v30, v32
	v_and_b32_e32 v32, 0xffff0000, v60
	v_mul_f32_e32 v26, v26, v34
	v_mul_f32_e32 v24, v24, v56
	v_mul_f32_e32 v28, v28, v32
	v_lshlrev_b32_e32 v32, 16, v61
	v_mul_f32_e32 v31, v31, v56
	v_mul_f32_e32 v24, v24, v35
	v_mul_f32_e32 v26, v26, v32
	v_and_b32_e32 v32, 0xffff0000, v61
	s_waitcnt lgkmcnt(0)
	v_mul_f32_e32 v31, v31, v36
	v_mul_f32_e32 v29, v29, v56
	v_mul_f32_e32 v32, v24, v32
	s_waitcnt vmcnt(8)
	v_lshlrev_b32_e32 v24, 16, v62
	v_mul_f32_e32 v29, v29, v37
	v_mul_f32_e32 v27, v27, v56
	v_mul_f32_e32 v31, v31, v24
	v_and_b32_e32 v24, 0xffff0000, v62
	v_mul_f32_e32 v27, v27, v38
	v_mul_f32_e32 v25, v25, v56
	v_mul_f32_e32 v29, v29, v24
	v_lshlrev_b32_e32 v24, 16, v63
	v_mul_f32_e32 v25, v25, v39
	v_mul_f32_e32 v27, v27, v24
	v_and_b32_e32 v24, 0xffff0000, v63
	v_mul_f32_e32 v33, v25, v24
	v_cvt_pk_bf16_f32 v24, v30, v28
	v_cvt_pk_bf16_f32 v25, v26, v32
	v_cvt_pk_bf16_f32 v26, v31, v29
	v_cvt_pk_bf16_f32 v27, v27, v33
	ds_read_b128 v[28:31], v57 offset:832
	ds_read_b128 v[32:35], v57 offset:864
	v_permlane32_swap_b32_e32 v24, v26
	v_permlane32_swap_b32_e32 v25, v27
	v_mul_f32_e32 v22, v22, v56
	global_store_dwordx4 v58, v[24:27], s[4:5] offset:384
	s_waitcnt lgkmcnt(1)
	v_mul_f32_e32 v22, v22, v28
	v_mul_f32_e32 v20, v20, v56
	s_waitcnt vmcnt(8)
	v_lshlrev_b32_e32 v24, 16, v64
	v_mul_f32_e32 v20, v20, v29
	v_mul_f32_e32 v18, v18, v56
	v_mul_f32_e32 v22, v22, v24
	v_and_b32_e32 v24, 0xffff0000, v64
	v_mul_f32_e32 v18, v18, v30
	v_mul_f32_e32 v16, v16, v56
	v_mul_f32_e32 v20, v20, v24
	v_lshlrev_b32_e32 v24, 16, v65
	v_mul_f32_e32 v23, v23, v56
	v_mul_f32_e32 v16, v16, v31
	v_mul_f32_e32 v18, v18, v24
	v_and_b32_e32 v24, 0xffff0000, v65
	s_waitcnt lgkmcnt(0)
	v_mul_f32_e32 v23, v23, v32
	v_mul_f32_e32 v21, v21, v56
	v_mul_f32_e32 v24, v16, v24
	s_waitcnt vmcnt(7)
	v_lshlrev_b32_e32 v16, 16, v66
	v_mul_f32_e32 v21, v21, v33
	v_mul_f32_e32 v19, v19, v56
	v_mul_f32_e32 v23, v23, v16
	v_and_b32_e32 v16, 0xffff0000, v66
	v_mul_f32_e32 v19, v19, v34
	v_mul_f32_e32 v17, v17, v56
	v_mul_f32_e32 v21, v21, v16
	v_lshlrev_b32_e32 v16, 16, v67
	v_mul_f32_e32 v17, v17, v35
	v_mul_f32_e32 v19, v19, v16
	v_and_b32_e32 v16, 0xffff0000, v67
	v_mul_f32_e32 v25, v17, v16
	v_cvt_pk_bf16_f32 v16, v22, v20
	v_cvt_pk_bf16_f32 v17, v18, v24
	v_cvt_pk_bf16_f32 v18, v23, v21
	v_cvt_pk_bf16_f32 v19, v19, v25
	v_or_b32_e32 v20, 0x180, v58
	v_permlane32_swap_b32_e32 v16, v18
	v_permlane32_swap_b32_e32 v17, v19
	global_store_dwordx4 v20, v[16:19], s[4:5] offset:32
	ds_read_b128 v[16:19], v57 offset:896
	ds_read_b128 v[20:23], v57 offset:928
	v_mul_f32_e32 v14, v14, v56
	v_mul_f32_e32 v12, v12, v56
	v_mul_f32_e32 v10, v10, v56
	s_waitcnt lgkmcnt(1)
	v_mul_f32_e32 v14, v14, v16
	s_waitcnt vmcnt(5)
	v_lshlrev_b32_e32 v16, 16, v40
	v_mul_f32_e32 v12, v12, v17
	v_mul_f32_e32 v14, v14, v16
	v_and_b32_e32 v16, 0xffff0000, v40
	v_mul_f32_e32 v10, v10, v18
	v_mul_f32_e32 v8, v8, v56
	v_mul_f32_e32 v12, v12, v16
	v_lshlrev_b32_e32 v16, 16, v41
	v_mul_f32_e32 v15, v15, v56
	v_mul_f32_e32 v8, v8, v19
	v_mul_f32_e32 v10, v10, v16
	v_and_b32_e32 v16, 0xffff0000, v41
	s_waitcnt lgkmcnt(0)
	v_mul_f32_e32 v15, v15, v20
	v_mul_f32_e32 v13, v13, v56
	v_mul_f32_e32 v16, v8, v16
	s_waitcnt vmcnt(4)
	v_lshlrev_b32_e32 v8, 16, v42
	v_mul_f32_e32 v13, v13, v21
	v_mul_f32_e32 v11, v11, v56
	v_mul_f32_e32 v15, v15, v8
	v_and_b32_e32 v8, 0xffff0000, v42
	v_mul_f32_e32 v11, v11, v22
	v_mul_f32_e32 v9, v9, v56
	v_mul_f32_e32 v13, v13, v8
	v_lshlrev_b32_e32 v8, 16, v43
	v_mul_f32_e32 v9, v9, v23
	v_mul_f32_e32 v11, v11, v8
	v_and_b32_e32 v8, 0xffff0000, v43
	v_mul_f32_e32 v17, v9, v8
	v_cvt_pk_bf16_f32 v8, v14, v12
	v_cvt_pk_bf16_f32 v9, v10, v16
	v_cvt_pk_bf16_f32 v10, v15, v13
	v_cvt_pk_bf16_f32 v11, v11, v17
	ds_read_b128 v[12:15], v57 offset:960
	ds_read_b128 v[16:19], v57 offset:992
	v_permlane32_swap_b32_e32 v8, v10
	v_permlane32_swap_b32_e32 v9, v11
	v_mul_f32_e32 v6, v6, v56
	global_store_dwordx4 v58, v[8:11], s[4:5] offset:448
	s_waitcnt lgkmcnt(1)
	v_mul_f32_e32 v6, v6, v12
	v_mul_f32_e32 v4, v4, v56
	s_waitcnt vmcnt(4)
	v_lshlrev_b32_e32 v8, 16, v44
	v_mul_f32_e32 v4, v4, v13
	v_mul_f32_e32 v2, v2, v56
	v_mul_f32_e32 v6, v6, v8
	v_and_b32_e32 v8, 0xffff0000, v44
	v_mul_f32_e32 v2, v2, v14
	v_mul_f32_e32 v0, v0, v56
	v_mul_f32_e32 v4, v4, v8
	v_lshlrev_b32_e32 v8, 16, v45
	v_mul_f32_e32 v7, v7, v56
	v_mul_f32_e32 v0, v0, v15
	v_mul_f32_e32 v2, v2, v8
	v_and_b32_e32 v8, 0xffff0000, v45
	s_waitcnt lgkmcnt(0)
	v_mul_f32_e32 v7, v7, v16
	v_mul_f32_e32 v5, v5, v56
	v_mul_f32_e32 v8, v0, v8
	s_waitcnt vmcnt(3)
	v_lshlrev_b32_e32 v0, 16, v46
	v_mul_f32_e32 v5, v5, v17
	v_mul_f32_e32 v3, v3, v56
	v_mul_f32_e32 v7, v7, v0
	v_and_b32_e32 v0, 0xffff0000, v46
	v_mul_f32_e32 v3, v3, v18
	v_mul_f32_e32 v1, v1, v56
	v_mul_f32_e32 v5, v5, v0
	v_lshlrev_b32_e32 v0, 16, v47
	v_mul_f32_e32 v1, v1, v19
	v_mul_f32_e32 v3, v3, v0
	v_and_b32_e32 v0, 0xffff0000, v47
	v_mul_f32_e32 v9, v1, v0
	v_cvt_pk_bf16_f32 v0, v6, v4
	v_cvt_pk_bf16_f32 v1, v2, v8
	v_cvt_pk_bf16_f32 v2, v7, v5
	v_cvt_pk_bf16_f32 v3, v3, v9
	v_readlane_b32 s2, v255, 38
	v_permlane32_swap_b32_e32 v0, v2
	v_permlane32_swap_b32_e32 v1, v3
	v_or_b32_e32 v4, 0x1c0, v58
	s_cmp_lg_u32 s10, s2
	s_mov_b32 s2, s10
	global_store_dwordx4 v4, v[0:3], s[4:5] offset:32
	s_cbranch_scc0 .LBB0_541

.Lstg_b6:
	s_add_i32 s6, s88, -1
	s_cmp_ge_u32 s6, s89
	s_cselect_b64 s[82:83], -1, 0
	s_mov_b64 s[4:5], -1
	s_and_b64 vcc, exec, s[82:83]
	s_cbranch_vccz .LBB0_524
	v_mov_b64_e32 v[144:145], s[0:1]
	flat_load_dword v146, v[144:145] sc0 sc1
	s_waitcnt vmcnt(0)
	v_mov_b64_e32 v[144:145], s[74:75]
	flat_load_dword v144, v[144:145] sc0 sc1
	s_waitcnt vmcnt(0) lgkmcnt(0)
	v_readfirstlane_b32 s4, v146
	v_readfirstlane_b32 s5, v144
	s_nop 1
	s_nop 3
	s_mov_b32 m0, s2
	s_nop 0
	global_load_lds_dwordx4 v170, s[4:5]
	s_nop 3
	s_mov_b32 m0, s91
	s_nop 0
	global_load_lds_dwordx4 v172, s[4:5]
	s_mov_b64 s[4:5], 0
.LBB0_524:
	s_andn2_b64 vcc, exec, s[4:5]
	s_cbranch_vccnz .LBB0_526
	s_add_u32 s4, s72, s66
	s_addc_u32 s5, s73, s67
	s_add_u32 s4, s4, 0x11a60400
	s_addc_u32 s5, s5, 0
	s_mov_b32 m0, s96
	s_nop 0
	global_load_lds_dwordx4 v170, s[4:5]
	s_mov_b32 m0, s97
	s_nop 0
	global_load_lds_dwordx4 v172, s[4:5]
.LBB0_526:
	s_add_u32 s33, s72, s84
	s_addc_u32 s92, s73, s90
	s_add_u32 s4, s33, 0x2dd40800
	s_addc_u32 s5, s92, 0
	s_mov_b32 m0, s81
	s_nop 0
	global_load_lds_dwordx4 v162, s[4:5]
	s_add_i32 m0, s78, 0xffffff80
	s_nop 0
	global_load_lds_dwordx4 v162, s[4:5] offset:128
	s_add_i32 m0, s69, 0xffffff00
	s_nop 0
	global_load_lds_dwordx4 v162, s[4:5] offset:256
	s_add_i32 m0, s68, 0xfffffe80
	s_nop 0
	global_load_lds_dwordx4 v162, s[4:5] offset:384
	ds_read_b64_tr_b16 v[144:145], v177 offset:0x8000
	ds_read_b64_tr_b16 v[146:147], v177 offset:0x9000
	ds_read_b64_tr_b16 v[148:149], v177 offset:0xa000
	ds_read_b64_tr_b16 v[150:151], v177 offset:0xb000
	ds_read_b64_tr_b16 v[152:153], v177 offset:0xc000
	ds_read_b64_tr_b16 v[154:155], v177 offset:0xd000
	ds_read_b64_tr_b16 v[156:157], v177 offset:0xe000
	ds_read_b64_tr_b16 v[158:159], v177 offset:0xf000
	ds_read_b64_tr_b16 v[236:237], v177 offset:0x8200
	ds_read_b64_tr_b16 v[238:239], v177 offset:0x9200
	ds_read_b64_tr_b16 v[240:241], v177 offset:0xa200
	ds_read_b64_tr_b16 v[242:243], v177 offset:0xb200
	ds_read_b64_tr_b16 v[244:245], v177 offset:0xc200
	ds_read_b64_tr_b16 v[246:247], v177 offset:0xd200
	ds_read_b64_tr_b16 v[248:249], v177 offset:0xe200
	ds_read_b64_tr_b16 v[250:251], v177 offset:0xf200
	s_waitcnt lgkmcnt(8)
	s_nop 1
	v_mfma_f32_32x32x16_bf16 v[112:127], v[144:147], v[128:131], v[112:127]
	v_mfma_f32_32x32x16_bf16 v[112:127], v[148:151], v[132:135], v[112:127]
	v_mfma_f32_32x32x16_bf16 v[112:127], v[152:155], v[136:139], v[112:127]
	v_mfma_f32_32x32x16_bf16 v[112:127], v[156:159], v[140:143], v[112:127]
	ds_read_b64_tr_b16 v[144:145], v177 offset:0x8400
	ds_read_b64_tr_b16 v[146:147], v177 offset:0x9400
	ds_read_b64_tr_b16 v[148:149], v177 offset:0xa400
	ds_read_b64_tr_b16 v[150:151], v177 offset:0xb400
	ds_read_b64_tr_b16 v[152:153], v177 offset:0xc400
	ds_read_b64_tr_b16 v[154:155], v177 offset:0xd400
	ds_read_b64_tr_b16 v[156:157], v177 offset:0xe400
	ds_read_b64_tr_b16 v[158:159], v177 offset:0xf400
	s_waitcnt lgkmcnt(8)
	v_mfma_f32_32x32x16_bf16 v[0:15], v[236:239], v[128:131], v[0:15]
	v_mfma_f32_32x32x16_bf16 v[0:15], v[240:243], v[132:135], v[0:15]
	v_mfma_f32_32x32x16_bf16 v[0:15], v[244:247], v[136:139], v[0:15]
	v_mfma_f32_32x32x16_bf16 v[0:15], v[248:251], v[140:143], v[0:15]
	ds_read_b64_tr_b16 v[236:237], v177 offset:0x8600
	ds_read_b64_tr_b16 v[238:239], v177 offset:0x9600
	ds_read_b64_tr_b16 v[240:241], v177 offset:0xa600
	ds_read_b64_tr_b16 v[242:243], v177 offset:0xb600
	ds_read_b64_tr_b16 v[244:245], v177 offset:0xc600
	ds_read_b64_tr_b16 v[246:247], v177 offset:0xd600
	ds_read_b64_tr_b16 v[248:249], v177 offset:0xe600
	ds_read_b64_tr_b16 v[250:251], v177 offset:0xf600
	s_waitcnt lgkmcnt(8)
	v_mfma_f32_32x32x16_bf16 v[16:31], v[144:147], v[128:131], v[16:31]
	v_mfma_f32_32x32x16_bf16 v[16:31], v[148:151], v[132:135], v[16:31]
	v_mfma_f32_32x32x16_bf16 v[16:31], v[152:155], v[136:139], v[16:31]
	v_mfma_f32_32x32x16_bf16 v[16:31], v[156:159], v[140:143], v[16:31]
	ds_read_b64_tr_b16 v[144:145], v177 offset:0x8800
	ds_read_b64_tr_b16 v[146:147], v177 offset:0x9800
	ds_read_b64_tr_b16 v[148:149], v177 offset:0xa800
	ds_read_b64_tr_b16 v[150:151], v177 offset:0xb800
	ds_read_b64_tr_b16 v[152:153], v177 offset:0xc800
	ds_read_b64_tr_b16 v[154:155], v177 offset:0xd800
	ds_read_b64_tr_b16 v[156:157], v177 offset:0xe800
	ds_read_b64_tr_b16 v[158:159], v177 offset:0xf800
	s_waitcnt lgkmcnt(8)
	v_mfma_f32_32x32x16_bf16 v[32:47], v[236:239], v[128:131], v[32:47]
	v_mfma_f32_32x32x16_bf16 v[32:47], v[240:243], v[132:135], v[32:47]
	v_mfma_f32_32x32x16_bf16 v[32:47], v[244:247], v[136:139], v[32:47]
	v_mfma_f32_32x32x16_bf16 v[32:47], v[248:251], v[140:143], v[32:47]
	ds_read_b64_tr_b16 v[236:237], v177 offset:0x8a00
	ds_read_b64_tr_b16 v[238:239], v177 offset:0x9a00
	ds_read_b64_tr_b16 v[240:241], v177 offset:0xaa00
	ds_read_b64_tr_b16 v[242:243], v177 offset:0xba00
	ds_read_b64_tr_b16 v[244:245], v177 offset:0xca00
	ds_read_b64_tr_b16 v[246:247], v177 offset:0xda00
	ds_read_b64_tr_b16 v[248:249], v177 offset:0xea00
	ds_read_b64_tr_b16 v[250:251], v177 offset:0xfa00
	s_waitcnt lgkmcnt(8)
	v_mfma_f32_32x32x16_bf16 v[48:63], v[144:147], v[128:131], v[48:63]
	v_mfma_f32_32x32x16_bf16 v[48:63], v[148:151], v[132:135], v[48:63]
	v_mfma_f32_32x32x16_bf16 v[48:63], v[152:155], v[136:139], v[48:63]
	v_mfma_f32_32x32x16_bf16 v[48:63], v[156:159], v[140:143], v[48:63]
	ds_read_b64_tr_b16 v[144:145], v177 offset:0x8c00
	ds_read_b64_tr_b16 v[146:147], v177 offset:0x9c00
	ds_read_b64_tr_b16 v[148:149], v177 offset:0xac00
	ds_read_b64_tr_b16 v[150:151], v177 offset:0xbc00
	ds_read_b64_tr_b16 v[152:153], v177 offset:0xcc00
	ds_read_b64_tr_b16 v[154:155], v177 offset:0xdc00
	ds_read_b64_tr_b16 v[156:157], v177 offset:0xec00
	ds_read_b64_tr_b16 v[158:159], v177 offset:0xfc00
	s_waitcnt lgkmcnt(8)
	v_mfma_f32_32x32x16_bf16 v[64:79], v[236:239], v[128:131], v[64:79]
	v_mfma_f32_32x32x16_bf16 v[64:79], v[240:243], v[132:135], v[64:79]
	v_mfma_f32_32x32x16_bf16 v[64:79], v[244:247], v[136:139], v[64:79]
	v_mfma_f32_32x32x16_bf16 v[64:79], v[248:251], v[140:143], v[64:79]
	ds_read_b64_tr_b16 v[236:237], v177 offset:0x8e00
	ds_read_b64_tr_b16 v[238:239], v177 offset:0x9e00
	ds_read_b64_tr_b16 v[240:241], v177 offset:0xae00
	ds_read_b64_tr_b16 v[242:243], v177 offset:0xbe00
	ds_read_b64_tr_b16 v[244:245], v177 offset:0xce00
	ds_read_b64_tr_b16 v[246:247], v177 offset:0xde00
	ds_read_b64_tr_b16 v[248:249], v177 offset:0xee00
	ds_read_b64_tr_b16 v[250:251], v177 offset:0xfe00
	s_waitcnt lgkmcnt(8)
	v_mfma_f32_32x32x16_bf16 v[80:95], v[144:147], v[128:131], v[80:95]
	v_mfma_f32_32x32x16_bf16 v[80:95], v[148:151], v[132:135], v[80:95]
	v_mfma_f32_32x32x16_bf16 v[80:95], v[152:155], v[136:139], v[80:95]
	v_mfma_f32_32x32x16_bf16 v[80:95], v[156:159], v[140:143], v[80:95]
	s_waitcnt lgkmcnt(0)
	v_mfma_f32_32x32x16_bf16 v[96:111], v[236:239], v[128:131], v[96:111]
	v_mfma_f32_32x32x16_bf16 v[96:111], v[240:243], v[132:135], v[96:111]
	v_mfma_f32_32x32x16_bf16 v[96:111], v[244:247], v[136:139], v[96:111]
	v_mfma_f32_32x32x16_bf16 v[96:111], v[248:251], v[140:143], v[96:111]
	ds_read_b128 v[128:131], v182 offset:0
	ds_read_b128 v[132:135], v182 offset:0x2000
	ds_read_b128 v[136:139], v181 offset:0
	ds_read_b128 v[236:239], v183 offset:0
	ds_read_b128 v[240:243], v183 offset:0x2000
	ds_read_b128 v[244:247], v181 offset:0x400
	s_waitcnt lgkmcnt(3)
	s_nop 0
	v_mfma_f32_32x32x16_bf16 v[144:159], v[128:131], v[136:139], 0
	v_mfma_f32_32x32x16_bf16 v[128:143], v[132:135], v[136:139], 0
	ds_read_b128 v[248:251], v184 offset:0
	ds_read_b128 v[194:197], v184 offset:0x2000
	ds_read_b128 v[222:225], v181 offset:0x800
	s_waitcnt lgkmcnt(3)
	v_mfma_f32_32x32x16_bf16 v[144:159], v[236:239], v[244:247], v[144:159]
	v_mfma_f32_32x32x16_bf16 v[128:143], v[240:243], v[244:247], v[128:143]
	ds_read_b128 v[236:239], v185 offset:0
	ds_read_b128 v[240:243], v185 offset:0x2000
	ds_read_b128 v[244:247], v181 offset:0xc00
	s_waitcnt lgkmcnt(3)
	v_mfma_f32_32x32x16_bf16 v[144:159], v[248:251], v[222:225], v[144:159]
	v_mfma_f32_32x32x16_bf16 v[128:143], v[194:197], v[222:225], v[128:143]
	ds_read_b128 v[194:197], v182 offset:0x80
	ds_read_b128 v[222:225], v182 offset:0x2080
	ds_read_b128 v[248:251], v181 offset:0x1000
	s_waitcnt lgkmcnt(3)
	v_mfma_f32_32x32x16_bf16 v[144:159], v[236:239], v[244:247], v[144:159]
	v_mfma_f32_32x32x16_bf16 v[128:143], v[240:243], v[244:247], v[128:143]
	ds_read_b128 v[236:239], v183 offset:0x80
	ds_read_b128 v[240:243], v183 offset:0x2080
	ds_read_b128 v[244:247], v181 offset:0x1400
	s_waitcnt lgkmcnt(3)
	v_mfma_f32_32x32x16_bf16 v[144:159], v[194:197], v[248:251], v[144:159]
	v_mfma_f32_32x32x16_bf16 v[128:143], v[222:225], v[248:251], v[128:143]
	ds_read_b128 v[194:197], v184 offset:0x80
	ds_read_b128 v[222:225], v184 offset:0x2080
	ds_read_b128 v[248:251], v181 offset:0x1800
	s_waitcnt lgkmcnt(3)
	v_mfma_f32_32x32x16_bf16 v[144:159], v[236:239], v[244:247], v[144:159]
	v_mfma_f32_32x32x16_bf16 v[128:143], v[240:243], v[244:247], v[128:143]
	ds_read_b128 v[236:239], v185 offset:0x80
	ds_read_b128 v[240:243], v185 offset:0x2080
	s_waitcnt lgkmcnt(2)
	v_mfma_f32_32x32x16_bf16 v[144:159], v[194:197], v[248:251], v[144:159]
	v_mfma_f32_32x32x16_bf16 v[128:143], v[222:225], v[248:251], v[128:143]
	s_waitcnt lgkmcnt(0)
	v_mfma_f32_32x32x16_bf16 v[144:159], v[236:239], v[166:169], v[144:159]
	v_mfma_f32_32x32x16_bf16 v[128:143], v[240:243], v[166:169], v[128:143]
	s_bitcmp0_b32 s100, 8
	s_cbranch_scc1 .Lstg_a3
	s_waitcnt vmcnt(0)
	s_waitcnt lgkmcnt(0)
	s_barrier

.Lstg_b7:
	s_cmp_gt_u32 s88, s89
	s_cbranch_scc1 .LBB0_533
	s_cmp_ge_u32 s88, s89
	s_mov_b64 s[4:5], -1
	s_cbranch_scc0 .LBB0_531
	v_mov_b64_e32 v[194:195], s[0:1]
	flat_load_dword v196, v[194:195] sc0 sc1
	s_waitcnt vmcnt(0)
	v_mov_b64_e32 v[194:195], s[74:75]
	flat_load_dword v194, v[194:195] sc0 sc1
	s_waitcnt vmcnt(0) lgkmcnt(0)
	v_readfirstlane_b32 s4, v196
	v_readfirstlane_b32 s5, v194
	s_nop 1
	s_nop 3
	s_mov_b32 m0, s2
	s_nop 0
	global_load_lds_dwordx4 v170, s[4:5]
	s_nop 3
	s_mov_b32 m0, s91
	s_nop 0
	global_load_lds_dwordx4 v172, s[4:5]
	s_mov_b64 s[4:5], 0
.LBB0_531:
	s_andn2_b64 vcc, exec, s[4:5]
	s_cbranch_vccnz .LBB0_533
	s_add_u32 s4, s72, s66
	s_addc_u32 s5, s73, s67
	s_add_u32 s4, s4, 0x11a80400
	s_addc_u32 s5, s5, 0
	s_mov_b32 m0, s2
	s_nop 0
	global_load_lds_dwordx4 v170, s[4:5]
	s_mov_b32 m0, s91
	s_nop 0
	global_load_lds_dwordx4 v172, s[4:5]
.LBB0_533:
	s_mov_b64 s[4:5], -1
	s_and_b64 vcc, exec, s[82:83]
	s_cbranch_vccz .LBB0_535
	v_mov_b64_e32 v[194:195], s[70:71]
	flat_load_dword v196, v[194:195] sc0 sc1
	s_waitcnt vmcnt(0)
	v_mov_b64_e32 v[194:195], s[76:77]
	flat_load_dword v194, v[194:195] sc0 sc1
	s_waitcnt vmcnt(0) lgkmcnt(0)
	v_readfirstlane_b32 s4, v196
	v_readfirstlane_b32 s5, v194
	s_nop 1
	s_nop 3
	s_mov_b32 m0, s81
	s_nop 0
	global_load_lds_dwordx4 v162, s[4:5]
	s_nop 3
	s_add_i32 m0, s78, 0xffffff80
	s_nop 0
	global_load_lds_dwordx4 v162, s[4:5] offset:128
	s_add_i32 m0, s69, 0xffffff00
	s_nop 0
	global_load_lds_dwordx4 v162, s[4:5] offset:256
	s_add_i32 m0, s68, 0xfffffe80
	s_nop 0
	global_load_lds_dwordx4 v162, s[4:5] offset:384
	s_mov_b64 s[4:5], 0
.LBB0_535:
	s_andn2_b64 vcc, exec, s[4:5]
	s_cbranch_vccnz .LBB0_537
	s_add_u32 s4, s33, 0x2dee0800
	s_addc_u32 s5, s92, 0
	s_mov_b32 m0, s3
	s_nop 0
	global_load_lds_dwordx4 v162, s[4:5]
	s_add_i32 m0, s95, 0xffffff80
	s_nop 0
	global_load_lds_dwordx4 v162, s[4:5] offset:128
	s_add_i32 m0, s93, 0xffffff00
	s_nop 0
	global_load_lds_dwordx4 v162, s[4:5] offset:256
	s_add_i32 m0, s79, 0xfffffe80
	s_nop 0
	global_load_lds_dwordx4 v162, s[4:5] offset:384

.Lstg_b14:
	s_add_i32 s8, s3, -1
	s_cmp_ge_u32 s8, s75
	s_cselect_b64 s[96:97], -1, 0
	s_mov_b64 s[6:7], -1
	s_and_b64 vcc, exec, s[96:97]
	s_cbranch_vccz .LBB0_561
	v_mov_b64_e32 v[144:145], s[80:81]
	flat_load_dword v146, v[144:145] sc0 sc1
	s_waitcnt vmcnt(0)
	v_mov_b64_e32 v[144:145], s[72:73]
	flat_load_dword v144, v[144:145] sc0 sc1
	s_waitcnt vmcnt(0) lgkmcnt(0)
	v_readfirstlane_b32 s6, v146
	v_readfirstlane_b32 s7, v144
	s_nop 1
	s_nop 3
	s_mov_b32 m0, s83
	s_nop 0
	global_load_lds_dwordx4 v160, s[6:7]
	s_nop 3
	s_mov_b32 m0, s78
	s_nop 0
	global_load_lds_dwordx4 v170, s[6:7]
	s_mov_b64 s[6:7], 0
.LBB0_561:
	s_andn2_b64 vcc, exec, s[6:7]
	s_cbranch_vccnz .LBB0_563
	s_add_u32 s6, s66, 0x19f000
	s_addc_u32 s7, s67, 0
	s_mov_b32 m0, s84
	s_nop 0
	global_load_lds_dwordx4 v160, s[6:7]
	s_mov_b32 m0, s85
	s_nop 0
	global_load_lds_dwordx4 v170, s[6:7]
.LBB0_563:
	v_sub_f32_e32 v144, v190, v172
	v_mul_f32_e32 v144, 0x3e0293ee, v144
	v_exp_f32_e32 v144, v144
	s_nop 0
	v_cndmask_b32_e64 v172, v144, 1.0, s[4:5]
	s_mov_b32 m0, s93
	s_nop 0
	global_load_lds_dwordx4 v162, s[66:67]
	s_add_i32 m0, s2, 0xffffff80
	s_nop 0
	global_load_lds_dwordx4 v162, s[66:67] offset:128
	s_add_i32 m0, s69, 0xffffff00
	s_nop 0
	global_load_lds_dwordx4 v162, s[66:67] offset:256
	s_add_i32 m0, s68, 0xfffffe80
	s_nop 0
	global_load_lds_dwordx4 v162, s[66:67] offset:384
	v_cmp_gt_f32_e32 vcc, 1.0, v172
	s_cbranch_vccz .LBB0_565
	v_pk_mul_f32 v[126:127], v[126:127], v[172:173] op_sel_hi:[1,0]
	v_pk_mul_f32 v[124:125], v[124:125], v[172:173] op_sel_hi:[1,0]
	v_pk_mul_f32 v[122:123], v[122:123], v[172:173] op_sel_hi:[1,0]
	v_pk_mul_f32 v[120:121], v[120:121], v[172:173] op_sel_hi:[1,0]
	v_pk_mul_f32 v[118:119], v[118:119], v[172:173] op_sel_hi:[1,0]
	v_pk_mul_f32 v[116:117], v[116:117], v[172:173] op_sel_hi:[1,0]
	v_pk_mul_f32 v[114:115], v[114:115], v[172:173] op_sel_hi:[1,0]
	v_pk_mul_f32 v[112:113], v[112:113], v[172:173] op_sel_hi:[1,0]
	v_pk_mul_f32 v[94:95], v[94:95], v[172:173] op_sel_hi:[1,0]
	v_pk_mul_f32 v[92:93], v[92:93], v[172:173] op_sel_hi:[1,0]
	v_pk_mul_f32 v[90:91], v[90:91], v[172:173] op_sel_hi:[1,0]
	v_pk_mul_f32 v[88:89], v[88:89], v[172:173] op_sel_hi:[1,0]
	v_pk_mul_f32 v[86:87], v[86:87], v[172:173] op_sel_hi:[1,0]
	v_pk_mul_f32 v[84:85], v[84:85], v[172:173] op_sel_hi:[1,0]
	v_pk_mul_f32 v[82:83], v[82:83], v[172:173] op_sel_hi:[1,0]
	v_pk_mul_f32 v[80:81], v[80:81], v[172:173] op_sel_hi:[1,0]
	v_pk_mul_f32 v[110:111], v[110:111], v[172:173] op_sel_hi:[1,0]
	v_pk_mul_f32 v[108:109], v[108:109], v[172:173] op_sel_hi:[1,0]
	v_pk_mul_f32 v[106:107], v[106:107], v[172:173] op_sel_hi:[1,0]
	v_pk_mul_f32 v[104:105], v[104:105], v[172:173] op_sel_hi:[1,0]
	v_pk_mul_f32 v[102:103], v[102:103], v[172:173] op_sel_hi:[1,0]
	v_pk_mul_f32 v[100:101], v[100:101], v[172:173] op_sel_hi:[1,0]
	v_pk_mul_f32 v[98:99], v[98:99], v[172:173] op_sel_hi:[1,0]
	v_pk_mul_f32 v[96:97], v[96:97], v[172:173] op_sel_hi:[1,0]
	v_pk_mul_f32 v[78:79], v[78:79], v[172:173] op_sel_hi:[1,0]
	v_pk_mul_f32 v[76:77], v[76:77], v[172:173] op_sel_hi:[1,0]
	v_pk_mul_f32 v[74:75], v[74:75], v[172:173] op_sel_hi:[1,0]
	v_pk_mul_f32 v[72:73], v[72:73], v[172:173] op_sel_hi:[1,0]
	v_pk_mul_f32 v[70:71], v[70:71], v[172:173] op_sel_hi:[1,0]
	v_pk_mul_f32 v[68:69], v[68:69], v[172:173] op_sel_hi:[1,0]
	v_pk_mul_f32 v[66:67], v[66:67], v[172:173] op_sel_hi:[1,0]
	v_pk_mul_f32 v[64:65], v[64:65], v[172:173] op_sel_hi:[1,0]
	v_pk_mul_f32 v[62:63], v[62:63], v[172:173] op_sel_hi:[1,0]
	v_pk_mul_f32 v[60:61], v[60:61], v[172:173] op_sel_hi:[1,0]
	v_pk_mul_f32 v[58:59], v[58:59], v[172:173] op_sel_hi:[1,0]
	v_pk_mul_f32 v[56:57], v[56:57], v[172:173] op_sel_hi:[1,0]
	v_pk_mul_f32 v[54:55], v[54:55], v[172:173] op_sel_hi:[1,0]
	v_pk_mul_f32 v[52:53], v[52:53], v[172:173] op_sel_hi:[1,0]
	v_pk_mul_f32 v[50:51], v[50:51], v[172:173] op_sel_hi:[1,0]
	v_pk_mul_f32 v[48:49], v[48:49], v[172:173] op_sel_hi:[1,0]
	v_pk_mul_f32 v[46:47], v[46:47], v[172:173] op_sel_hi:[1,0]
	v_pk_mul_f32 v[44:45], v[44:45], v[172:173] op_sel_hi:[1,0]
	v_pk_mul_f32 v[42:43], v[42:43], v[172:173] op_sel_hi:[1,0]
	v_pk_mul_f32 v[40:41], v[40:41], v[172:173] op_sel_hi:[1,0]
	v_pk_mul_f32 v[38:39], v[38:39], v[172:173] op_sel_hi:[1,0]
	v_pk_mul_f32 v[36:37], v[36:37], v[172:173] op_sel_hi:[1,0]
	v_pk_mul_f32 v[34:35], v[34:35], v[172:173] op_sel_hi:[1,0]
	v_pk_mul_f32 v[32:33], v[32:33], v[172:173] op_sel_hi:[1,0]
	v_pk_mul_f32 v[30:31], v[30:31], v[172:173] op_sel_hi:[1,0]
	v_pk_mul_f32 v[28:29], v[28:29], v[172:173] op_sel_hi:[1,0]
	v_pk_mul_f32 v[26:27], v[26:27], v[172:173] op_sel_hi:[1,0]
	v_pk_mul_f32 v[24:25], v[24:25], v[172:173] op_sel_hi:[1,0]
	v_pk_mul_f32 v[22:23], v[22:23], v[172:173] op_sel_hi:[1,0]
	v_pk_mul_f32 v[20:21], v[20:21], v[172:173] op_sel_hi:[1,0]
	v_pk_mul_f32 v[18:19], v[18:19], v[172:173] op_sel_hi:[1,0]
	v_pk_mul_f32 v[16:17], v[16:17], v[172:173] op_sel_hi:[1,0]
	v_pk_mul_f32 v[14:15], v[14:15], v[172:173] op_sel_hi:[1,0]
	v_pk_mul_f32 v[12:13], v[12:13], v[172:173] op_sel_hi:[1,0]
	v_pk_mul_f32 v[10:11], v[10:11], v[172:173] op_sel_hi:[1,0]
	v_pk_mul_f32 v[8:9], v[8:9], v[172:173] op_sel_hi:[1,0]
	v_pk_mul_f32 v[6:7], v[6:7], v[172:173] op_sel_hi:[1,0]
	v_pk_mul_f32 v[4:5], v[4:5], v[172:173] op_sel_hi:[1,0]
	v_pk_mul_f32 v[2:3], v[2:3], v[172:173] op_sel_hi:[1,0]
	v_pk_mul_f32 v[0:1], v[0:1], v[172:173] op_sel_hi:[1,0]

.Lstg_b15:
	s_cmp_gt_u32 s3, s75
	s_cbranch_scc1 .LBB0_572
	s_cmp_ge_u32 s3, s75
	s_mov_b64 s[6:7], -1
	s_cbranch_scc0 .LBB0_570
	v_mov_b64_e32 v[148:149], s[80:81]
	flat_load_dword v144, v[148:149] sc0 sc1
	s_waitcnt vmcnt(0)
	v_mov_b64_e32 v[148:149], s[72:73]
	flat_load_dword v147, v[148:149] sc0 sc1
	s_waitcnt vmcnt(0) lgkmcnt(0)
	v_readfirstlane_b32 s6, v144
	v_readfirstlane_b32 s7, v147
	s_nop 1
	s_nop 3
	s_mov_b32 m0, s83
	s_nop 0
	global_load_lds_dwordx4 v160, s[6:7]
	s_nop 3
	s_mov_b32 m0, s78
	s_nop 0
	global_load_lds_dwordx4 v170, s[6:7]
	s_mov_b64 s[6:7], 0
.LBB0_570:
	s_andn2_b64 vcc, exec, s[6:7]
	s_cbranch_vccnz .LBB0_572
	s_add_u32 s6, s66, 0x33f000
	s_addc_u32 s7, s67, 0
	s_mov_b32 m0, s83
	s_nop 0
	global_load_lds_dwordx4 v160, s[6:7]
	s_mov_b32 m0, s78
	s_nop 0
	global_load_lds_dwordx4 v170, s[6:7]
.LBB0_572:
	s_mov_b64 s[6:7], -1
	s_and_b64 vcc, exec, s[96:97]
	s_cbranch_vccz .LBB0_574
	v_mov_b64_e32 v[148:149], s[0:1]
	flat_load_dword v144, v[148:149] sc0 sc1
	s_waitcnt vmcnt(0)
	v_mov_b64_e32 v[148:149], s[70:71]
	flat_load_dword v147, v[148:149] sc0 sc1
	s_waitcnt vmcnt(0) lgkmcnt(0)
	v_readfirstlane_b32 s6, v144
	v_readfirstlane_b32 s7, v147
	s_nop 1
	s_nop 3
	s_mov_b32 m0, s93
	s_nop 0
	global_load_lds_dwordx4 v162, s[6:7]
	s_nop 3
	s_add_i32 m0, s2, 0xffffff80
	s_nop 0
	global_load_lds_dwordx4 v162, s[6:7] offset:128
	s_add_i32 m0, s69, 0xffffff00
	s_nop 0
	global_load_lds_dwordx4 v162, s[6:7] offset:256
	s_add_i32 m0, s68, 0xfffffe80
	s_nop 0
	global_load_lds_dwordx4 v162, s[6:7] offset:384
	s_mov_b64 s[6:7], 0
.LBB0_574:
	s_andn2_b64 vcc, exec, s[6:7]
	s_cbranch_vccnz .LBB0_576
	s_add_u32 s6, s66, 0x1a0000
	s_addc_u32 s7, s67, 0
	s_mov_b32 m0, s90
	s_nop 0
	global_load_lds_dwordx4 v162, s[6:7]
	s_add_i32 m0, s91, 0xffffff80
	s_nop 0
	global_load_lds_dwordx4 v162, s[6:7] offset:128
	s_add_i32 m0, s88, 0xffffff00
	s_nop 0
	global_load_lds_dwordx4 v162, s[6:7] offset:256
	s_add_i32 m0, s89, 0xfffffe80
	s_nop 0
	global_load_lds_dwordx4 v162, s[6:7] offset:384

.Lstg_b16:
	v_mov_b64_e32 v[146:147], s[0:1]
	flat_load_dword v148, v[146:147] sc0 sc1
	s_waitcnt vmcnt(0)
	v_mov_b64_e32 v[146:147], s[70:71]
	flat_load_dword v146, v[146:147] sc0 sc1
	s_waitcnt vmcnt(0) lgkmcnt(0)
	v_readfirstlane_b32 s4, v148
	v_readfirstlane_b32 s5, v146
	s_nop 1
	s_nop 3
	s_mov_b32 m0, s93
	s_nop 0
	global_load_lds_dwordx4 v162, s[4:5]
	s_nop 3
	s_add_i32 m0, s2, 0xffffff80
	s_nop 0
	global_load_lds_dwordx4 v162, s[4:5] offset:128
	s_add_i32 m0, s69, 0xffffff00
	s_nop 0
	global_load_lds_dwordx4 v162, s[4:5] offset:256
	s_add_i32 m0, s68, 0xfffffe80
	s_nop 0
	global_load_lds_dwordx4 v162, s[4:5] offset:384
	v_cmp_gt_f32_e32 vcc, 1.0, v160
	s_cbranch_vccz .LBB0_584
	v_pk_mul_f32 v[126:127], v[126:127], v[160:161] op_sel_hi:[1,0]
	v_pk_mul_f32 v[124:125], v[124:125], v[160:161] op_sel_hi:[1,0]
	v_pk_mul_f32 v[122:123], v[122:123], v[160:161] op_sel_hi:[1,0]
	v_pk_mul_f32 v[120:121], v[120:121], v[160:161] op_sel_hi:[1,0]
	v_pk_mul_f32 v[118:119], v[118:119], v[160:161] op_sel_hi:[1,0]
	v_pk_mul_f32 v[116:117], v[116:117], v[160:161] op_sel_hi:[1,0]
	v_pk_mul_f32 v[114:115], v[114:115], v[160:161] op_sel_hi:[1,0]
	v_pk_mul_f32 v[112:113], v[112:113], v[160:161] op_sel_hi:[1,0]
	v_pk_mul_f32 v[94:95], v[94:95], v[160:161] op_sel_hi:[1,0]
	v_pk_mul_f32 v[92:93], v[92:93], v[160:161] op_sel_hi:[1,0]
	v_pk_mul_f32 v[90:91], v[90:91], v[160:161] op_sel_hi:[1,0]
	v_pk_mul_f32 v[88:89], v[88:89], v[160:161] op_sel_hi:[1,0]
	v_pk_mul_f32 v[86:87], v[86:87], v[160:161] op_sel_hi:[1,0]
	v_pk_mul_f32 v[84:85], v[84:85], v[160:161] op_sel_hi:[1,0]
	v_pk_mul_f32 v[82:83], v[82:83], v[160:161] op_sel_hi:[1,0]
	v_pk_mul_f32 v[80:81], v[80:81], v[160:161] op_sel_hi:[1,0]
	v_pk_mul_f32 v[110:111], v[110:111], v[160:161] op_sel_hi:[1,0]
	v_pk_mul_f32 v[108:109], v[108:109], v[160:161] op_sel_hi:[1,0]
	v_pk_mul_f32 v[106:107], v[106:107], v[160:161] op_sel_hi:[1,0]
	v_pk_mul_f32 v[104:105], v[104:105], v[160:161] op_sel_hi:[1,0]
	v_pk_mul_f32 v[102:103], v[102:103], v[160:161] op_sel_hi:[1,0]
	v_pk_mul_f32 v[100:101], v[100:101], v[160:161] op_sel_hi:[1,0]
	v_pk_mul_f32 v[98:99], v[98:99], v[160:161] op_sel_hi:[1,0]
	v_pk_mul_f32 v[96:97], v[96:97], v[160:161] op_sel_hi:[1,0]
	v_pk_mul_f32 v[78:79], v[78:79], v[160:161] op_sel_hi:[1,0]
	v_pk_mul_f32 v[76:77], v[76:77], v[160:161] op_sel_hi:[1,0]
	v_pk_mul_f32 v[74:75], v[74:75], v[160:161] op_sel_hi:[1,0]
	v_pk_mul_f32 v[72:73], v[72:73], v[160:161] op_sel_hi:[1,0]
	v_pk_mul_f32 v[70:71], v[70:71], v[160:161] op_sel_hi:[1,0]
	v_pk_mul_f32 v[68:69], v[68:69], v[160:161] op_sel_hi:[1,0]
	v_pk_mul_f32 v[66:67], v[66:67], v[160:161] op_sel_hi:[1,0]
	v_pk_mul_f32 v[64:65], v[64:65], v[160:161] op_sel_hi:[1,0]
	v_pk_mul_f32 v[62:63], v[62:63], v[160:161] op_sel_hi:[1,0]
	v_pk_mul_f32 v[60:61], v[60:61], v[160:161] op_sel_hi:[1,0]
	v_pk_mul_f32 v[58:59], v[58:59], v[160:161] op_sel_hi:[1,0]
	v_pk_mul_f32 v[56:57], v[56:57], v[160:161] op_sel_hi:[1,0]
	v_pk_mul_f32 v[54:55], v[54:55], v[160:161] op_sel_hi:[1,0]
	v_pk_mul_f32 v[52:53], v[52:53], v[160:161] op_sel_hi:[1,0]
	v_pk_mul_f32 v[50:51], v[50:51], v[160:161] op_sel_hi:[1,0]
	v_pk_mul_f32 v[48:49], v[48:49], v[160:161] op_sel_hi:[1,0]
	v_pk_mul_f32 v[46:47], v[46:47], v[160:161] op_sel_hi:[1,0]
	v_pk_mul_f32 v[44:45], v[44:45], v[160:161] op_sel_hi:[1,0]
	v_pk_mul_f32 v[42:43], v[42:43], v[160:161] op_sel_hi:[1,0]
	v_pk_mul_f32 v[40:41], v[40:41], v[160:161] op_sel_hi:[1,0]
	v_pk_mul_f32 v[38:39], v[38:39], v[160:161] op_sel_hi:[1,0]
	v_pk_mul_f32 v[36:37], v[36:37], v[160:161] op_sel_hi:[1,0]
	v_pk_mul_f32 v[34:35], v[34:35], v[160:161] op_sel_hi:[1,0]
	v_pk_mul_f32 v[32:33], v[32:33], v[160:161] op_sel_hi:[1,0]
	v_pk_mul_f32 v[30:31], v[30:31], v[160:161] op_sel_hi:[1,0]
	v_pk_mul_f32 v[28:29], v[28:29], v[160:161] op_sel_hi:[1,0]
	v_pk_mul_f32 v[26:27], v[26:27], v[160:161] op_sel_hi:[1,0]
	v_pk_mul_f32 v[24:25], v[24:25], v[160:161] op_sel_hi:[1,0]
	v_pk_mul_f32 v[22:23], v[22:23], v[160:161] op_sel_hi:[1,0]
	v_pk_mul_f32 v[20:21], v[20:21], v[160:161] op_sel_hi:[1,0]
	v_pk_mul_f32 v[18:19], v[18:19], v[160:161] op_sel_hi:[1,0]
	v_pk_mul_f32 v[16:17], v[16:17], v[160:161] op_sel_hi:[1,0]
	v_pk_mul_f32 v[14:15], v[14:15], v[160:161] op_sel_hi:[1,0]
	v_pk_mul_f32 v[12:13], v[12:13], v[160:161] op_sel_hi:[1,0]
	v_pk_mul_f32 v[10:11], v[10:11], v[160:161] op_sel_hi:[1,0]
	v_pk_mul_f32 v[8:9], v[8:9], v[160:161] op_sel_hi:[1,0]
	v_pk_mul_f32 v[6:7], v[6:7], v[160:161] op_sel_hi:[1,0]
	v_pk_mul_f32 v[4:5], v[4:5], v[160:161] op_sel_hi:[1,0]
	v_pk_mul_f32 v[2:3], v[2:3], v[160:161] op_sel_hi:[1,0]
	v_pk_mul_f32 v[0:1], v[0:1], v[160:161] op_sel_hi:[1,0]

.Lstg_b22:
	s_add_i32 s8, s85, -1
	s_cmp_ge_u32 s8, s75
	s_cselect_b64 s[66:67], -1, 0
	s_mov_b64 s[6:7], -1
	s_and_b64 vcc, exec, s[66:67]
	s_cbranch_vccz .LBB0_593
	v_mov_b64_e32 v[144:145], s[80:81]
	flat_load_dword v146, v[144:145] sc0 sc1
	s_waitcnt vmcnt(0)
	v_mov_b64_e32 v[144:145], s[72:73]
	flat_load_dword v144, v[144:145] sc0 sc1
	s_waitcnt vmcnt(0) lgkmcnt(0)
	v_readfirstlane_b32 s6, v146
	v_readfirstlane_b32 s7, v144
	s_nop 1
	s_nop 3
	s_mov_b32 m0, s78
	s_nop 0
	global_load_lds_dwordx4 v160, s[6:7]
	s_nop 3
	s_mov_b32 m0, s93
	s_nop 0
	global_load_lds_dwordx4 v170, s[6:7]
	s_mov_b64 s[6:7], 0
.LBB0_593:
	s_andn2_b64 vcc, exec, s[6:7]
	s_cbranch_vccnz .LBB0_595
	s_add_u32 s6, s76, 0x19f100
	s_addc_u32 s7, s77, 0
	s_mov_b32 m0, s82
	s_nop 0
	global_load_lds_dwordx4 v160, s[6:7]
	s_mov_b32 m0, s84
	s_nop 0
	global_load_lds_dwordx4 v170, s[6:7]
.LBB0_595:
	v_sub_f32_e32 v144, v190, v172
	v_mul_f32_e32 v144, 0x3e0293ee, v144
	v_exp_f32_e32 v144, v144
	s_nop 0
	v_cndmask_b32_e64 v172, v144, 1.0, s[4:5]
	s_mov_b32 m0, s3
	s_nop 0
	global_load_lds_dwordx4 v162, s[76:77]
	s_add_i32 m0, s69, 0xffffff80
	s_nop 0
	global_load_lds_dwordx4 v162, s[76:77] offset:128
	s_add_i32 m0, s68, 0xffffff00
	s_nop 0
	global_load_lds_dwordx4 v162, s[76:77] offset:256
	s_add_i32 m0, s2, 0xfffffe80
	s_nop 0
	global_load_lds_dwordx4 v162, s[76:77] offset:384
	v_cmp_gt_f32_e32 vcc, 1.0, v172
	s_cbranch_vccz .LBB0_597
	v_pk_mul_f32 v[126:127], v[126:127], v[172:173] op_sel_hi:[1,0]
	v_pk_mul_f32 v[124:125], v[124:125], v[172:173] op_sel_hi:[1,0]
	v_pk_mul_f32 v[122:123], v[122:123], v[172:173] op_sel_hi:[1,0]
	v_pk_mul_f32 v[120:121], v[120:121], v[172:173] op_sel_hi:[1,0]
	v_pk_mul_f32 v[118:119], v[118:119], v[172:173] op_sel_hi:[1,0]
	v_pk_mul_f32 v[116:117], v[116:117], v[172:173] op_sel_hi:[1,0]
	v_pk_mul_f32 v[114:115], v[114:115], v[172:173] op_sel_hi:[1,0]
	v_pk_mul_f32 v[112:113], v[112:113], v[172:173] op_sel_hi:[1,0]
	v_pk_mul_f32 v[110:111], v[110:111], v[172:173] op_sel_hi:[1,0]
	v_pk_mul_f32 v[108:109], v[108:109], v[172:173] op_sel_hi:[1,0]
	v_pk_mul_f32 v[106:107], v[106:107], v[172:173] op_sel_hi:[1,0]
	v_pk_mul_f32 v[104:105], v[104:105], v[172:173] op_sel_hi:[1,0]
	v_pk_mul_f32 v[102:103], v[102:103], v[172:173] op_sel_hi:[1,0]
	v_pk_mul_f32 v[100:101], v[100:101], v[172:173] op_sel_hi:[1,0]
	v_pk_mul_f32 v[98:99], v[98:99], v[172:173] op_sel_hi:[1,0]
	v_pk_mul_f32 v[96:97], v[96:97], v[172:173] op_sel_hi:[1,0]
	v_pk_mul_f32 v[94:95], v[94:95], v[172:173] op_sel_hi:[1,0]
	v_pk_mul_f32 v[92:93], v[92:93], v[172:173] op_sel_hi:[1,0]
	v_pk_mul_f32 v[90:91], v[90:91], v[172:173] op_sel_hi:[1,0]
	v_pk_mul_f32 v[88:89], v[88:89], v[172:173] op_sel_hi:[1,0]
	v_pk_mul_f32 v[86:87], v[86:87], v[172:173] op_sel_hi:[1,0]
	v_pk_mul_f32 v[84:85], v[84:85], v[172:173] op_sel_hi:[1,0]
	v_pk_mul_f32 v[82:83], v[82:83], v[172:173] op_sel_hi:[1,0]
	v_pk_mul_f32 v[80:81], v[80:81], v[172:173] op_sel_hi:[1,0]
	v_pk_mul_f32 v[78:79], v[78:79], v[172:173] op_sel_hi:[1,0]
	v_pk_mul_f32 v[76:77], v[76:77], v[172:173] op_sel_hi:[1,0]
	v_pk_mul_f32 v[74:75], v[74:75], v[172:173] op_sel_hi:[1,0]
	v_pk_mul_f32 v[72:73], v[72:73], v[172:173] op_sel_hi:[1,0]
	v_pk_mul_f32 v[70:71], v[70:71], v[172:173] op_sel_hi:[1,0]
	v_pk_mul_f32 v[68:69], v[68:69], v[172:173] op_sel_hi:[1,0]
	v_pk_mul_f32 v[66:67], v[66:67], v[172:173] op_sel_hi:[1,0]
	v_pk_mul_f32 v[64:65], v[64:65], v[172:173] op_sel_hi:[1,0]
	v_pk_mul_f32 v[62:63], v[62:63], v[172:173] op_sel_hi:[1,0]
	v_pk_mul_f32 v[60:61], v[60:61], v[172:173] op_sel_hi:[1,0]
	v_pk_mul_f32 v[58:59], v[58:59], v[172:173] op_sel_hi:[1,0]
	v_pk_mul_f32 v[56:57], v[56:57], v[172:173] op_sel_hi:[1,0]
	v_pk_mul_f32 v[54:55], v[54:55], v[172:173] op_sel_hi:[1,0]
	v_pk_mul_f32 v[52:53], v[52:53], v[172:173] op_sel_hi:[1,0]
	v_pk_mul_f32 v[50:51], v[50:51], v[172:173] op_sel_hi:[1,0]
	v_pk_mul_f32 v[48:49], v[48:49], v[172:173] op_sel_hi:[1,0]
	v_pk_mul_f32 v[46:47], v[46:47], v[172:173] op_sel_hi:[1,0]
	v_pk_mul_f32 v[44:45], v[44:45], v[172:173] op_sel_hi:[1,0]
	v_pk_mul_f32 v[42:43], v[42:43], v[172:173] op_sel_hi:[1,0]
	v_pk_mul_f32 v[40:41], v[40:41], v[172:173] op_sel_hi:[1,0]
	v_pk_mul_f32 v[38:39], v[38:39], v[172:173] op_sel_hi:[1,0]
	v_pk_mul_f32 v[36:37], v[36:37], v[172:173] op_sel_hi:[1,0]
	v_pk_mul_f32 v[34:35], v[34:35], v[172:173] op_sel_hi:[1,0]
	v_pk_mul_f32 v[32:33], v[32:33], v[172:173] op_sel_hi:[1,0]
	v_pk_mul_f32 v[30:31], v[30:31], v[172:173] op_sel_hi:[1,0]
	v_pk_mul_f32 v[28:29], v[28:29], v[172:173] op_sel_hi:[1,0]
	v_pk_mul_f32 v[26:27], v[26:27], v[172:173] op_sel_hi:[1,0]
	v_pk_mul_f32 v[24:25], v[24:25], v[172:173] op_sel_hi:[1,0]
	v_pk_mul_f32 v[22:23], v[22:23], v[172:173] op_sel_hi:[1,0]
	v_pk_mul_f32 v[20:21], v[20:21], v[172:173] op_sel_hi:[1,0]
	v_pk_mul_f32 v[18:19], v[18:19], v[172:173] op_sel_hi:[1,0]
	v_pk_mul_f32 v[16:17], v[16:17], v[172:173] op_sel_hi:[1,0]
	v_pk_mul_f32 v[14:15], v[14:15], v[172:173] op_sel_hi:[1,0]
	v_pk_mul_f32 v[12:13], v[12:13], v[172:173] op_sel_hi:[1,0]
	v_pk_mul_f32 v[10:11], v[10:11], v[172:173] op_sel_hi:[1,0]
	v_pk_mul_f32 v[8:9], v[8:9], v[172:173] op_sel_hi:[1,0]
	v_pk_mul_f32 v[6:7], v[6:7], v[172:173] op_sel_hi:[1,0]
	v_pk_mul_f32 v[4:5], v[4:5], v[172:173] op_sel_hi:[1,0]
	v_pk_mul_f32 v[2:3], v[2:3], v[172:173] op_sel_hi:[1,0]
	v_pk_mul_f32 v[0:1], v[0:1], v[172:173] op_sel_hi:[1,0]

.Lstg_b23:
	s_cmp_gt_u32 s85, s75
	s_cbranch_scc1 .LBB0_604
	s_cmp_ge_u32 s85, s75
	s_mov_b64 s[6:7], -1
	s_cbranch_scc0 .LBB0_602
	v_mov_b64_e32 v[148:149], s[80:81]
	flat_load_dword v144, v[148:149] sc0 sc1
	s_waitcnt vmcnt(0)
	v_mov_b64_e32 v[148:149], s[72:73]
	flat_load_dword v147, v[148:149] sc0 sc1
	s_waitcnt vmcnt(0) lgkmcnt(0)
	v_readfirstlane_b32 s6, v144
	v_readfirstlane_b32 s7, v147
	s_nop 1
	s_nop 3
	s_mov_b32 m0, s78
	s_nop 0
	global_load_lds_dwordx4 v160, s[6:7]
	s_nop 3
	s_mov_b32 m0, s93
	s_nop 0
	global_load_lds_dwordx4 v170, s[6:7]
	s_mov_b64 s[6:7], 0
.LBB0_602:
	s_andn2_b64 vcc, exec, s[6:7]
	s_cbranch_vccnz .LBB0_604
	s_add_u32 s6, s76, 0x33f100
	s_addc_u32 s7, s77, 0
	s_mov_b32 m0, s78
	s_nop 0
	global_load_lds_dwordx4 v160, s[6:7]
	s_mov_b32 m0, s93
	s_nop 0
	global_load_lds_dwordx4 v170, s[6:7]
.LBB0_604:
	s_mov_b64 s[6:7], -1
	s_and_b64 vcc, exec, s[66:67]
	s_cbranch_vccz .LBB0_606
	v_mov_b64_e32 v[148:149], s[0:1]
	flat_load_dword v144, v[148:149] sc0 sc1
	s_waitcnt vmcnt(0)
	v_mov_b64_e32 v[148:149], s[70:71]
	flat_load_dword v147, v[148:149] sc0 sc1
	s_waitcnt vmcnt(0) lgkmcnt(0)
	v_readfirstlane_b32 s6, v144
	v_readfirstlane_b32 s7, v147
	s_nop 1
	s_nop 3
	s_mov_b32 m0, s3
	s_nop 0
	global_load_lds_dwordx4 v162, s[6:7]
	s_nop 3
	s_add_i32 m0, s69, 0xffffff80
	s_nop 0
	global_load_lds_dwordx4 v162, s[6:7] offset:128
	s_add_i32 m0, s68, 0xffffff00
	s_nop 0
	global_load_lds_dwordx4 v162, s[6:7] offset:256
	s_add_i32 m0, s2, 0xfffffe80
	s_nop 0
	global_load_lds_dwordx4 v162, s[6:7] offset:384
	s_mov_b64 s[6:7], 0
.LBB0_606:
	s_andn2_b64 vcc, exec, s[6:7]
	s_cbranch_vccnz .LBB0_608
	s_add_u32 s6, s76, 0x1a0000
	s_addc_u32 s7, s77, 0
	s_mov_b32 m0, s90
	s_nop 0
	global_load_lds_dwordx4 v162, s[6:7]
	s_add_i32 m0, s91, 0xffffff80
	s_nop 0
	global_load_lds_dwordx4 v162, s[6:7] offset:128
	s_add_i32 m0, s88, 0xffffff00
	s_nop 0
	global_load_lds_dwordx4 v162, s[6:7] offset:256
	s_add_i32 m0, s89, 0xfffffe80
	s_nop 0
	global_load_lds_dwordx4 v162, s[6:7] offset:384

.Lstg_b24:
	v_mov_b64_e32 v[146:147], s[0:1]
	flat_load_dword v148, v[146:147] sc0 sc1
	s_waitcnt vmcnt(0)
	v_mov_b64_e32 v[146:147], s[70:71]
	flat_load_dword v146, v[146:147] sc0 sc1
	s_waitcnt vmcnt(0) lgkmcnt(0)
	v_readfirstlane_b32 s4, v148
	v_readfirstlane_b32 s5, v146
	s_nop 1
	s_nop 3
	s_mov_b32 m0, s3
	s_nop 0
	global_load_lds_dwordx4 v162, s[4:5]
	s_nop 3
	s_add_i32 m0, s69, 0xffffff80
	s_nop 0
	global_load_lds_dwordx4 v162, s[4:5] offset:128
	s_add_i32 m0, s68, 0xffffff00
	s_nop 0
	global_load_lds_dwordx4 v162, s[4:5] offset:256
	s_add_i32 m0, s2, 0xfffffe80
	s_nop 0
	global_load_lds_dwordx4 v162, s[4:5] offset:384
	v_cmp_gt_f32_e32 vcc, 1.0, v160
	s_cbranch_vccz .LBB0_551
	v_pk_mul_f32 v[126:127], v[126:127], v[160:161] op_sel_hi:[1,0]
	v_pk_mul_f32 v[124:125], v[124:125], v[160:161] op_sel_hi:[1,0]
	v_pk_mul_f32 v[122:123], v[122:123], v[160:161] op_sel_hi:[1,0]
	v_pk_mul_f32 v[120:121], v[120:121], v[160:161] op_sel_hi:[1,0]
	v_pk_mul_f32 v[118:119], v[118:119], v[160:161] op_sel_hi:[1,0]
	v_pk_mul_f32 v[116:117], v[116:117], v[160:161] op_sel_hi:[1,0]
	v_pk_mul_f32 v[114:115], v[114:115], v[160:161] op_sel_hi:[1,0]
	v_pk_mul_f32 v[112:113], v[112:113], v[160:161] op_sel_hi:[1,0]
	v_pk_mul_f32 v[110:111], v[110:111], v[160:161] op_sel_hi:[1,0]
	v_pk_mul_f32 v[108:109], v[108:109], v[160:161] op_sel_hi:[1,0]
	v_pk_mul_f32 v[106:107], v[106:107], v[160:161] op_sel_hi:[1,0]
	v_pk_mul_f32 v[104:105], v[104:105], v[160:161] op_sel_hi:[1,0]
	v_pk_mul_f32 v[102:103], v[102:103], v[160:161] op_sel_hi:[1,0]
	v_pk_mul_f32 v[100:101], v[100:101], v[160:161] op_sel_hi:[1,0]
	v_pk_mul_f32 v[98:99], v[98:99], v[160:161] op_sel_hi:[1,0]
	v_pk_mul_f32 v[96:97], v[96:97], v[160:161] op_sel_hi:[1,0]
	v_pk_mul_f32 v[94:95], v[94:95], v[160:161] op_sel_hi:[1,0]
	v_pk_mul_f32 v[92:93], v[92:93], v[160:161] op_sel_hi:[1,0]
	v_pk_mul_f32 v[90:91], v[90:91], v[160:161] op_sel_hi:[1,0]
	v_pk_mul_f32 v[88:89], v[88:89], v[160:161] op_sel_hi:[1,0]
	v_pk_mul_f32 v[86:87], v[86:87], v[160:161] op_sel_hi:[1,0]
	v_pk_mul_f32 v[84:85], v[84:85], v[160:161] op_sel_hi:[1,0]
	v_pk_mul_f32 v[82:83], v[82:83], v[160:161] op_sel_hi:[1,0]
	v_pk_mul_f32 v[80:81], v[80:81], v[160:161] op_sel_hi:[1,0]
	v_pk_mul_f32 v[78:79], v[78:79], v[160:161] op_sel_hi:[1,0]
	v_pk_mul_f32 v[76:77], v[76:77], v[160:161] op_sel_hi:[1,0]
	v_pk_mul_f32 v[74:75], v[74:75], v[160:161] op_sel_hi:[1,0]
	v_pk_mul_f32 v[72:73], v[72:73], v[160:161] op_sel_hi:[1,0]
	v_pk_mul_f32 v[70:71], v[70:71], v[160:161] op_sel_hi:[1,0]
	v_pk_mul_f32 v[68:69], v[68:69], v[160:161] op_sel_hi:[1,0]
	v_pk_mul_f32 v[66:67], v[66:67], v[160:161] op_sel_hi:[1,0]
	v_pk_mul_f32 v[64:65], v[64:65], v[160:161] op_sel_hi:[1,0]
	v_pk_mul_f32 v[62:63], v[62:63], v[160:161] op_sel_hi:[1,0]
	v_pk_mul_f32 v[60:61], v[60:61], v[160:161] op_sel_hi:[1,0]
	v_pk_mul_f32 v[58:59], v[58:59], v[160:161] op_sel_hi:[1,0]
	v_pk_mul_f32 v[56:57], v[56:57], v[160:161] op_sel_hi:[1,0]
	v_pk_mul_f32 v[54:55], v[54:55], v[160:161] op_sel_hi:[1,0]
	v_pk_mul_f32 v[52:53], v[52:53], v[160:161] op_sel_hi:[1,0]
	v_pk_mul_f32 v[50:51], v[50:51], v[160:161] op_sel_hi:[1,0]
	v_pk_mul_f32 v[48:49], v[48:49], v[160:161] op_sel_hi:[1,0]
	v_pk_mul_f32 v[46:47], v[46:47], v[160:161] op_sel_hi:[1,0]
	v_pk_mul_f32 v[44:45], v[44:45], v[160:161] op_sel_hi:[1,0]
	v_pk_mul_f32 v[42:43], v[42:43], v[160:161] op_sel_hi:[1,0]
	v_pk_mul_f32 v[40:41], v[40:41], v[160:161] op_sel_hi:[1,0]
	v_pk_mul_f32 v[38:39], v[38:39], v[160:161] op_sel_hi:[1,0]
	v_pk_mul_f32 v[36:37], v[36:37], v[160:161] op_sel_hi:[1,0]
	v_pk_mul_f32 v[34:35], v[34:35], v[160:161] op_sel_hi:[1,0]
	v_pk_mul_f32 v[32:33], v[32:33], v[160:161] op_sel_hi:[1,0]
	v_pk_mul_f32 v[30:31], v[30:31], v[160:161] op_sel_hi:[1,0]
	v_pk_mul_f32 v[28:29], v[28:29], v[160:161] op_sel_hi:[1,0]
	v_pk_mul_f32 v[26:27], v[26:27], v[160:161] op_sel_hi:[1,0]
	v_pk_mul_f32 v[24:25], v[24:25], v[160:161] op_sel_hi:[1,0]
	v_pk_mul_f32 v[22:23], v[22:23], v[160:161] op_sel_hi:[1,0]
	v_pk_mul_f32 v[20:21], v[20:21], v[160:161] op_sel_hi:[1,0]
	v_pk_mul_f32 v[18:19], v[18:19], v[160:161] op_sel_hi:[1,0]
	v_pk_mul_f32 v[16:17], v[16:17], v[160:161] op_sel_hi:[1,0]
	v_pk_mul_f32 v[14:15], v[14:15], v[160:161] op_sel_hi:[1,0]
	v_pk_mul_f32 v[12:13], v[12:13], v[160:161] op_sel_hi:[1,0]
	v_pk_mul_f32 v[10:11], v[10:11], v[160:161] op_sel_hi:[1,0]
	v_pk_mul_f32 v[8:9], v[8:9], v[160:161] op_sel_hi:[1,0]
	v_pk_mul_f32 v[6:7], v[6:7], v[160:161] op_sel_hi:[1,0]
	v_pk_mul_f32 v[4:5], v[4:5], v[160:161] op_sel_hi:[1,0]
	v_pk_mul_f32 v[2:3], v[2:3], v[160:161] op_sel_hi:[1,0]
	v_pk_mul_f32 v[0:1], v[0:1], v[160:161] op_sel_hi:[1,0]
	s_branch .LBB0_551

.LBB0_750:
	v_mov_b64_e32 v[0:1], 0x400
	s_ashr_i32 s7, s6, 31
	v_cmp_lt_i64_e32 vcc, s[8:9], v[0:1]
	s_lshl_b64 s[8:9], s[6:7], 20
	s_add_u32 s8, s23, s8
	s_addc_u32 s9, s24, s9
	s_and_b64 s[10:11], vcc, exec
	s_cselect_b32 s7, s9, s17
	s_cselect_b32 s50, s8, s16
	s_ashr_i32 s5, s4, 31
	s_lshl_b64 s[10:11], s[4:5], 20
	s_add_u32 s10, s25, s10
	s_addc_u32 s11, s26, s11
	s_and_b64 s[18:19], vcc, exec
	s_cselect_b32 s5, s11, s15
	s_cselect_b32 s51, s10, s14
	s_add_u32 s52, s14, 0x100
	s_addc_u32 s53, s15, 0
	s_add_u32 s14, s16, 0x80080
	v_mov_b32_e32 v0, 0
	s_addc_u32 s15, s17, 0
	s_mov_b32 s54, -2
	s_cmp_eq_u32 s48, 1
	s_cbranch_scc1 .Lpeel_zero_P5
	v_add_u32_e32 v120, s13, v230
	v_add_u32_e32 v148, s29, v230
	ds_read_b128 v[88:91], v120
	ds_read_b128 v[100:103], v120 offset:1024
	ds_read_b128 v[112:115], v120 offset:2048
	ds_read_b128 v[120:123], v120 offset:3072
	ds_read_b128 v[124:127], v148
	ds_read_b128 v[140:143], v148 offset:1024
	ds_read_b128 v[144:147], v148 offset:2048
	ds_read_b128 v[148:151], v148 offset:3072
	s_add_u32 s16, s14, 0xfff80080
	s_addc_u32 s17, s15, -1
	s_cmp_eq_u32 s54, 28
	s_cselect_b32 s19, s7, s17
	s_cselect_b32 s18, s50, s16
	s_cselect_b32 s17, s5, s53
	s_cselect_b32 s16, s51, s52
	v_lshl_add_u64 v[206:207], s[14:15], 0, v[204:205]
	s_add_i32 m0, s34, 0xc000
	ds_read_b128 v[152:155], v232
	ds_read_b128 v[170:173], v232 offset:1024
	ds_read_b128 v[174:177], v232 offset:2048
	ds_read_b128 v[178:181], v232 offset:3072
	ds_read_b128 v[182:185], v232 offset:4096
	ds_read_b128 v[186:189], v232 offset:5120
	ds_read_b128 v[190:193], v232 offset:6144
	ds_read_b128 v[194:197], v232 offset:7168
	global_load_lds_dwordx4 v[206:207], off
	v_lshl_add_u64 v[206:207], s[14:15], 0, v[202:203]
	s_add_i32 m0, s34, 0xe000
	s_nop 0
	global_load_lds_dwordx4 v[206:207], off
	s_waitcnt vmcnt(40)
	s_waitcnt lgkmcnt(0)
	s_barrier
	s_setprio 1
	s_waitcnt lgkmcnt(0)
	v_mfma_f32_16x16x32_bf16 v[166:169], v[88:91], v[152:155], 0
	v_mfma_f32_16x16x32_bf16 v[156:159], v[112:115], v[152:155], 0
	v_mfma_f32_16x16x32_bf16 v[128:131], v[88:91], v[174:177], 0
	v_mfma_f32_16x16x32_bf16 v[116:119], v[112:115], v[174:177], 0
	v_mfma_f32_16x16x32_bf16 v[96:99], v[88:91], v[182:185], 0
	v_mfma_f32_16x16x32_bf16 v[92:95], v[112:115], v[182:185], 0
	v_mfma_f32_16x16x32_bf16 v[76:79], v[88:91], v[190:193], 0
	v_mfma_f32_16x16x32_bf16 v[72:75], v[112:115], v[190:193], 0
	v_mfma_f32_16x16x32_bf16 v[166:169], v[100:103], v[170:173], v[166:169]
	v_mfma_f32_16x16x32_bf16 v[156:159], v[120:123], v[170:173], v[156:159]
	v_mfma_f32_16x16x32_bf16 v[128:131], v[100:103], v[178:181], v[128:131]
	v_mfma_f32_16x16x32_bf16 v[116:119], v[120:123], v[178:181], v[116:119]
	v_mfma_f32_16x16x32_bf16 v[96:99], v[100:103], v[186:189], v[96:99]
	v_mfma_f32_16x16x32_bf16 v[92:95], v[120:123], v[186:189], v[92:95]
	v_mfma_f32_16x16x32_bf16 v[76:79], v[100:103], v[194:197], v[76:79]
	v_mfma_f32_16x16x32_bf16 v[72:75], v[120:123], v[194:197], v[72:75]
	s_setprio 0
	s_setprio 1
	v_mfma_f32_16x16x32_bf16 v[136:139], v[124:127], v[152:155], 0
	v_mfma_f32_16x16x32_bf16 v[132:135], v[144:147], v[152:155], 0
	v_mfma_f32_16x16x32_bf16 v[108:111], v[124:127], v[174:177], 0
	v_mfma_f32_16x16x32_bf16 v[104:107], v[144:147], v[174:177], 0
	v_mfma_f32_16x16x32_bf16 v[84:87], v[124:127], v[182:185], 0
	v_mfma_f32_16x16x32_bf16 v[80:83], v[144:147], v[182:185], 0
	v_mfma_f32_16x16x32_bf16 v[68:71], v[124:127], v[190:193], 0
	v_mfma_f32_16x16x32_bf16 v[64:67], v[144:147], v[190:193], 0
	v_mfma_f32_16x16x32_bf16 v[136:139], v[140:143], v[170:173], v[136:139]
	v_mfma_f32_16x16x32_bf16 v[132:135], v[148:151], v[170:173], v[132:135]
	v_mfma_f32_16x16x32_bf16 v[108:111], v[140:143], v[178:181], v[108:111]
	v_mfma_f32_16x16x32_bf16 v[104:107], v[148:151], v[178:181], v[104:107]
	v_mfma_f32_16x16x32_bf16 v[84:87], v[140:143], v[186:189], v[84:87]
	v_mfma_f32_16x16x32_bf16 v[80:83], v[148:151], v[186:189], v[80:83]
	v_mfma_f32_16x16x32_bf16 v[68:71], v[140:143], v[194:197], v[68:71]
	v_mfma_f32_16x16x32_bf16 v[64:67], v[148:151], v[194:197], v[64:67]
	s_setprio 0
	s_barrier
	s_mov_b32 m0, s27
	v_lshl_add_u64 v[206:207], s[16:17], 0, v[160:161]
	s_add_u32 s56, s16, 0x80000
	ds_read_b128 v[152:155], v232 offset:16384
	ds_read_b128 v[170:173], v232 offset:17408
	ds_read_b128 v[174:177], v232 offset:18432
	ds_read_b128 v[178:181], v232 offset:19456
	ds_read_b128 v[182:185], v232 offset:20480
	ds_read_b128 v[186:189], v232 offset:21504
	ds_read_b128 v[190:193], v232 offset:22528
	ds_read_b128 v[194:197], v232 offset:23552
	global_load_lds_dwordx4 v[206:207], off
	v_lshl_add_u64 v[208:209], s[16:17], 0, v[200:201]
	s_mov_b32 m0, s28
	s_addc_u32 s57, s17, 0
	global_load_lds_dwordx4 v[208:209], off
	v_lshl_add_u64 v[210:211], s[56:57], 0, v[160:161]
	s_mov_b32 m0, s30
	v_lshl_add_u64 v[212:213], s[18:19], 0, v[198:199]
	global_load_lds_dwordx4 v[210:211], off
	v_lshl_add_u64 v[210:211], s[56:57], 0, v[200:201]
	s_mov_b32 m0, s31
	s_nop 0
	global_load_lds_dwordx4 v[210:211], off
	v_lshl_add_u64 v[210:211], s[18:19], 0, v[162:163]
	s_mov_b32 m0, s34
	s_nop 0
	global_load_lds_dwordx4 v[210:211], off
	s_mov_b32 m0, s35
	s_nop 0
	global_load_lds_dwordx4 v[212:213], off
	s_waitcnt vmcnt(40)
	s_waitcnt lgkmcnt(0)
	s_barrier
	s_setprio 1
	s_waitcnt lgkmcnt(0)
	v_mfma_f32_16x16x32_bf16 v[60:63], v[88:91], v[152:155], 0
	v_mfma_f32_16x16x32_bf16 v[56:59], v[112:115], v[152:155], 0
	v_mfma_f32_16x16x32_bf16 v[44:47], v[88:91], v[174:177], 0
	v_mfma_f32_16x16x32_bf16 v[40:43], v[112:115], v[174:177], 0
	v_mfma_f32_16x16x32_bf16 v[28:31], v[88:91], v[182:185], 0
	v_mfma_f32_16x16x32_bf16 v[24:27], v[112:115], v[182:185], 0
	v_mfma_f32_16x16x32_bf16 v[12:15], v[88:91], v[190:193], 0
	v_mfma_f32_16x16x32_bf16 v[8:11], v[112:115], v[190:193], 0
	v_mfma_f32_16x16x32_bf16 v[60:63], v[100:103], v[170:173], v[60:63]
	v_mfma_f32_16x16x32_bf16 v[56:59], v[120:123], v[170:173], v[56:59]
	v_mfma_f32_16x16x32_bf16 v[44:47], v[100:103], v[178:181], v[44:47]
	v_mfma_f32_16x16x32_bf16 v[40:43], v[120:123], v[178:181], v[40:43]
	v_mfma_f32_16x16x32_bf16 v[28:31], v[100:103], v[186:189], v[28:31]
	v_mfma_f32_16x16x32_bf16 v[24:27], v[120:123], v[186:189], v[24:27]
	v_mfma_f32_16x16x32_bf16 v[12:15], v[100:103], v[194:197], v[12:15]
	v_mfma_f32_16x16x32_bf16 v[8:11], v[120:123], v[194:197], v[8:11]
	s_setprio 0
	s_setprio 1
	v_mfma_f32_16x16x32_bf16 v[52:55], v[124:127], v[152:155], 0
	v_mfma_f32_16x16x32_bf16 v[48:51], v[144:147], v[152:155], 0
	v_mfma_f32_16x16x32_bf16 v[36:39], v[124:127], v[174:177], 0
	v_mfma_f32_16x16x32_bf16 v[32:35], v[144:147], v[174:177], 0
	v_mfma_f32_16x16x32_bf16 v[20:23], v[124:127], v[182:185], 0
	v_mfma_f32_16x16x32_bf16 v[16:19], v[144:147], v[182:185], 0
	v_mfma_f32_16x16x32_bf16 v[4:7], v[124:127], v[190:193], 0
	v_mfma_f32_16x16x32_bf16 v[0:3], v[144:147], v[190:193], 0
	v_mfma_f32_16x16x32_bf16 v[52:55], v[140:143], v[170:173], v[52:55]
	v_mfma_f32_16x16x32_bf16 v[48:51], v[148:151], v[170:173], v[48:51]
	v_mfma_f32_16x16x32_bf16 v[36:39], v[140:143], v[178:181], v[36:39]
	v_mfma_f32_16x16x32_bf16 v[32:35], v[148:151], v[178:181], v[32:35]
	v_mfma_f32_16x16x32_bf16 v[20:23], v[140:143], v[186:189], v[20:23]
	v_mfma_f32_16x16x32_bf16 v[16:19], v[148:151], v[186:189], v[16:19]
	v_mfma_f32_16x16x32_bf16 v[4:7], v[140:143], v[194:197], v[4:7]
	v_mfma_f32_16x16x32_bf16 v[0:3], v[148:151], v[194:197], v[0:3]
	s_setprio 0
	s_barrier
	v_add_u32_e32 v120, s39, v230
	v_add_u32_e32 v148, s44, v230
	ds_read_b128 v[88:91], v120
	ds_read_b128 v[100:103], v120 offset:1024
	ds_read_b128 v[112:115], v120 offset:2048
	ds_read_b128 v[120:123], v120 offset:3072
	ds_read_b128 v[124:127], v148
	ds_read_b128 v[140:143], v148 offset:1024
	ds_read_b128 v[144:147], v148 offset:2048
	ds_read_b128 v[148:151], v148 offset:3072
	s_add_u32 s18, s18, 0x80000
	s_addc_u32 s19, s19, 0
	s_mov_b32 m0, s36
	v_lshl_add_u64 v[214:215], s[18:19], 0, v[162:163]
	ds_read_b128 v[152:155], v232 offset:32768
	ds_read_b128 v[170:173], v232 offset:33792
	ds_read_b128 v[174:177], v232 offset:34816
	ds_read_b128 v[178:181], v232 offset:35840
	ds_read_b128 v[182:185], v232 offset:36864
	ds_read_b128 v[186:189], v232 offset:37888
	ds_read_b128 v[190:193], v232 offset:38912
	ds_read_b128 v[194:197], v232 offset:39936
	global_load_lds_dwordx4 v[214:215], off
	v_lshl_add_u64 v[214:215], s[18:19], 0, v[198:199]
	s_mov_b32 m0, s37
	s_nop 0
	global_load_lds_dwordx4 v[214:215], off
	s_waitcnt vmcnt(8)
	s_waitcnt lgkmcnt(0)
	s_barrier
	s_setprio 1
	s_waitcnt lgkmcnt(0)
	v_mfma_f32_16x16x32_bf16 v[166:169], v[88:91], v[152:155], v[166:169]
	v_mfma_f32_16x16x32_bf16 v[156:159], v[112:115], v[152:155], v[156:159]
	v_mfma_f32_16x16x32_bf16 v[128:131], v[88:91], v[174:177], v[128:131]
	v_mfma_f32_16x16x32_bf16 v[116:119], v[112:115], v[174:177], v[116:119]
	v_mfma_f32_16x16x32_bf16 v[96:99], v[88:91], v[182:185], v[96:99]
	v_mfma_f32_16x16x32_bf16 v[92:95], v[112:115], v[182:185], v[92:95]
	v_mfma_f32_16x16x32_bf16 v[76:79], v[88:91], v[190:193], v[76:79]
	v_mfma_f32_16x16x32_bf16 v[72:75], v[112:115], v[190:193], v[72:75]
	v_mfma_f32_16x16x32_bf16 v[166:169], v[100:103], v[170:173], v[166:169]
	v_mfma_f32_16x16x32_bf16 v[156:159], v[120:123], v[170:173], v[156:159]
	v_mfma_f32_16x16x32_bf16 v[128:131], v[100:103], v[178:181], v[128:131]
	v_mfma_f32_16x16x32_bf16 v[116:119], v[120:123], v[178:181], v[116:119]
	v_mfma_f32_16x16x32_bf16 v[96:99], v[100:103], v[186:189], v[96:99]
	v_mfma_f32_16x16x32_bf16 v[92:95], v[120:123], v[186:189], v[92:95]
	v_mfma_f32_16x16x32_bf16 v[76:79], v[100:103], v[194:197], v[76:79]
	v_mfma_f32_16x16x32_bf16 v[72:75], v[120:123], v[194:197], v[72:75]
	s_setprio 0
	s_setprio 1
	v_mfma_f32_16x16x32_bf16 v[136:139], v[124:127], v[152:155], v[136:139]
	v_mfma_f32_16x16x32_bf16 v[132:135], v[144:147], v[152:155], v[132:135]
	v_mfma_f32_16x16x32_bf16 v[108:111], v[124:127], v[174:177], v[108:111]
	v_mfma_f32_16x16x32_bf16 v[104:107], v[144:147], v[174:177], v[104:107]
	v_mfma_f32_16x16x32_bf16 v[84:87], v[124:127], v[182:185], v[84:87]
	v_mfma_f32_16x16x32_bf16 v[80:83], v[144:147], v[182:185], v[80:83]
	v_mfma_f32_16x16x32_bf16 v[68:71], v[124:127], v[190:193], v[68:71]
	v_mfma_f32_16x16x32_bf16 v[64:67], v[144:147], v[190:193], v[64:67]
	v_mfma_f32_16x16x32_bf16 v[136:139], v[140:143], v[170:173], v[136:139]
	v_mfma_f32_16x16x32_bf16 v[132:135], v[148:151], v[170:173], v[132:135]
	v_mfma_f32_16x16x32_bf16 v[108:111], v[140:143], v[178:181], v[108:111]
	v_mfma_f32_16x16x32_bf16 v[104:107], v[148:151], v[178:181], v[104:107]
	v_mfma_f32_16x16x32_bf16 v[84:87], v[140:143], v[186:189], v[84:87]
	v_mfma_f32_16x16x32_bf16 v[80:83], v[148:151], v[186:189], v[80:83]
	v_mfma_f32_16x16x32_bf16 v[68:71], v[140:143], v[194:197], v[68:71]
	v_mfma_f32_16x16x32_bf16 v[64:67], v[148:151], v[194:197], v[64:67]
	s_setprio 0
	s_barrier
	s_mov_b32 m0, s40
	v_lshl_add_u64 v[206:207], v[206:207], 0, s[86:87]
	s_add_u32 s16, s16, 0x80080
	ds_read_b128 v[152:155], v232 offset:49152
	ds_read_b128 v[170:173], v232 offset:50176
	ds_read_b128 v[174:177], v232 offset:51200
	ds_read_b128 v[178:181], v232 offset:52224
	ds_read_b128 v[182:185], v232 offset:53248
	ds_read_b128 v[186:189], v232 offset:54272
	ds_read_b128 v[190:193], v232 offset:55296
	ds_read_b128 v[194:197], v232 offset:56320
	global_load_lds_dwordx4 v[206:207], off
	v_lshl_add_u64 v[206:207], v[208:209], 0, s[86:87]
	s_mov_b32 m0, s41
	s_addc_u32 s17, s17, 0
	global_load_lds_dwordx4 v[206:207], off
	v_lshl_add_u64 v[206:207], s[16:17], 0, v[160:161]
	s_mov_b32 m0, s45
	s_nop 0
	global_load_lds_dwordx4 v[206:207], off
	v_lshl_add_u64 v[206:207], s[16:17], 0, v[200:201]
	s_mov_b32 m0, s46
	s_nop 0
	global_load_lds_dwordx4 v[206:207], off
	v_lshl_add_u64 v[206:207], v[210:211], 0, s[86:87]
	s_mov_b32 m0, s42
	s_nop 0
	global_load_lds_dwordx4 v[206:207], off
	v_lshl_add_u64 v[206:207], v[212:213], 0, s[86:87]
	s_mov_b32 m0, s43
	s_nop 0
	global_load_lds_dwordx4 v[206:207], off
	s_waitcnt vmcnt(8)
	s_waitcnt lgkmcnt(0)
	s_barrier
	s_setprio 1
	s_waitcnt lgkmcnt(0)
	v_mfma_f32_16x16x32_bf16 v[60:63], v[88:91], v[152:155], v[60:63]
	v_mfma_f32_16x16x32_bf16 v[56:59], v[112:115], v[152:155], v[56:59]
	v_mfma_f32_16x16x32_bf16 v[44:47], v[88:91], v[174:177], v[44:47]
	v_mfma_f32_16x16x32_bf16 v[40:43], v[112:115], v[174:177], v[40:43]
	v_mfma_f32_16x16x32_bf16 v[28:31], v[88:91], v[182:185], v[28:31]
	v_mfma_f32_16x16x32_bf16 v[24:27], v[112:115], v[182:185], v[24:27]
	v_mfma_f32_16x16x32_bf16 v[12:15], v[88:91], v[190:193], v[12:15]
	v_mfma_f32_16x16x32_bf16 v[8:11], v[112:115], v[190:193], v[8:11]
	v_mfma_f32_16x16x32_bf16 v[60:63], v[100:103], v[170:173], v[60:63]
	v_mfma_f32_16x16x32_bf16 v[56:59], v[120:123], v[170:173], v[56:59]
	v_mfma_f32_16x16x32_bf16 v[44:47], v[100:103], v[178:181], v[44:47]
	v_mfma_f32_16x16x32_bf16 v[40:43], v[120:123], v[178:181], v[40:43]
	v_mfma_f32_16x16x32_bf16 v[28:31], v[100:103], v[186:189], v[28:31]
	v_mfma_f32_16x16x32_bf16 v[24:27], v[120:123], v[186:189], v[24:27]
	v_mfma_f32_16x16x32_bf16 v[12:15], v[100:103], v[194:197], v[12:15]
	v_mfma_f32_16x16x32_bf16 v[8:11], v[120:123], v[194:197], v[8:11]
	s_setprio 0
	s_setprio 1
	v_mfma_f32_16x16x32_bf16 v[52:55], v[124:127], v[152:155], v[52:55]
	v_mfma_f32_16x16x32_bf16 v[48:51], v[144:147], v[152:155], v[48:51]
	v_mfma_f32_16x16x32_bf16 v[36:39], v[124:127], v[174:177], v[36:39]
	v_mfma_f32_16x16x32_bf16 v[32:35], v[144:147], v[174:177], v[32:35]
	v_mfma_f32_16x16x32_bf16 v[20:23], v[124:127], v[182:185], v[20:23]
	v_mfma_f32_16x16x32_bf16 v[16:19], v[144:147], v[182:185], v[16:19]
	v_mfma_f32_16x16x32_bf16 v[4:7], v[124:127], v[190:193], v[4:7]
	v_mfma_f32_16x16x32_bf16 v[0:3], v[144:147], v[190:193], v[0:3]
	v_mfma_f32_16x16x32_bf16 v[52:55], v[140:143], v[170:173], v[52:55]
	v_mfma_f32_16x16x32_bf16 v[48:51], v[148:151], v[170:173], v[48:51]
	v_mfma_f32_16x16x32_bf16 v[36:39], v[140:143], v[178:181], v[36:39]
	v_mfma_f32_16x16x32_bf16 v[32:35], v[148:151], v[178:181], v[32:35]
	v_mfma_f32_16x16x32_bf16 v[20:23], v[140:143], v[186:189], v[20:23]
	v_mfma_f32_16x16x32_bf16 v[16:19], v[148:151], v[186:189], v[16:19]
	v_mfma_f32_16x16x32_bf16 v[4:7], v[140:143], v[194:197], v[4:7]
	v_mfma_f32_16x16x32_bf16 v[0:3], v[148:151], v[194:197], v[0:3]
	s_setprio 0
	s_barrier
	s_add_i32 s54, s54, 2
	s_add_u32 s52, s52, 0x100
	s_addc_u32 s53, s53, 0
	s_add_u32 s14, s14, 0x100
	s_addc_u32 s15, s15, 0
	s_branch .LBB0_751
.Lpeel_zero_P5:
	v_mov_b32_e32 v1, v0
	v_mov_b32_e32 v2, v0
	v_mov_b32_e32 v3, v0
	v_mov_b32_e32 v4, v0
	v_mov_b32_e32 v5, v0
	v_mov_b32_e32 v6, v0
	v_mov_b32_e32 v7, v0
	v_mov_b32_e32 v16, v0
	v_mov_b32_e32 v17, v0
	v_mov_b32_e32 v18, v0
	v_mov_b32_e32 v19, v0
	v_mov_b32_e32 v20, v0
	v_mov_b32_e32 v21, v0
	v_mov_b32_e32 v22, v0
	v_mov_b32_e32 v23, v0
	v_mov_b32_e32 v32, v0
	v_mov_b32_e32 v33, v0
	v_mov_b32_e32 v34, v0
	v_mov_b32_e32 v35, v0
	v_mov_b32_e32 v36, v0
	v_mov_b32_e32 v37, v0
	v_mov_b32_e32 v38, v0
	v_mov_b32_e32 v39, v0
	v_mov_b32_e32 v48, v0
	v_mov_b32_e32 v49, v0
	v_mov_b32_e32 v50, v0
	v_mov_b32_e32 v51, v0
	v_mov_b32_e32 v52, v0
	v_mov_b32_e32 v53, v0
	v_mov_b32_e32 v54, v0
	v_mov_b32_e32 v55, v0
	v_mov_b32_e32 v8, v0
	v_mov_b32_e32 v9, v0
	v_mov_b32_e32 v10, v0
	v_mov_b32_e32 v11, v0
	v_mov_b32_e32 v12, v0
	v_mov_b32_e32 v13, v0
	v_mov_b32_e32 v14, v0
	v_mov_b32_e32 v15, v0
	v_mov_b32_e32 v24, v0
	v_mov_b32_e32 v25, v0
	v_mov_b32_e32 v26, v0
	v_mov_b32_e32 v27, v0
	v_mov_b32_e32 v28, v0
	v_mov_b32_e32 v29, v0
	v_mov_b32_e32 v30, v0
	v_mov_b32_e32 v31, v0
	v_mov_b32_e32 v40, v0
	v_mov_b32_e32 v41, v0
	v_mov_b32_e32 v42, v0
	v_mov_b32_e32 v43, v0
	v_mov_b32_e32 v44, v0
	v_mov_b32_e32 v45, v0
	v_mov_b32_e32 v46, v0
	v_mov_b32_e32 v47, v0
	v_mov_b32_e32 v56, v0
	v_mov_b32_e32 v57, v0
	v_mov_b32_e32 v58, v0
	v_mov_b32_e32 v59, v0
	v_mov_b32_e32 v60, v0
	v_mov_b32_e32 v61, v0
	v_mov_b32_e32 v62, v0
	v_mov_b32_e32 v63, v0
	v_mov_b32_e32 v64, v0
	v_mov_b32_e32 v65, v0
	v_mov_b32_e32 v66, v0
	v_mov_b32_e32 v67, v0
	v_mov_b32_e32 v68, v0
	v_mov_b32_e32 v69, v0
	v_mov_b32_e32 v70, v0
	v_mov_b32_e32 v71, v0
	v_mov_b32_e32 v80, v0
	v_mov_b32_e32 v81, v0
	v_mov_b32_e32 v82, v0
	v_mov_b32_e32 v83, v0
	v_mov_b32_e32 v84, v0
	v_mov_b32_e32 v85, v0
	v_mov_b32_e32 v86, v0
	v_mov_b32_e32 v87, v0
	v_mov_b32_e32 v104, v0
	v_mov_b32_e32 v105, v0
	v_mov_b32_e32 v106, v0
	v_mov_b32_e32 v107, v0
	v_mov_b32_e32 v108, v0
	v_mov_b32_e32 v109, v0
	v_mov_b32_e32 v110, v0
	v_mov_b32_e32 v111, v0
	v_mov_b32_e32 v132, v0
	v_mov_b32_e32 v133, v0
	v_mov_b32_e32 v134, v0
	v_mov_b32_e32 v135, v0
	v_mov_b32_e32 v136, v0
	v_mov_b32_e32 v137, v0
	v_mov_b32_e32 v138, v0
	v_mov_b32_e32 v139, v0
	v_mov_b32_e32 v72, v0
	v_mov_b32_e32 v73, v0
	v_mov_b32_e32 v74, v0
	v_mov_b32_e32 v75, v0
	v_mov_b32_e32 v76, v0
	v_mov_b32_e32 v77, v0
	v_mov_b32_e32 v78, v0
	v_mov_b32_e32 v79, v0
	v_mov_b32_e32 v92, v0
	v_mov_b32_e32 v93, v0
	v_mov_b32_e32 v94, v0
	v_mov_b32_e32 v95, v0
	v_mov_b32_e32 v96, v0
	v_mov_b32_e32 v97, v0
	v_mov_b32_e32 v98, v0
	v_mov_b32_e32 v99, v0
	v_mov_b32_e32 v116, v0
	v_mov_b32_e32 v117, v0
	v_mov_b32_e32 v118, v0
	v_mov_b32_e32 v119, v0
	v_mov_b32_e32 v128, v0
	v_mov_b32_e32 v129, v0
	v_mov_b32_e32 v130, v0
	v_mov_b32_e32 v131, v0
	v_mov_b32_e32 v156, v0
	v_mov_b32_e32 v157, v0
	v_mov_b32_e32 v158, v0
	v_mov_b32_e32 v159, v0
	v_mov_b32_e32 v166, v0
	v_mov_b32_e32 v167, v0
	v_mov_b32_e32 v168, v0
	v_mov_b32_e32 v169, v0

.LBB0_855:
	s_ashr_i32 s11, s10, 31
	s_lshl_b64 s[12:13], s[10:11], 20
	s_add_u32 s12, s25, s12
	s_addc_u32 s13, s26, s13
	s_and_b64 s[14:15], s[2:3], exec
	s_cselect_b32 s11, s13, s21
	s_cselect_b32 s53, s12, s20
	s_ashr_i32 s9, s8, 31
	s_lshl_b64 s[14:15], s[8:9], 20
	s_add_u32 s14, s27, s14
	s_addc_u32 s15, s28, s15
	s_and_b64 s[22:23], s[2:3], exec
	s_cselect_b32 s9, s15, s19
	s_cselect_b32 s54, s14, s18
	s_add_u32 s55, s18, 0x100
	s_addc_u32 s56, s19, 0
	s_add_u32 s18, s20, 0x80080
	v_mov_b32_e32 v0, 0
	s_addc_u32 s19, s21, 0
	s_mov_b32 s57, -2
	s_cmp_eq_u32 s52, 1
	s_cbranch_scc1 .Lpeel_zero_P7
	v_add_u32_e32 v154, s30, v139
	v_add_u32_e32 v158, s35, v139
	ds_read_b128 v[142:145], v154
	ds_read_b128 v[146:149], v154 offset:1024
	ds_read_b128 v[150:153], v154 offset:2048
	ds_read_b128 v[154:157], v154 offset:3072
	ds_read_b128 v[166:169], v158
	ds_read_b128 v[170:173], v158 offset:1024
	ds_read_b128 v[174:177], v158 offset:2048
	ds_read_b128 v[178:181], v158 offset:3072
	s_add_u32 s20, s18, 0xfff80080
	s_addc_u32 s21, s19, -1
	s_cmp_eq_u32 s57, 28
	s_cselect_b32 s23, s11, s21
	s_cselect_b32 s22, s53, s20
	s_cselect_b32 s21, s9, s56
	s_cselect_b32 s20, s54, s55
	v_lshl_add_u64 v[158:159], s[18:19], 0, v[136:137]
	s_add_i32 m0, s38, 0xc000
	ds_read_b128 v[182:185], v141
	ds_read_b128 v[186:189], v141 offset:1024
	ds_read_b128 v[190:193], v141 offset:2048
	ds_read_b128 v[194:197], v141 offset:3072
	ds_read_b128 v[198:201], v141 offset:4096
	ds_read_b128 v[202:205], v141 offset:5120
	ds_read_b128 v[206:209], v141 offset:6144
	ds_read_b128 v[210:213], v141 offset:7168
	global_load_lds_dwordx4 v[158:159], off
	v_lshl_add_u64 v[158:159], s[18:19], 0, v[134:135]
	s_add_i32 m0, s38, 0xe000
	s_nop 0
	global_load_lds_dwordx4 v[158:159], off
	s_waitcnt vmcnt(16)
	s_waitcnt lgkmcnt(0)
	s_barrier
	s_setprio 1
	s_waitcnt lgkmcnt(0)
	v_mfma_f32_16x16x32_bf16 v[124:127], v[142:145], v[182:185], 0
	v_mfma_f32_16x16x32_bf16 v[116:119], v[150:153], v[182:185], 0
	v_mfma_f32_16x16x32_bf16 v[108:111], v[142:145], v[190:193], 0
	v_mfma_f32_16x16x32_bf16 v[100:103], v[150:153], v[190:193], 0
	v_mfma_f32_16x16x32_bf16 v[92:95], v[142:145], v[198:201], 0
	v_mfma_f32_16x16x32_bf16 v[84:87], v[150:153], v[198:201], 0
	v_mfma_f32_16x16x32_bf16 v[76:79], v[142:145], v[206:209], 0
	v_mfma_f32_16x16x32_bf16 v[68:71], v[150:153], v[206:209], 0
	v_mfma_f32_16x16x32_bf16 v[124:127], v[146:149], v[186:189], v[124:127]
	v_mfma_f32_16x16x32_bf16 v[116:119], v[154:157], v[186:189], v[116:119]
	v_mfma_f32_16x16x32_bf16 v[108:111], v[146:149], v[194:197], v[108:111]
	v_mfma_f32_16x16x32_bf16 v[100:103], v[154:157], v[194:197], v[100:103]
	v_mfma_f32_16x16x32_bf16 v[92:95], v[146:149], v[202:205], v[92:95]
	v_mfma_f32_16x16x32_bf16 v[84:87], v[154:157], v[202:205], v[84:87]
	v_mfma_f32_16x16x32_bf16 v[76:79], v[146:149], v[210:213], v[76:79]
	v_mfma_f32_16x16x32_bf16 v[68:71], v[154:157], v[210:213], v[68:71]
	s_setprio 0
	s_setprio 1
	v_mfma_f32_16x16x32_bf16 v[120:123], v[166:169], v[182:185], 0
	v_mfma_f32_16x16x32_bf16 v[112:115], v[174:177], v[182:185], 0
	v_mfma_f32_16x16x32_bf16 v[104:107], v[166:169], v[190:193], 0
	v_mfma_f32_16x16x32_bf16 v[96:99], v[174:177], v[190:193], 0
	v_mfma_f32_16x16x32_bf16 v[88:91], v[166:169], v[198:201], 0
	v_mfma_f32_16x16x32_bf16 v[80:83], v[174:177], v[198:201], 0
	v_mfma_f32_16x16x32_bf16 v[72:75], v[166:169], v[206:209], 0
	v_mfma_f32_16x16x32_bf16 v[64:67], v[174:177], v[206:209], 0
	v_mfma_f32_16x16x32_bf16 v[120:123], v[170:173], v[186:189], v[120:123]
	v_mfma_f32_16x16x32_bf16 v[112:115], v[178:181], v[186:189], v[112:115]
	v_mfma_f32_16x16x32_bf16 v[104:107], v[170:173], v[194:197], v[104:107]
	v_mfma_f32_16x16x32_bf16 v[96:99], v[178:181], v[194:197], v[96:99]
	v_mfma_f32_16x16x32_bf16 v[88:91], v[170:173], v[202:205], v[88:91]
	v_mfma_f32_16x16x32_bf16 v[80:83], v[178:181], v[202:205], v[80:83]
	v_mfma_f32_16x16x32_bf16 v[72:75], v[170:173], v[210:213], v[72:75]
	v_mfma_f32_16x16x32_bf16 v[64:67], v[178:181], v[210:213], v[64:67]
	s_setprio 0
	s_barrier
	s_mov_b32 m0, s31
	v_lshl_add_u64 v[158:159], s[20:21], 0, v[160:161]
	s_add_u32 s58, s20, 0x80000
	ds_read_b128 v[182:185], v141 offset:16384
	ds_read_b128 v[186:189], v141 offset:17408
	ds_read_b128 v[190:193], v141 offset:18432
	ds_read_b128 v[194:197], v141 offset:19456
	ds_read_b128 v[198:201], v141 offset:20480
	ds_read_b128 v[202:205], v141 offset:21504
	ds_read_b128 v[206:209], v141 offset:22528
	ds_read_b128 v[210:213], v141 offset:23552
	global_load_lds_dwordx4 v[158:159], off
	v_lshl_add_u64 v[162:163], s[20:21], 0, v[128:129]
	s_mov_b32 m0, s34
	s_addc_u32 s59, s21, 0
	global_load_lds_dwordx4 v[162:163], off
	v_lshl_add_u64 v[214:215], s[58:59], 0, v[160:161]
	s_mov_b32 m0, s36
	v_lshl_add_u64 v[216:217], s[22:23], 0, v[130:131]
	global_load_lds_dwordx4 v[214:215], off
	v_lshl_add_u64 v[214:215], s[58:59], 0, v[128:129]
	s_mov_b32 m0, s37
	s_nop 0
	global_load_lds_dwordx4 v[214:215], off
	v_lshl_add_u64 v[214:215], s[22:23], 0, v[132:133]
	s_mov_b32 m0, s38
	s_nop 0
	global_load_lds_dwordx4 v[214:215], off
	s_mov_b32 m0, s39
	s_nop 0
	global_load_lds_dwordx4 v[216:217], off
	s_waitcnt vmcnt(16)
	s_waitcnt lgkmcnt(0)
	s_barrier
	s_setprio 1
	s_waitcnt lgkmcnt(0)
	v_mfma_f32_16x16x32_bf16 v[60:63], v[142:145], v[182:185], 0
	v_mfma_f32_16x16x32_bf16 v[52:55], v[150:153], v[182:185], 0
	v_mfma_f32_16x16x32_bf16 v[44:47], v[142:145], v[190:193], 0
	v_mfma_f32_16x16x32_bf16 v[36:39], v[150:153], v[190:193], 0
	v_mfma_f32_16x16x32_bf16 v[28:31], v[142:145], v[198:201], 0
	v_mfma_f32_16x16x32_bf16 v[20:23], v[150:153], v[198:201], 0
	v_mfma_f32_16x16x32_bf16 v[12:15], v[142:145], v[206:209], 0
	v_mfma_f32_16x16x32_bf16 v[4:7], v[150:153], v[206:209], 0
	v_mfma_f32_16x16x32_bf16 v[60:63], v[146:149], v[186:189], v[60:63]
	v_mfma_f32_16x16x32_bf16 v[52:55], v[154:157], v[186:189], v[52:55]
	v_mfma_f32_16x16x32_bf16 v[44:47], v[146:149], v[194:197], v[44:47]
	v_mfma_f32_16x16x32_bf16 v[36:39], v[154:157], v[194:197], v[36:39]
	v_mfma_f32_16x16x32_bf16 v[28:31], v[146:149], v[202:205], v[28:31]
	v_mfma_f32_16x16x32_bf16 v[20:23], v[154:157], v[202:205], v[20:23]
	v_mfma_f32_16x16x32_bf16 v[12:15], v[146:149], v[210:213], v[12:15]
	v_mfma_f32_16x16x32_bf16 v[4:7], v[154:157], v[210:213], v[4:7]
	s_setprio 0
	s_setprio 1
	v_mfma_f32_16x16x32_bf16 v[56:59], v[166:169], v[182:185], 0
	v_mfma_f32_16x16x32_bf16 v[48:51], v[174:177], v[182:185], 0
	v_mfma_f32_16x16x32_bf16 v[40:43], v[166:169], v[190:193], 0
	v_mfma_f32_16x16x32_bf16 v[32:35], v[174:177], v[190:193], 0
	v_mfma_f32_16x16x32_bf16 v[24:27], v[166:169], v[198:201], 0
	v_mfma_f32_16x16x32_bf16 v[16:19], v[174:177], v[198:201], 0
	v_mfma_f32_16x16x32_bf16 v[8:11], v[166:169], v[206:209], 0
	v_mfma_f32_16x16x32_bf16 v[0:3], v[174:177], v[206:209], 0
	v_mfma_f32_16x16x32_bf16 v[56:59], v[170:173], v[186:189], v[56:59]
	v_mfma_f32_16x16x32_bf16 v[48:51], v[178:181], v[186:189], v[48:51]
	v_mfma_f32_16x16x32_bf16 v[40:43], v[170:173], v[194:197], v[40:43]
	v_mfma_f32_16x16x32_bf16 v[32:35], v[178:181], v[194:197], v[32:35]
	v_mfma_f32_16x16x32_bf16 v[24:27], v[170:173], v[202:205], v[24:27]
	v_mfma_f32_16x16x32_bf16 v[16:19], v[178:181], v[202:205], v[16:19]
	v_mfma_f32_16x16x32_bf16 v[8:11], v[170:173], v[210:213], v[8:11]
	v_mfma_f32_16x16x32_bf16 v[0:3], v[178:181], v[210:213], v[0:3]
	s_setprio 0
	s_barrier
	v_add_u32_e32 v154, s43, v139
	v_add_u32_e32 v165, s48, v139
	ds_read_b128 v[142:145], v154
	ds_read_b128 v[146:149], v154 offset:1024
	ds_read_b128 v[150:153], v154 offset:2048
	ds_read_b128 v[154:157], v154 offset:3072
	ds_read_b128 v[166:169], v165
	ds_read_b128 v[170:173], v165 offset:1024
	ds_read_b128 v[174:177], v165 offset:2048
	ds_read_b128 v[178:181], v165 offset:3072
	s_add_u32 s22, s22, 0x80000
	s_addc_u32 s23, s23, 0
	s_mov_b32 m0, s40
	v_lshl_add_u64 v[218:219], s[22:23], 0, v[132:133]
	ds_read_b128 v[182:185], v141 offset:32768
	ds_read_b128 v[186:189], v141 offset:33792
	ds_read_b128 v[190:193], v141 offset:34816
	ds_read_b128 v[194:197], v141 offset:35840
	ds_read_b128 v[198:201], v141 offset:36864
	ds_read_b128 v[202:205], v141 offset:37888
	ds_read_b128 v[206:209], v141 offset:38912
	ds_read_b128 v[210:213], v141 offset:39936
	global_load_lds_dwordx4 v[218:219], off
	v_lshl_add_u64 v[218:219], s[22:23], 0, v[130:131]
	s_mov_b32 m0, s41
	s_nop 0
	global_load_lds_dwordx4 v[218:219], off
	s_waitcnt vmcnt(8)
	s_waitcnt lgkmcnt(0)
	s_barrier
	s_setprio 1
	s_waitcnt lgkmcnt(0)
	v_mfma_f32_16x16x32_bf16 v[124:127], v[142:145], v[182:185], v[124:127]
	v_mfma_f32_16x16x32_bf16 v[116:119], v[150:153], v[182:185], v[116:119]
	v_mfma_f32_16x16x32_bf16 v[108:111], v[142:145], v[190:193], v[108:111]
	v_mfma_f32_16x16x32_bf16 v[100:103], v[150:153], v[190:193], v[100:103]
	v_mfma_f32_16x16x32_bf16 v[92:95], v[142:145], v[198:201], v[92:95]
	v_mfma_f32_16x16x32_bf16 v[84:87], v[150:153], v[198:201], v[84:87]
	v_mfma_f32_16x16x32_bf16 v[76:79], v[142:145], v[206:209], v[76:79]
	v_mfma_f32_16x16x32_bf16 v[68:71], v[150:153], v[206:209], v[68:71]
	v_mfma_f32_16x16x32_bf16 v[124:127], v[146:149], v[186:189], v[124:127]
	v_mfma_f32_16x16x32_bf16 v[116:119], v[154:157], v[186:189], v[116:119]
	v_mfma_f32_16x16x32_bf16 v[108:111], v[146:149], v[194:197], v[108:111]
	v_mfma_f32_16x16x32_bf16 v[100:103], v[154:157], v[194:197], v[100:103]
	v_mfma_f32_16x16x32_bf16 v[92:95], v[146:149], v[202:205], v[92:95]
	v_mfma_f32_16x16x32_bf16 v[84:87], v[154:157], v[202:205], v[84:87]
	v_mfma_f32_16x16x32_bf16 v[76:79], v[146:149], v[210:213], v[76:79]
	v_mfma_f32_16x16x32_bf16 v[68:71], v[154:157], v[210:213], v[68:71]
	s_setprio 0
	s_setprio 1
	v_mfma_f32_16x16x32_bf16 v[120:123], v[166:169], v[182:185], v[120:123]
	v_mfma_f32_16x16x32_bf16 v[112:115], v[174:177], v[182:185], v[112:115]
	v_mfma_f32_16x16x32_bf16 v[104:107], v[166:169], v[190:193], v[104:107]
	v_mfma_f32_16x16x32_bf16 v[96:99], v[174:177], v[190:193], v[96:99]
	v_mfma_f32_16x16x32_bf16 v[88:91], v[166:169], v[198:201], v[88:91]
	v_mfma_f32_16x16x32_bf16 v[80:83], v[174:177], v[198:201], v[80:83]
	v_mfma_f32_16x16x32_bf16 v[72:75], v[166:169], v[206:209], v[72:75]
	v_mfma_f32_16x16x32_bf16 v[64:67], v[174:177], v[206:209], v[64:67]
	v_mfma_f32_16x16x32_bf16 v[120:123], v[170:173], v[186:189], v[120:123]
	v_mfma_f32_16x16x32_bf16 v[112:115], v[178:181], v[186:189], v[112:115]
	v_mfma_f32_16x16x32_bf16 v[104:107], v[170:173], v[194:197], v[104:107]
	v_mfma_f32_16x16x32_bf16 v[96:99], v[178:181], v[194:197], v[96:99]
	v_mfma_f32_16x16x32_bf16 v[88:91], v[170:173], v[202:205], v[88:91]
	v_mfma_f32_16x16x32_bf16 v[80:83], v[178:181], v[202:205], v[80:83]
	v_mfma_f32_16x16x32_bf16 v[72:75], v[170:173], v[210:213], v[72:75]
	v_mfma_f32_16x16x32_bf16 v[64:67], v[178:181], v[210:213], v[64:67]
	s_setprio 0
	s_barrier
	s_mov_b32 m0, s44
	v_lshl_add_u64 v[158:159], v[158:159], 0, s[86:87]
	s_add_u32 s20, s20, 0x80080
	ds_read_b128 v[182:185], v141 offset:49152
	ds_read_b128 v[186:189], v141 offset:50176
	ds_read_b128 v[190:193], v141 offset:51200
	ds_read_b128 v[194:197], v141 offset:52224
	ds_read_b128 v[198:201], v141 offset:53248
	ds_read_b128 v[202:205], v141 offset:54272
	ds_read_b128 v[206:209], v141 offset:55296
	ds_read_b128 v[210:213], v141 offset:56320
	global_load_lds_dwordx4 v[158:159], off
	v_lshl_add_u64 v[158:159], v[162:163], 0, s[86:87]
	s_mov_b32 m0, s45
	s_addc_u32 s21, s21, 0
	global_load_lds_dwordx4 v[158:159], off
	v_lshl_add_u64 v[158:159], s[20:21], 0, v[160:161]
	s_mov_b32 m0, s49
	s_nop 0
	global_load_lds_dwordx4 v[158:159], off
	v_lshl_add_u64 v[158:159], s[20:21], 0, v[128:129]
	s_mov_b32 m0, s50
	s_nop 0
	global_load_lds_dwordx4 v[158:159], off
	v_lshl_add_u64 v[158:159], v[214:215], 0, s[86:87]
	s_mov_b32 m0, s46
	s_nop 0
	global_load_lds_dwordx4 v[158:159], off
	v_lshl_add_u64 v[158:159], v[216:217], 0, s[86:87]
	s_mov_b32 m0, s47
	s_nop 0
	global_load_lds_dwordx4 v[158:159], off
	s_waitcnt vmcnt(8)
	s_waitcnt lgkmcnt(0)
	s_barrier
	s_setprio 1
	s_waitcnt lgkmcnt(0)
	v_mfma_f32_16x16x32_bf16 v[60:63], v[142:145], v[182:185], v[60:63]
	v_mfma_f32_16x16x32_bf16 v[52:55], v[150:153], v[182:185], v[52:55]
	v_mfma_f32_16x16x32_bf16 v[44:47], v[142:145], v[190:193], v[44:47]
	v_mfma_f32_16x16x32_bf16 v[36:39], v[150:153], v[190:193], v[36:39]
	v_mfma_f32_16x16x32_bf16 v[28:31], v[142:145], v[198:201], v[28:31]
	v_mfma_f32_16x16x32_bf16 v[20:23], v[150:153], v[198:201], v[20:23]
	v_mfma_f32_16x16x32_bf16 v[12:15], v[142:145], v[206:209], v[12:15]
	v_mfma_f32_16x16x32_bf16 v[4:7], v[150:153], v[206:209], v[4:7]
	v_mfma_f32_16x16x32_bf16 v[60:63], v[146:149], v[186:189], v[60:63]
	v_mfma_f32_16x16x32_bf16 v[52:55], v[154:157], v[186:189], v[52:55]
	v_mfma_f32_16x16x32_bf16 v[44:47], v[146:149], v[194:197], v[44:47]
	v_mfma_f32_16x16x32_bf16 v[36:39], v[154:157], v[194:197], v[36:39]
	v_mfma_f32_16x16x32_bf16 v[28:31], v[146:149], v[202:205], v[28:31]
	v_mfma_f32_16x16x32_bf16 v[20:23], v[154:157], v[202:205], v[20:23]
	v_mfma_f32_16x16x32_bf16 v[12:15], v[146:149], v[210:213], v[12:15]
	v_mfma_f32_16x16x32_bf16 v[4:7], v[154:157], v[210:213], v[4:7]
	s_setprio 0
	s_setprio 1
	v_mfma_f32_16x16x32_bf16 v[56:59], v[166:169], v[182:185], v[56:59]
	v_mfma_f32_16x16x32_bf16 v[48:51], v[174:177], v[182:185], v[48:51]
	v_mfma_f32_16x16x32_bf16 v[40:43], v[166:169], v[190:193], v[40:43]
	v_mfma_f32_16x16x32_bf16 v[32:35], v[174:177], v[190:193], v[32:35]
	v_mfma_f32_16x16x32_bf16 v[24:27], v[166:169], v[198:201], v[24:27]
	v_mfma_f32_16x16x32_bf16 v[16:19], v[174:177], v[198:201], v[16:19]
	v_mfma_f32_16x16x32_bf16 v[8:11], v[166:169], v[206:209], v[8:11]
	v_mfma_f32_16x16x32_bf16 v[0:3], v[174:177], v[206:209], v[0:3]
	v_mfma_f32_16x16x32_bf16 v[56:59], v[170:173], v[186:189], v[56:59]
	v_mfma_f32_16x16x32_bf16 v[48:51], v[178:181], v[186:189], v[48:51]
	v_mfma_f32_16x16x32_bf16 v[40:43], v[170:173], v[194:197], v[40:43]
	v_mfma_f32_16x16x32_bf16 v[32:35], v[178:181], v[194:197], v[32:35]
	v_mfma_f32_16x16x32_bf16 v[24:27], v[170:173], v[202:205], v[24:27]
	v_mfma_f32_16x16x32_bf16 v[16:19], v[178:181], v[202:205], v[16:19]
	v_mfma_f32_16x16x32_bf16 v[8:11], v[170:173], v[210:213], v[8:11]
	v_mfma_f32_16x16x32_bf16 v[0:3], v[178:181], v[210:213], v[0:3]
	s_setprio 0
	s_barrier
	s_add_i32 s57, s57, 2
	s_add_u32 s55, s55, 0x100
	s_addc_u32 s56, s56, 0
	s_add_u32 s18, s18, 0x100
	s_addc_u32 s19, s19, 0
	s_branch .LBB0_856
.Lpeel_zero_P7:
	v_mov_b32_e32 v1, v0
	v_mov_b32_e32 v2, v0
	v_mov_b32_e32 v3, v0
	v_mov_b32_e32 v8, v0
	v_mov_b32_e32 v9, v0
	v_mov_b32_e32 v10, v0
	v_mov_b32_e32 v11, v0
	v_mov_b32_e32 v16, v0
	v_mov_b32_e32 v17, v0
	v_mov_b32_e32 v18, v0
	v_mov_b32_e32 v19, v0
	v_mov_b32_e32 v24, v0
	v_mov_b32_e32 v25, v0
	v_mov_b32_e32 v26, v0
	v_mov_b32_e32 v27, v0
	v_mov_b32_e32 v32, v0
	v_mov_b32_e32 v33, v0
	v_mov_b32_e32 v34, v0
	v_mov_b32_e32 v35, v0
	v_mov_b32_e32 v40, v0
	v_mov_b32_e32 v41, v0
	v_mov_b32_e32 v42, v0
	v_mov_b32_e32 v43, v0
	v_mov_b32_e32 v48, v0
	v_mov_b32_e32 v49, v0
	v_mov_b32_e32 v50, v0
	v_mov_b32_e32 v51, v0
	v_mov_b32_e32 v56, v0
	v_mov_b32_e32 v57, v0
	v_mov_b32_e32 v58, v0
	v_mov_b32_e32 v59, v0
	v_mov_b32_e32 v4, v0
	v_mov_b32_e32 v5, v0
	v_mov_b32_e32 v6, v0
	v_mov_b32_e32 v7, v0
	v_mov_b32_e32 v12, v0
	v_mov_b32_e32 v13, v0
	v_mov_b32_e32 v14, v0
	v_mov_b32_e32 v15, v0
	v_mov_b32_e32 v20, v0
	v_mov_b32_e32 v21, v0
	v_mov_b32_e32 v22, v0
	v_mov_b32_e32 v23, v0
	v_mov_b32_e32 v28, v0
	v_mov_b32_e32 v29, v0
	v_mov_b32_e32 v30, v0
	v_mov_b32_e32 v31, v0
	v_mov_b32_e32 v36, v0
	v_mov_b32_e32 v37, v0
	v_mov_b32_e32 v38, v0
	v_mov_b32_e32 v39, v0
	v_mov_b32_e32 v44, v0
	v_mov_b32_e32 v45, v0
	v_mov_b32_e32 v46, v0
	v_mov_b32_e32 v47, v0
	v_mov_b32_e32 v52, v0
	v_mov_b32_e32 v53, v0
	v_mov_b32_e32 v54, v0
	v_mov_b32_e32 v55, v0
	v_mov_b32_e32 v60, v0
	v_mov_b32_e32 v61, v0
	v_mov_b32_e32 v62, v0
	v_mov_b32_e32 v63, v0
	v_mov_b32_e32 v64, v0
	v_mov_b32_e32 v65, v0
	v_mov_b32_e32 v66, v0
	v_mov_b32_e32 v67, v0
	v_mov_b32_e32 v72, v0
	v_mov_b32_e32 v73, v0
	v_mov_b32_e32 v74, v0
	v_mov_b32_e32 v75, v0
	v_mov_b32_e32 v80, v0
	v_mov_b32_e32 v81, v0
	v_mov_b32_e32 v82, v0
	v_mov_b32_e32 v83, v0
	v_mov_b32_e32 v88, v0
	v_mov_b32_e32 v89, v0
	v_mov_b32_e32 v90, v0
	v_mov_b32_e32 v91, v0
	v_mov_b32_e32 v96, v0
	v_mov_b32_e32 v97, v0
	v_mov_b32_e32 v98, v0
	v_mov_b32_e32 v99, v0
	v_mov_b32_e32 v104, v0
	v_mov_b32_e32 v105, v0
	v_mov_b32_e32 v106, v0
	v_mov_b32_e32 v107, v0
	v_mov_b32_e32 v112, v0
	v_mov_b32_e32 v113, v0
	v_mov_b32_e32 v114, v0
	v_mov_b32_e32 v115, v0
	v_mov_b32_e32 v120, v0
	v_mov_b32_e32 v121, v0
	v_mov_b32_e32 v122, v0
	v_mov_b32_e32 v123, v0
	v_mov_b32_e32 v68, v0
	v_mov_b32_e32 v69, v0
	v_mov_b32_e32 v70, v0
	v_mov_b32_e32 v71, v0
	v_mov_b32_e32 v76, v0
	v_mov_b32_e32 v77, v0
	v_mov_b32_e32 v78, v0
	v_mov_b32_e32 v79, v0
	v_mov_b32_e32 v84, v0
	v_mov_b32_e32 v85, v0
	v_mov_b32_e32 v86, v0
	v_mov_b32_e32 v87, v0
	v_mov_b32_e32 v92, v0
	v_mov_b32_e32 v93, v0
	v_mov_b32_e32 v94, v0
	v_mov_b32_e32 v95, v0
	v_mov_b32_e32 v100, v0
	v_mov_b32_e32 v101, v0
	v_mov_b32_e32 v102, v0
	v_mov_b32_e32 v103, v0
	v_mov_b32_e32 v108, v0
	v_mov_b32_e32 v109, v0
	v_mov_b32_e32 v110, v0
	v_mov_b32_e32 v111, v0
	v_mov_b32_e32 v116, v0
	v_mov_b32_e32 v117, v0
	v_mov_b32_e32 v118, v0
	v_mov_b32_e32 v119, v0
	v_mov_b32_e32 v124, v0
	v_mov_b32_e32 v125, v0
	v_mov_b32_e32 v126, v0
	v_mov_b32_e32 v127, v0

.LBB0_926:
	s_add_u32 s50, s10, 0x100
	v_mov_b32_e32 v0, 0
	s_addc_u32 s51, s11, 0
	s_mov_b32 s52, -2
	s_cmp_eq_u32 s45, 1
	s_cbranch_scc1 .Lpeel_zero_P8
	v_add_u32_e32 v120, s23, v230
	v_add_u32_e32 v148, s26, v230
	ds_read_b128 v[88:91], v120
	ds_read_b128 v[100:103], v120 offset:1024
	ds_read_b128 v[112:115], v120 offset:2048
	ds_read_b128 v[120:123], v120 offset:3072
	ds_read_b128 v[124:127], v148
	ds_read_b128 v[140:143], v148 offset:1024
	ds_read_b128 v[144:147], v148 offset:2048
	ds_read_b128 v[148:151], v148 offset:3072
	s_add_u32 s10, s8, 0x100
	s_addc_u32 s11, s9, 0
	s_cmpk_eq_i32 s52, 0x54
	s_cselect_b32 s15, s5, s11
	s_cselect_b32 s14, s4, s10
	s_cselect_b32 s13, s7, s51
	s_cselect_b32 s12, s6, s50
	v_lshl_add_u64 v[206:207], s[8:9], 0, v[204:205]
	s_add_i32 m0, s29, 0xc000
	ds_read_b128 v[152:155], v232
	ds_read_b128 v[170:173], v232 offset:1024
	ds_read_b128 v[174:177], v232 offset:2048
	ds_read_b128 v[178:181], v232 offset:3072
	ds_read_b128 v[182:185], v232 offset:4096
	ds_read_b128 v[186:189], v232 offset:5120
	ds_read_b128 v[190:193], v232 offset:6144
	ds_read_b128 v[194:197], v232 offset:7168
	global_load_lds_dwordx4 v[206:207], off
	v_lshl_add_u64 v[206:207], s[8:9], 0, v[202:203]
	s_add_i32 m0, s29, 0xe000
	s_nop 0
	global_load_lds_dwordx4 v[206:207], off
	s_waitcnt vmcnt(40)
	s_waitcnt lgkmcnt(0)
	s_barrier
	s_setprio 1
	s_waitcnt lgkmcnt(0)
	v_mfma_f32_16x16x32_bf16 v[166:169], v[88:91], v[152:155], 0
	v_mfma_f32_16x16x32_bf16 v[156:159], v[112:115], v[152:155], 0
	v_mfma_f32_16x16x32_bf16 v[128:131], v[88:91], v[174:177], 0
	v_mfma_f32_16x16x32_bf16 v[116:119], v[112:115], v[174:177], 0
	v_mfma_f32_16x16x32_bf16 v[96:99], v[88:91], v[182:185], 0
	v_mfma_f32_16x16x32_bf16 v[92:95], v[112:115], v[182:185], 0
	v_mfma_f32_16x16x32_bf16 v[76:79], v[88:91], v[190:193], 0
	v_mfma_f32_16x16x32_bf16 v[72:75], v[112:115], v[190:193], 0
	v_mfma_f32_16x16x32_bf16 v[166:169], v[100:103], v[170:173], v[166:169]
	v_mfma_f32_16x16x32_bf16 v[156:159], v[120:123], v[170:173], v[156:159]
	v_mfma_f32_16x16x32_bf16 v[128:131], v[100:103], v[178:181], v[128:131]
	v_mfma_f32_16x16x32_bf16 v[116:119], v[120:123], v[178:181], v[116:119]
	v_mfma_f32_16x16x32_bf16 v[96:99], v[100:103], v[186:189], v[96:99]
	v_mfma_f32_16x16x32_bf16 v[92:95], v[120:123], v[186:189], v[92:95]
	v_mfma_f32_16x16x32_bf16 v[76:79], v[100:103], v[194:197], v[76:79]
	v_mfma_f32_16x16x32_bf16 v[72:75], v[120:123], v[194:197], v[72:75]
	s_setprio 0
	s_setprio 1
	v_mfma_f32_16x16x32_bf16 v[136:139], v[124:127], v[152:155], 0
	v_mfma_f32_16x16x32_bf16 v[132:135], v[144:147], v[152:155], 0
	v_mfma_f32_16x16x32_bf16 v[108:111], v[124:127], v[174:177], 0
	v_mfma_f32_16x16x32_bf16 v[104:107], v[144:147], v[174:177], 0
	v_mfma_f32_16x16x32_bf16 v[84:87], v[124:127], v[182:185], 0
	v_mfma_f32_16x16x32_bf16 v[80:83], v[144:147], v[182:185], 0
	v_mfma_f32_16x16x32_bf16 v[68:71], v[124:127], v[190:193], 0
	v_mfma_f32_16x16x32_bf16 v[64:67], v[144:147], v[190:193], 0
	v_mfma_f32_16x16x32_bf16 v[136:139], v[140:143], v[170:173], v[136:139]
	v_mfma_f32_16x16x32_bf16 v[132:135], v[148:151], v[170:173], v[132:135]
	v_mfma_f32_16x16x32_bf16 v[108:111], v[140:143], v[178:181], v[108:111]
	v_mfma_f32_16x16x32_bf16 v[104:107], v[148:151], v[178:181], v[104:107]
	v_mfma_f32_16x16x32_bf16 v[84:87], v[140:143], v[186:189], v[84:87]
	v_mfma_f32_16x16x32_bf16 v[80:83], v[148:151], v[186:189], v[80:83]
	v_mfma_f32_16x16x32_bf16 v[68:71], v[140:143], v[194:197], v[68:71]
	v_mfma_f32_16x16x32_bf16 v[64:67], v[148:151], v[194:197], v[64:67]
	s_setprio 0
	s_barrier
	s_mov_b32 m0, s24
	v_lshl_add_u64 v[206:207], s[12:13], 0, v[160:161]
	s_add_u32 s8, s12, 0x160000
	ds_read_b128 v[152:155], v232 offset:16384
	ds_read_b128 v[170:173], v232 offset:17408
	ds_read_b128 v[174:177], v232 offset:18432
	ds_read_b128 v[178:181], v232 offset:19456
	ds_read_b128 v[182:185], v232 offset:20480
	ds_read_b128 v[186:189], v232 offset:21504
	ds_read_b128 v[190:193], v232 offset:22528
	ds_read_b128 v[194:197], v232 offset:23552
	global_load_lds_dwordx4 v[206:207], off
	v_lshl_add_u64 v[208:209], s[12:13], 0, v[200:201]
	s_mov_b32 m0, s25
	s_addc_u32 s9, s13, 0
	global_load_lds_dwordx4 v[208:209], off
	v_lshl_add_u64 v[210:211], s[8:9], 0, v[160:161]
	s_mov_b32 m0, s27
	v_lshl_add_u64 v[212:213], s[14:15], 0, v[198:199]
	global_load_lds_dwordx4 v[210:211], off
	v_lshl_add_u64 v[210:211], s[8:9], 0, v[200:201]
	s_mov_b32 m0, s28
	s_nop 0
	global_load_lds_dwordx4 v[210:211], off
	v_lshl_add_u64 v[210:211], s[14:15], 0, v[162:163]
	s_mov_b32 m0, s29
	s_nop 0
	global_load_lds_dwordx4 v[210:211], off
	s_mov_b32 m0, s30
	s_nop 0
	global_load_lds_dwordx4 v[212:213], off
	s_waitcnt vmcnt(40)
	s_waitcnt lgkmcnt(0)
	s_barrier
	s_setprio 1
	s_waitcnt lgkmcnt(0)
	v_mfma_f32_16x16x32_bf16 v[60:63], v[88:91], v[152:155], 0
	v_mfma_f32_16x16x32_bf16 v[56:59], v[112:115], v[152:155], 0
	v_mfma_f32_16x16x32_bf16 v[44:47], v[88:91], v[174:177], 0
	v_mfma_f32_16x16x32_bf16 v[40:43], v[112:115], v[174:177], 0
	v_mfma_f32_16x16x32_bf16 v[28:31], v[88:91], v[182:185], 0
	v_mfma_f32_16x16x32_bf16 v[24:27], v[112:115], v[182:185], 0
	v_mfma_f32_16x16x32_bf16 v[12:15], v[88:91], v[190:193], 0
	v_mfma_f32_16x16x32_bf16 v[8:11], v[112:115], v[190:193], 0
	v_mfma_f32_16x16x32_bf16 v[60:63], v[100:103], v[170:173], v[60:63]
	v_mfma_f32_16x16x32_bf16 v[56:59], v[120:123], v[170:173], v[56:59]
	v_mfma_f32_16x16x32_bf16 v[44:47], v[100:103], v[178:181], v[44:47]
	v_mfma_f32_16x16x32_bf16 v[40:43], v[120:123], v[178:181], v[40:43]
	v_mfma_f32_16x16x32_bf16 v[28:31], v[100:103], v[186:189], v[28:31]
	v_mfma_f32_16x16x32_bf16 v[24:27], v[120:123], v[186:189], v[24:27]
	v_mfma_f32_16x16x32_bf16 v[12:15], v[100:103], v[194:197], v[12:15]
	v_mfma_f32_16x16x32_bf16 v[8:11], v[120:123], v[194:197], v[8:11]
	s_setprio 0
	s_setprio 1
	v_mfma_f32_16x16x32_bf16 v[52:55], v[124:127], v[152:155], 0
	v_mfma_f32_16x16x32_bf16 v[48:51], v[144:147], v[152:155], 0
	v_mfma_f32_16x16x32_bf16 v[36:39], v[124:127], v[174:177], 0
	v_mfma_f32_16x16x32_bf16 v[32:35], v[144:147], v[174:177], 0
	v_mfma_f32_16x16x32_bf16 v[20:23], v[124:127], v[182:185], 0
	v_mfma_f32_16x16x32_bf16 v[16:19], v[144:147], v[182:185], 0
	v_mfma_f32_16x16x32_bf16 v[4:7], v[124:127], v[190:193], 0
	v_mfma_f32_16x16x32_bf16 v[0:3], v[144:147], v[190:193], 0
	v_mfma_f32_16x16x32_bf16 v[52:55], v[140:143], v[170:173], v[52:55]
	v_mfma_f32_16x16x32_bf16 v[48:51], v[148:151], v[170:173], v[48:51]
	v_mfma_f32_16x16x32_bf16 v[36:39], v[140:143], v[178:181], v[36:39]
	v_mfma_f32_16x16x32_bf16 v[32:35], v[148:151], v[178:181], v[32:35]
	v_mfma_f32_16x16x32_bf16 v[20:23], v[140:143], v[186:189], v[20:23]
	v_mfma_f32_16x16x32_bf16 v[16:19], v[148:151], v[186:189], v[16:19]
	v_mfma_f32_16x16x32_bf16 v[4:7], v[140:143], v[194:197], v[4:7]
	v_mfma_f32_16x16x32_bf16 v[0:3], v[148:151], v[194:197], v[0:3]
	s_setprio 0
	s_barrier
	v_add_u32_e32 v120, s36, v230
	v_add_u32_e32 v148, s41, v230
	ds_read_b128 v[88:91], v120
	ds_read_b128 v[100:103], v120 offset:1024
	ds_read_b128 v[112:115], v120 offset:2048
	ds_read_b128 v[120:123], v120 offset:3072
	ds_read_b128 v[124:127], v148
	ds_read_b128 v[140:143], v148 offset:1024
	ds_read_b128 v[144:147], v148 offset:2048
	ds_read_b128 v[148:151], v148 offset:3072
	s_add_u32 s8, s14, 0x160000
	s_addc_u32 s9, s15, 0
	s_mov_b32 m0, s31
	v_lshl_add_u64 v[214:215], s[8:9], 0, v[162:163]
	ds_read_b128 v[152:155], v232 offset:32768
	ds_read_b128 v[170:173], v232 offset:33792
	ds_read_b128 v[174:177], v232 offset:34816
	ds_read_b128 v[178:181], v232 offset:35840
	ds_read_b128 v[182:185], v232 offset:36864
	ds_read_b128 v[186:189], v232 offset:37888
	ds_read_b128 v[190:193], v232 offset:38912
	ds_read_b128 v[194:197], v232 offset:39936
	global_load_lds_dwordx4 v[214:215], off
	v_lshl_add_u64 v[214:215], s[8:9], 0, v[198:199]
	s_mov_b32 m0, s34
	s_nop 0
	global_load_lds_dwordx4 v[214:215], off
	s_waitcnt vmcnt(8)
	s_waitcnt lgkmcnt(0)
	s_barrier
	s_setprio 1
	s_waitcnt lgkmcnt(0)
	v_mfma_f32_16x16x32_bf16 v[166:169], v[88:91], v[152:155], v[166:169]
	v_mfma_f32_16x16x32_bf16 v[156:159], v[112:115], v[152:155], v[156:159]
	v_mfma_f32_16x16x32_bf16 v[128:131], v[88:91], v[174:177], v[128:131]
	v_mfma_f32_16x16x32_bf16 v[116:119], v[112:115], v[174:177], v[116:119]
	v_mfma_f32_16x16x32_bf16 v[96:99], v[88:91], v[182:185], v[96:99]
	v_mfma_f32_16x16x32_bf16 v[92:95], v[112:115], v[182:185], v[92:95]
	v_mfma_f32_16x16x32_bf16 v[76:79], v[88:91], v[190:193], v[76:79]
	v_mfma_f32_16x16x32_bf16 v[72:75], v[112:115], v[190:193], v[72:75]
	v_mfma_f32_16x16x32_bf16 v[166:169], v[100:103], v[170:173], v[166:169]
	v_mfma_f32_16x16x32_bf16 v[156:159], v[120:123], v[170:173], v[156:159]
	v_mfma_f32_16x16x32_bf16 v[128:131], v[100:103], v[178:181], v[128:131]
	v_mfma_f32_16x16x32_bf16 v[116:119], v[120:123], v[178:181], v[116:119]
	v_mfma_f32_16x16x32_bf16 v[96:99], v[100:103], v[186:189], v[96:99]
	v_mfma_f32_16x16x32_bf16 v[92:95], v[120:123], v[186:189], v[92:95]
	v_mfma_f32_16x16x32_bf16 v[76:79], v[100:103], v[194:197], v[76:79]
	v_mfma_f32_16x16x32_bf16 v[72:75], v[120:123], v[194:197], v[72:75]
	s_setprio 0
	s_setprio 1
	v_mfma_f32_16x16x32_bf16 v[136:139], v[124:127], v[152:155], v[136:139]
	v_mfma_f32_16x16x32_bf16 v[132:135], v[144:147], v[152:155], v[132:135]
	v_mfma_f32_16x16x32_bf16 v[108:111], v[124:127], v[174:177], v[108:111]
	v_mfma_f32_16x16x32_bf16 v[104:107], v[144:147], v[174:177], v[104:107]
	v_mfma_f32_16x16x32_bf16 v[84:87], v[124:127], v[182:185], v[84:87]
	v_mfma_f32_16x16x32_bf16 v[80:83], v[144:147], v[182:185], v[80:83]
	v_mfma_f32_16x16x32_bf16 v[68:71], v[124:127], v[190:193], v[68:71]
	v_mfma_f32_16x16x32_bf16 v[64:67], v[144:147], v[190:193], v[64:67]
	v_mfma_f32_16x16x32_bf16 v[136:139], v[140:143], v[170:173], v[136:139]
	v_mfma_f32_16x16x32_bf16 v[132:135], v[148:151], v[170:173], v[132:135]
	v_mfma_f32_16x16x32_bf16 v[108:111], v[140:143], v[178:181], v[108:111]
	v_mfma_f32_16x16x32_bf16 v[104:107], v[148:151], v[178:181], v[104:107]
	v_mfma_f32_16x16x32_bf16 v[84:87], v[140:143], v[186:189], v[84:87]
	v_mfma_f32_16x16x32_bf16 v[80:83], v[148:151], v[186:189], v[80:83]
	v_mfma_f32_16x16x32_bf16 v[68:71], v[140:143], v[194:197], v[68:71]
	v_mfma_f32_16x16x32_bf16 v[64:67], v[148:151], v[194:197], v[64:67]
	s_setprio 0
	s_barrier
	s_mov_b32 m0, s37
	v_lshl_add_u64 v[206:207], v[206:207], 0, s[86:87]
	s_add_u32 s8, s12, 0x160080
	ds_read_b128 v[152:155], v232 offset:49152
	ds_read_b128 v[170:173], v232 offset:50176
	ds_read_b128 v[174:177], v232 offset:51200
	ds_read_b128 v[178:181], v232 offset:52224
	ds_read_b128 v[182:185], v232 offset:53248
	ds_read_b128 v[186:189], v232 offset:54272
	ds_read_b128 v[190:193], v232 offset:55296
	ds_read_b128 v[194:197], v232 offset:56320
	global_load_lds_dwordx4 v[206:207], off
	v_lshl_add_u64 v[206:207], v[208:209], 0, s[86:87]
	s_mov_b32 m0, s38
	s_addc_u32 s9, s13, 0
	global_load_lds_dwordx4 v[206:207], off
	v_lshl_add_u64 v[206:207], s[8:9], 0, v[160:161]
	s_mov_b32 m0, s42
	s_nop 0
	global_load_lds_dwordx4 v[206:207], off
	v_lshl_add_u64 v[206:207], s[8:9], 0, v[200:201]
	s_mov_b32 m0, s43
	s_nop 0
	global_load_lds_dwordx4 v[206:207], off
	v_lshl_add_u64 v[206:207], v[210:211], 0, s[86:87]
	s_mov_b32 m0, s39
	s_nop 0
	global_load_lds_dwordx4 v[206:207], off
	v_lshl_add_u64 v[206:207], v[212:213], 0, s[86:87]
	s_mov_b32 m0, s40
	s_nop 0
	global_load_lds_dwordx4 v[206:207], off
	s_waitcnt vmcnt(8)
	s_waitcnt lgkmcnt(0)
	s_barrier
	s_setprio 1
	s_waitcnt lgkmcnt(0)
	v_mfma_f32_16x16x32_bf16 v[60:63], v[88:91], v[152:155], v[60:63]
	v_mfma_f32_16x16x32_bf16 v[56:59], v[112:115], v[152:155], v[56:59]
	v_mfma_f32_16x16x32_bf16 v[44:47], v[88:91], v[174:177], v[44:47]
	v_mfma_f32_16x16x32_bf16 v[40:43], v[112:115], v[174:177], v[40:43]
	v_mfma_f32_16x16x32_bf16 v[28:31], v[88:91], v[182:185], v[28:31]
	v_mfma_f32_16x16x32_bf16 v[24:27], v[112:115], v[182:185], v[24:27]
	v_mfma_f32_16x16x32_bf16 v[12:15], v[88:91], v[190:193], v[12:15]
	v_mfma_f32_16x16x32_bf16 v[8:11], v[112:115], v[190:193], v[8:11]
	v_mfma_f32_16x16x32_bf16 v[60:63], v[100:103], v[170:173], v[60:63]
	v_mfma_f32_16x16x32_bf16 v[56:59], v[120:123], v[170:173], v[56:59]
	v_mfma_f32_16x16x32_bf16 v[44:47], v[100:103], v[178:181], v[44:47]
	v_mfma_f32_16x16x32_bf16 v[40:43], v[120:123], v[178:181], v[40:43]
	v_mfma_f32_16x16x32_bf16 v[28:31], v[100:103], v[186:189], v[28:31]
	v_mfma_f32_16x16x32_bf16 v[24:27], v[120:123], v[186:189], v[24:27]
	v_mfma_f32_16x16x32_bf16 v[12:15], v[100:103], v[194:197], v[12:15]
	v_mfma_f32_16x16x32_bf16 v[8:11], v[120:123], v[194:197], v[8:11]
	s_setprio 0
	s_setprio 1
	v_mfma_f32_16x16x32_bf16 v[52:55], v[124:127], v[152:155], v[52:55]
	v_mfma_f32_16x16x32_bf16 v[48:51], v[144:147], v[152:155], v[48:51]
	v_mfma_f32_16x16x32_bf16 v[36:39], v[124:127], v[174:177], v[36:39]
	v_mfma_f32_16x16x32_bf16 v[32:35], v[144:147], v[174:177], v[32:35]
	v_mfma_f32_16x16x32_bf16 v[20:23], v[124:127], v[182:185], v[20:23]
	v_mfma_f32_16x16x32_bf16 v[16:19], v[144:147], v[182:185], v[16:19]
	v_mfma_f32_16x16x32_bf16 v[4:7], v[124:127], v[190:193], v[4:7]
	v_mfma_f32_16x16x32_bf16 v[0:3], v[144:147], v[190:193], v[0:3]
	v_mfma_f32_16x16x32_bf16 v[52:55], v[140:143], v[170:173], v[52:55]
	v_mfma_f32_16x16x32_bf16 v[48:51], v[148:151], v[170:173], v[48:51]
	v_mfma_f32_16x16x32_bf16 v[36:39], v[140:143], v[178:181], v[36:39]
	v_mfma_f32_16x16x32_bf16 v[32:35], v[148:151], v[178:181], v[32:35]
	v_mfma_f32_16x16x32_bf16 v[20:23], v[140:143], v[186:189], v[20:23]
	v_mfma_f32_16x16x32_bf16 v[16:19], v[148:151], v[186:189], v[16:19]
	v_mfma_f32_16x16x32_bf16 v[4:7], v[140:143], v[194:197], v[4:7]
	v_mfma_f32_16x16x32_bf16 v[0:3], v[148:151], v[194:197], v[0:3]
	s_setprio 0
	s_barrier
	s_add_i32 s52, s52, 2
	s_add_u32 s50, s50, 0x100
	s_addc_u32 s51, s51, 0
	s_mov_b64 s[8:9], s[10:11]
	s_branch .LBB0_927
